# loop-edge edit: loop-carried SALU and exit test hoisted above the loop-back s_barrier in the 7 dense GEMM K-loops (on top of barrier-wait conversion)
# baseline (speedup 1.0000x reference)
; #define PG8_STAGE(bufoff, gbase, voff) do { _Pragma("unroll") for (int _i = 0; _i < 2; ++_i) \
;         __builtin_amdgcn_global_load_lds((const unsigned*)((const char*)(gbase) + (voff)[_i]), (LAS unsigned*)(lds + (bufoff) + ldsw + _i * 8192), 16, 0, 0); } while (0)
; #define PG8_STAGE_A(bufoff, h, kp, nx) do { if constexpr (GATHER) { const unsigned _p = (nx) ? ng[h] : cg[h]; unsigned _v[2]; _v[0] = (_p & 0xffffu) * lda + CA2[0]; _v[1] = (_p >> 16) * lda + CA2[1]; PG8_STAGE(bufoff, kp, _v); } \
;         else { PG8_STAGE(bufoff, (kp) + (h) * hstepA, voffA); } } while (0)
; #define PG8_LDA(dst, b, h) do { _Pragma("unroll") for (int m = 0; m < 4; ++m) _Pragma("unroll") for (int k = 0; k < 2; ++k) dst[m][k] = *(const LAS bf16x8*)(lds + PG8_SA(b, h) + aoff + m * 2048 + k * 1024); } while (0)
; #define PG8_LDB(dst, b, h) do { _Pragma("unroll") for (int n = 0; n < 2; ++n) _Pragma("unroll") for (int k = 0; k < 2; ++k) dst[n][k] = *(const LAS bf16x8*)(lds + PG8_SB(b, h) + boff + n * 2048 + k * 1024); } while (0)
; #define PG8_MMA(ai, bj, At, Bt) do { __builtin_amdgcn_s_setprio(1); _Pragma("unroll") for (int m = 0; m < 4; ++m) _Pragma("unroll") for (int n = 0; n < 2; ++n) _Pragma("unroll") for (int k = 0; k < 2; ++k) \
;         acc[ai][bj][m][n] = __builtin_amdgcn_mfma_f32_16x16x32_bf16(Bt[n][k], At[m][k], acc[ai][bj][m][n], 0, 0, 0); __builtin_amdgcn_s_setprio(0); } while (0)
; #define PG8_WAIT_V(n) asm volatile("s_waitcnt vmcnt(" #n ")" ::: "memory")
;     ...
;         for (int t = 0; t < nt; t += 2) {
;             const bool last = (t == nt - 2);
;             const char* a1 = cA + (size_t)(t + 1) * kstep;
;             const char* a2 = last ? nA : cA + (size_t)(t + 2) * kstep; const char* b2 = last ? nB : cB + (size_t)(t + 2) * kstep;
;             const char* a3 = a2 + kstep; const char* b3 = b2 + kstep;
;             PG8_LDB(B0, 0, 0); PG8_LDB(B1, 0, 1); PG8_SCHED; PG8_LDA(At, 0, 0); PG8_STAGE_A(PG8_SA(1, 1), 1, a1, false);
;             PG8_WAIT_V(8); PG8_WAIT_L(0); PG8_BAR; if (cur.amask & 1) { PG8_MMA(0, 0, At, B0); PG8_MMA(0, 1, At, B1); } PG8_BAR; PG8_SCHED;
;             PG8_LDA(At, 0, 1); PG8_STAGE(PG8_SB(0, 0), b2, voffB); PG8_STAGE(PG8_SB(0, 1), b2 + hstepB, voffB); PG8_STAGE_A(PG8_SA(0, 0), 0, a2, last);
;             PG8_WAIT_V(8); PG8_WAIT_L(0); PG8_BAR; if (cur.amask & 2) { PG8_MMA(1, 0, At, B0); PG8_MMA(1, 1, At, B1); } PG8_BAR; PG8_SCHED;
.LBB0_544:
	s_add_i32 s34, s31, 2
	s_add_u32 s54, s76, 0xfff80080
	s_addc_u32 s55, s77, -1
	s_add_i32 s82, 0, 0x10000
	s_cmp_eq_u32 s28, s31
	s_cselect_b32 s87, s24, s55
	s_cselect_b32 s86, s25, s54
	v_add_u32_e32 v142, s82, v146
	s_cselect_b32 s81, s26, s30
	s_cselect_b32 s80, s27, s29
	s_add_i32 s31, 0, 0x14000
	ds_read_b128 v[150:153], v142
	ds_read_b128 v[154:157], v142 offset:1024
	ds_read_b128 v[158:161], v142 offset:2048
	ds_read_b128 v[162:165], v142 offset:3072
	v_add_u32_e32 v142, s31, v146
	ds_read_b128 v[166:169], v142
	ds_read_b128 v[170:173], v142 offset:1024
	ds_read_b128 v[174:177], v142 offset:2048
	ds_read_b128 v[178:181], v142 offset:3072
	v_lshl_add_u64 v[142:143], s[76:77], 0, v[138:139]
	s_add_i32 m0, s7, 0xc000
	ds_read_b128 v[182:185], v147
	ds_read_b128 v[186:189], v147 offset:1024
	ds_read_b128 v[190:193], v147 offset:2048
	ds_read_b128 v[194:197], v147 offset:3072
	ds_read_b128 v[198:201], v147 offset:4096
	ds_read_b128 v[202:205], v147 offset:5120
	ds_read_b128 v[206:209], v147 offset:6144
	ds_read_b128 v[210:213], v147 offset:7168
	global_load_lds_dwordx4 v[142:143], off
	v_lshl_add_u64 v[142:143], s[76:77], 0, v[140:141]
	s_add_i32 m0, s7, 0xe000
	s_nop 0
	global_load_lds_dwordx4 v[142:143], off
	s_waitcnt vmcnt(8)
	s_waitcnt lgkmcnt(0)
	s_barrier
	s_setprio 1
	s_waitcnt lgkmcnt(0)
	v_mfma_f32_16x16x32_bf16 v[114:117], v[150:153], v[182:185], v[114:117]
	v_mfma_f32_16x16x32_bf16 v[118:121], v[158:161], v[182:185], v[118:121]
	v_mfma_f32_16x16x32_bf16 v[98:101], v[150:153], v[190:193], v[98:101]
	v_mfma_f32_16x16x32_bf16 v[102:105], v[158:161], v[190:193], v[102:105]
	v_mfma_f32_16x16x32_bf16 v[82:85], v[150:153], v[198:201], v[82:85]
	v_mfma_f32_16x16x32_bf16 v[86:89], v[158:161], v[198:201], v[86:89]
	v_mfma_f32_16x16x32_bf16 v[66:69], v[150:153], v[206:209], v[66:69]
	v_mfma_f32_16x16x32_bf16 v[70:73], v[158:161], v[206:209], v[70:73]
	v_mfma_f32_16x16x32_bf16 v[114:117], v[154:157], v[186:189], v[114:117]
	v_mfma_f32_16x16x32_bf16 v[118:121], v[162:165], v[186:189], v[118:121]
	v_mfma_f32_16x16x32_bf16 v[98:101], v[154:157], v[194:197], v[98:101]
	v_mfma_f32_16x16x32_bf16 v[102:105], v[162:165], v[194:197], v[102:105]
	v_mfma_f32_16x16x32_bf16 v[82:85], v[154:157], v[202:205], v[82:85]
	v_mfma_f32_16x16x32_bf16 v[86:89], v[162:165], v[202:205], v[86:89]
	v_mfma_f32_16x16x32_bf16 v[66:69], v[154:157], v[210:213], v[66:69]
	v_mfma_f32_16x16x32_bf16 v[70:73], v[162:165], v[210:213], v[70:73]
	s_setprio 0
	s_setprio 1
	v_mfma_f32_16x16x32_bf16 v[122:125], v[166:169], v[182:185], v[122:125]
	v_mfma_f32_16x16x32_bf16 v[126:129], v[174:177], v[182:185], v[126:129]
	v_mfma_f32_16x16x32_bf16 v[106:109], v[166:169], v[190:193], v[106:109]
	v_mfma_f32_16x16x32_bf16 v[110:113], v[174:177], v[190:193], v[110:113]
	v_mfma_f32_16x16x32_bf16 v[90:93], v[166:169], v[198:201], v[90:93]
	v_mfma_f32_16x16x32_bf16 v[94:97], v[174:177], v[198:201], v[94:97]
	v_mfma_f32_16x16x32_bf16 v[74:77], v[166:169], v[206:209], v[74:77]
	v_mfma_f32_16x16x32_bf16 v[78:81], v[174:177], v[206:209], v[78:81]
	v_mfma_f32_16x16x32_bf16 v[122:125], v[170:173], v[186:189], v[122:125]
	v_mfma_f32_16x16x32_bf16 v[126:129], v[178:181], v[186:189], v[126:129]
	v_mfma_f32_16x16x32_bf16 v[106:109], v[170:173], v[194:197], v[106:109]
	v_mfma_f32_16x16x32_bf16 v[110:113], v[178:181], v[194:197], v[110:113]
	v_mfma_f32_16x16x32_bf16 v[90:93], v[170:173], v[202:205], v[90:93]
	v_mfma_f32_16x16x32_bf16 v[94:97], v[178:181], v[202:205], v[94:97]
	v_mfma_f32_16x16x32_bf16 v[74:77], v[170:173], v[210:213], v[74:77]
	v_mfma_f32_16x16x32_bf16 v[78:81], v[178:181], v[210:213], v[78:81]
	s_setprio 0
	s_barrier
	s_add_i32 s54, s82, s43
	v_lshl_add_u64 v[142:143], s[80:81], 0, v[0:1]
	s_mov_b32 m0, s54
	ds_read_b128 v[182:185], v147 offset:16384
	ds_read_b128 v[186:189], v147 offset:17408
	ds_read_b128 v[190:193], v147 offset:18432
	ds_read_b128 v[194:197], v147 offset:19456
	ds_read_b128 v[198:201], v147 offset:20480
	ds_read_b128 v[202:205], v147 offset:21504
	ds_read_b128 v[206:209], v147 offset:22528
	ds_read_b128 v[210:213], v147 offset:23552
	global_load_lds_dwordx4 v[142:143], off
	s_add_i32 m0, s54, 0x2000
	s_add_u32 s54, s80, 0x80000
	v_lshl_add_u64 v[214:215], s[80:81], 0, v[134:135]
	s_addc_u32 s55, s81, 0
	s_add_i32 s31, s31, s43
	global_load_lds_dwordx4 v[214:215], off
	v_lshl_add_u64 v[224:225], s[54:55], 0, v[0:1]
	s_mov_b32 m0, s31
	v_lshl_add_u64 v[226:227], s[86:87], 0, v[132:133]
	global_load_lds_dwordx4 v[224:225], off
	v_lshl_add_u64 v[224:225], s[54:55], 0, v[134:135]
	s_add_i32 m0, s31, 0x2000
	s_nop 0
	global_load_lds_dwordx4 v[224:225], off
	v_lshl_add_u64 v[224:225], s[86:87], 0, v[130:131]
	s_mov_b32 m0, s7
	s_nop 0
	global_load_lds_dwordx4 v[224:225], off
	s_mov_b32 m0, s8
	s_nop 0
	global_load_lds_dwordx4 v[226:227], off
	s_waitcnt vmcnt(8)
	s_waitcnt lgkmcnt(0)
	s_barrier
; #define PG8_STAGE(bufoff, gbase, voff) do { _Pragma("unroll") for (int _i = 0; _i < 2; ++_i) \
;         __builtin_amdgcn_global_load_lds((const unsigned*)((const char*)(gbase) + (voff)[_i]), (LAS unsigned*)(lds + (bufoff) + ldsw + _i * 8192), 16, 0, 0); } while (0)
; #define PG8_STAGE_A(bufoff, h, kp, nx) do { if constexpr (GATHER) { const unsigned _p = (nx) ? ng[h] : cg[h]; unsigned _v[2]; _v[0] = (_p & 0xffffu) * lda + CA2[0]; _v[1] = (_p >> 16) * lda + CA2[1]; PG8_STAGE(bufoff, kp, _v); } \
;         else { PG8_STAGE(bufoff, (kp) + (h) * hstepA, voffA); } } while (0)
; #define PG8_LDA(dst, b, h) do { _Pragma("unroll") for (int m = 0; m < 4; ++m) _Pragma("unroll") for (int k = 0; k < 2; ++k) dst[m][k] = *(const LAS bf16x8*)(lds + PG8_SA(b, h) + aoff + m * 2048 + k * 1024); } while (0)
; #define PG8_LDB(dst, b, h) do { _Pragma("unroll") for (int n = 0; n < 2; ++n) _Pragma("unroll") for (int k = 0; k < 2; ++k) dst[n][k] = *(const LAS bf16x8*)(lds + PG8_SB(b, h) + boff + n * 2048 + k * 1024); } while (0)
; #define PG8_MMA(ai, bj, At, Bt) do { __builtin_amdgcn_s_setprio(1); _Pragma("unroll") for (int m = 0; m < 4; ++m) _Pragma("unroll") for (int n = 0; n < 2; ++n) _Pragma("unroll") for (int k = 0; k < 2; ++k) \
;         acc[ai][bj][m][n] = __builtin_amdgcn_mfma_f32_16x16x32_bf16(Bt[n][k], At[m][k], acc[ai][bj][m][n], 0, 0, 0); __builtin_amdgcn_s_setprio(0); } while (0)
; #define PG8_WAIT_V(n) asm volatile("s_waitcnt vmcnt(" #n ")" ::: "memory")
; #define PG8_WAIT_L(n) asm volatile("s_waitcnt lgkmcnt(" #n ")" ::: "memory")
; #define PG8_BAR __builtin_amdgcn_s_barrier()
; #define PG8_SCHED __builtin_amdgcn_sched_barrier(0)
;     ...
;             PG8_WAIT_V(8); PG8_WAIT_L(0); PG8_BAR; if (cur.amask & 2) { PG8_MMA(1, 0, At, B0); PG8_MMA(1, 1, At, B1); } PG8_BAR; PG8_SCHED;
;             PG8_LDB(B0, 1, 0); PG8_LDB(B1, 1, 1); PG8_SCHED; PG8_LDA(At, 1, 0); PG8_STAGE_A(PG8_SA(0, 1), 1, a2, last);
;             PG8_WAIT_V(8); PG8_WAIT_L(0); PG8_BAR; if (cur.amask & 1) { PG8_MMA(0, 0, At, B0); PG8_MMA(0, 1, At, B1); } PG8_BAR; PG8_SCHED;
;             PG8_LDA(At, 1, 1); PG8_STAGE(PG8_SB(1, 0), b3, voffB); PG8_STAGE(PG8_SB(1, 1), b3 + hstepB, voffB); PG8_STAGE_A(PG8_SA(1, 0), 0, a3, last);
	s_setprio 1
	s_waitcnt lgkmcnt(0)
	v_mfma_f32_16x16x32_bf16 v[50:53], v[150:153], v[182:185], v[50:53]
	v_mfma_f32_16x16x32_bf16 v[54:57], v[158:161], v[182:185], v[54:57]
	v_mfma_f32_16x16x32_bf16 v[34:37], v[150:153], v[190:193], v[34:37]
	v_mfma_f32_16x16x32_bf16 v[38:41], v[158:161], v[190:193], v[38:41]
	v_mfma_f32_16x16x32_bf16 v[18:21], v[150:153], v[198:201], v[18:21]
	v_mfma_f32_16x16x32_bf16 v[22:25], v[158:161], v[198:201], v[22:25]
	v_mfma_f32_16x16x32_bf16 v[2:5], v[150:153], v[206:209], v[2:5]
	v_mfma_f32_16x16x32_bf16 v[6:9], v[158:161], v[206:209], v[6:9]
	v_mfma_f32_16x16x32_bf16 v[50:53], v[154:157], v[186:189], v[50:53]
	v_mfma_f32_16x16x32_bf16 v[54:57], v[162:165], v[186:189], v[54:57]
	v_mfma_f32_16x16x32_bf16 v[34:37], v[154:157], v[194:197], v[34:37]
	v_mfma_f32_16x16x32_bf16 v[38:41], v[162:165], v[194:197], v[38:41]
	v_mfma_f32_16x16x32_bf16 v[18:21], v[154:157], v[202:205], v[18:21]
	v_mfma_f32_16x16x32_bf16 v[22:25], v[162:165], v[202:205], v[22:25]
	v_mfma_f32_16x16x32_bf16 v[2:5], v[154:157], v[210:213], v[2:5]
	v_mfma_f32_16x16x32_bf16 v[6:9], v[162:165], v[210:213], v[6:9]
	s_setprio 0
	s_setprio 1
	v_mfma_f32_16x16x32_bf16 v[58:61], v[166:169], v[182:185], v[58:61]
	v_mfma_f32_16x16x32_bf16 v[62:65], v[174:177], v[182:185], v[62:65]
	v_mfma_f32_16x16x32_bf16 v[42:45], v[166:169], v[190:193], v[42:45]
	v_mfma_f32_16x16x32_bf16 v[46:49], v[174:177], v[190:193], v[46:49]
	v_mfma_f32_16x16x32_bf16 v[26:29], v[166:169], v[198:201], v[26:29]
	v_mfma_f32_16x16x32_bf16 v[30:33], v[174:177], v[198:201], v[30:33]
	v_mfma_f32_16x16x32_bf16 v[10:13], v[166:169], v[206:209], v[10:13]
	v_mfma_f32_16x16x32_bf16 v[14:17], v[174:177], v[206:209], v[14:17]
	v_mfma_f32_16x16x32_bf16 v[58:61], v[170:173], v[186:189], v[58:61]
	v_mfma_f32_16x16x32_bf16 v[62:65], v[178:181], v[186:189], v[62:65]
	v_mfma_f32_16x16x32_bf16 v[42:45], v[170:173], v[194:197], v[42:45]
	v_mfma_f32_16x16x32_bf16 v[46:49], v[178:181], v[194:197], v[46:49]
	v_mfma_f32_16x16x32_bf16 v[26:29], v[170:173], v[202:205], v[26:29]
	v_mfma_f32_16x16x32_bf16 v[30:33], v[178:181], v[202:205], v[30:33]
	v_mfma_f32_16x16x32_bf16 v[10:13], v[170:173], v[210:213], v[10:13]
	v_mfma_f32_16x16x32_bf16 v[14:17], v[178:181], v[210:213], v[14:17]
	s_setprio 0
	s_barrier
	s_add_i32 s31, 0, 0x18000
	v_add_u32_e32 v148, s31, v146
	s_add_i32 s82, 0, 0x1c000
	ds_read_b128 v[150:153], v148
	ds_read_b128 v[154:157], v148 offset:1024
	ds_read_b128 v[158:161], v148 offset:2048
	ds_read_b128 v[162:165], v148 offset:3072
	v_add_u32_e32 v148, s82, v146
	ds_read_b128 v[166:169], v148
	ds_read_b128 v[170:173], v148 offset:1024
	ds_read_b128 v[174:177], v148 offset:2048
	ds_read_b128 v[178:181], v148 offset:3072
	s_add_u32 s54, s86, 0x80000
	s_addc_u32 s55, s87, 0
	s_mov_b32 m0, s9
	v_lshl_add_u64 v[228:229], s[54:55], 0, v[130:131]
	ds_read_b128 v[182:185], v147 offset:32768
	ds_read_b128 v[186:189], v147 offset:33792
	ds_read_b128 v[190:193], v147 offset:34816
	ds_read_b128 v[194:197], v147 offset:35840
	ds_read_b128 v[198:201], v147 offset:36864
	ds_read_b128 v[202:205], v147 offset:37888
	ds_read_b128 v[206:209], v147 offset:38912
	ds_read_b128 v[210:213], v147 offset:39936
	global_load_lds_dwordx4 v[228:229], off
	v_lshl_add_u64 v[228:229], s[54:55], 0, v[132:133]
	s_mov_b32 m0, s10
	s_nop 0
	global_load_lds_dwordx4 v[228:229], off
	s_waitcnt vmcnt(8)
	s_waitcnt lgkmcnt(0)
	s_barrier
	s_setprio 1
	s_waitcnt lgkmcnt(0)
	v_mfma_f32_16x16x32_bf16 v[114:117], v[150:153], v[182:185], v[114:117]
	v_mfma_f32_16x16x32_bf16 v[118:121], v[158:161], v[182:185], v[118:121]
	v_mfma_f32_16x16x32_bf16 v[98:101], v[150:153], v[190:193], v[98:101]
	v_mfma_f32_16x16x32_bf16 v[102:105], v[158:161], v[190:193], v[102:105]
	v_mfma_f32_16x16x32_bf16 v[82:85], v[150:153], v[198:201], v[82:85]
	v_mfma_f32_16x16x32_bf16 v[86:89], v[158:161], v[198:201], v[86:89]
	v_mfma_f32_16x16x32_bf16 v[66:69], v[150:153], v[206:209], v[66:69]
	v_mfma_f32_16x16x32_bf16 v[70:73], v[158:161], v[206:209], v[70:73]
	v_mfma_f32_16x16x32_bf16 v[114:117], v[154:157], v[186:189], v[114:117]
	v_mfma_f32_16x16x32_bf16 v[118:121], v[162:165], v[186:189], v[118:121]
	v_mfma_f32_16x16x32_bf16 v[98:101], v[154:157], v[194:197], v[98:101]
	v_mfma_f32_16x16x32_bf16 v[102:105], v[162:165], v[194:197], v[102:105]
	v_mfma_f32_16x16x32_bf16 v[82:85], v[154:157], v[202:205], v[82:85]
	v_mfma_f32_16x16x32_bf16 v[86:89], v[162:165], v[202:205], v[86:89]
	v_mfma_f32_16x16x32_bf16 v[66:69], v[154:157], v[210:213], v[66:69]
	v_mfma_f32_16x16x32_bf16 v[70:73], v[162:165], v[210:213], v[70:73]
	s_setprio 0
	s_setprio 1
	v_mfma_f32_16x16x32_bf16 v[122:125], v[166:169], v[182:185], v[122:125]
	v_mfma_f32_16x16x32_bf16 v[126:129], v[174:177], v[182:185], v[126:129]
	v_mfma_f32_16x16x32_bf16 v[106:109], v[166:169], v[190:193], v[106:109]
	v_mfma_f32_16x16x32_bf16 v[110:113], v[174:177], v[190:193], v[110:113]
	v_mfma_f32_16x16x32_bf16 v[90:93], v[166:169], v[198:201], v[90:93]
	v_mfma_f32_16x16x32_bf16 v[94:97], v[174:177], v[198:201], v[94:97]
	v_mfma_f32_16x16x32_bf16 v[74:77], v[166:169], v[206:209], v[74:77]
	v_mfma_f32_16x16x32_bf16 v[78:81], v[174:177], v[206:209], v[78:81]
	v_mfma_f32_16x16x32_bf16 v[122:125], v[170:173], v[186:189], v[122:125]
	v_mfma_f32_16x16x32_bf16 v[126:129], v[178:181], v[186:189], v[126:129]
	v_mfma_f32_16x16x32_bf16 v[106:109], v[170:173], v[194:197], v[106:109]
	v_mfma_f32_16x16x32_bf16 v[110:113], v[178:181], v[194:197], v[110:113]
	v_mfma_f32_16x16x32_bf16 v[90:93], v[170:173], v[202:205], v[90:93]
	v_mfma_f32_16x16x32_bf16 v[94:97], v[178:181], v[202:205], v[94:97]
	v_mfma_f32_16x16x32_bf16 v[74:77], v[170:173], v[210:213], v[74:77]
	v_mfma_f32_16x16x32_bf16 v[78:81], v[178:181], v[210:213], v[78:81]
	s_setprio 0
	s_barrier
; #define PG8_STAGE(bufoff, gbase, voff) do { _Pragma("unroll") for (int _i = 0; _i < 2; ++_i) \
;         __builtin_amdgcn_global_load_lds((const unsigned*)((const char*)(gbase) + (voff)[_i]), (LAS unsigned*)(lds + (bufoff) + ldsw + _i * 8192), 16, 0, 0); } while (0)
; #define PG8_STAGE_A(bufoff, h, kp, nx) do { if constexpr (GATHER) { const unsigned _p = (nx) ? ng[h] : cg[h]; unsigned _v[2]; _v[0] = (_p & 0xffffu) * lda + CA2[0]; _v[1] = (_p >> 16) * lda + CA2[1]; PG8_STAGE(bufoff, kp, _v); } \
;         else { PG8_STAGE(bufoff, (kp) + (h) * hstepA, voffA); } } while (0)
; #define PG8_LDA(dst, b, h) do { _Pragma("unroll") for (int m = 0; m < 4; ++m) _Pragma("unroll") for (int k = 0; k < 2; ++k) dst[m][k] = *(const LAS bf16x8*)(lds + PG8_SA(b, h) + aoff + m * 2048 + k * 1024); } while (0)
; #define PG8_MMA(ai, bj, At, Bt) do { __builtin_amdgcn_s_setprio(1); _Pragma("unroll") for (int m = 0; m < 4; ++m) _Pragma("unroll") for (int n = 0; n < 2; ++n) _Pragma("unroll") for (int k = 0; k < 2; ++k) \
;         acc[ai][bj][m][n] = __builtin_amdgcn_mfma_f32_16x16x32_bf16(Bt[n][k], At[m][k], acc[ai][bj][m][n], 0, 0, 0); __builtin_amdgcn_s_setprio(0); } while (0)
; #define PG8_WAIT_V(n) asm volatile("s_waitcnt vmcnt(" #n ")" ::: "memory")
; #define PG8_WAIT_L(n) asm volatile("s_waitcnt lgkmcnt(" #n ")" ::: "memory")
; #define PG8_BAR __builtin_amdgcn_s_barrier()
; #define PG8_SCHED __builtin_amdgcn_sched_barrier(0)
;     ...
;             PG8_LDA(At, 1, 1); PG8_STAGE(PG8_SB(1, 0), b3, voffB); PG8_STAGE(PG8_SB(1, 1), b3 + hstepB, voffB); PG8_STAGE_A(PG8_SA(1, 0), 0, a3, last);
;             PG8_WAIT_V(8); PG8_WAIT_L(0); PG8_BAR; if (cur.amask & 2) { PG8_MMA(1, 0, At, B0); PG8_MMA(1, 1, At, B1); } PG8_BAR; PG8_SCHED;
;         }
;         if constexpr (ALIGN_EPI) { if (wr == 0) PG8_BAR; }
	s_add_i32 s31, s31, s43
	v_lshl_add_u64 v[142:143], v[142:143], 0, s[92:93]
	s_mov_b32 m0, s31
	ds_read_b128 v[182:185], v147 offset:49152
	ds_read_b128 v[186:189], v147 offset:50176
	ds_read_b128 v[190:193], v147 offset:51200
	ds_read_b128 v[194:197], v147 offset:52224
	ds_read_b128 v[198:201], v147 offset:53248
	ds_read_b128 v[202:205], v147 offset:54272
	ds_read_b128 v[206:209], v147 offset:55296
	ds_read_b128 v[210:213], v147 offset:56320
	global_load_lds_dwordx4 v[142:143], off
	s_add_i32 m0, s31, 0x2000
	s_add_u32 s54, s80, 0x80080
	v_lshl_add_u64 v[142:143], v[214:215], 0, s[92:93]
	s_addc_u32 s55, s81, 0
	s_add_i32 s31, s82, s43
	global_load_lds_dwordx4 v[142:143], off
	v_lshl_add_u64 v[142:143], s[54:55], 0, v[0:1]
	s_mov_b32 m0, s31
	s_nop 0
	global_load_lds_dwordx4 v[142:143], off
	v_lshl_add_u64 v[142:143], s[54:55], 0, v[134:135]
	s_add_i32 m0, s31, 0x2000
	s_nop 0
	global_load_lds_dwordx4 v[142:143], off
	v_lshl_add_u64 v[142:143], v[224:225], 0, s[92:93]
	s_mov_b32 m0, s16
	s_nop 0
	global_load_lds_dwordx4 v[142:143], off
	v_lshl_add_u64 v[142:143], v[226:227], 0, s[92:93]
	s_mov_b32 m0, s17
	s_nop 0
	global_load_lds_dwordx4 v[142:143], off
	s_waitcnt vmcnt(8)
	s_waitcnt lgkmcnt(0)
	s_barrier
	s_setprio 1
	s_waitcnt lgkmcnt(0)
	v_mfma_f32_16x16x32_bf16 v[50:53], v[150:153], v[182:185], v[50:53]
	v_mfma_f32_16x16x32_bf16 v[54:57], v[158:161], v[182:185], v[54:57]
	v_mfma_f32_16x16x32_bf16 v[34:37], v[150:153], v[190:193], v[34:37]
	v_mfma_f32_16x16x32_bf16 v[38:41], v[158:161], v[190:193], v[38:41]
	v_mfma_f32_16x16x32_bf16 v[18:21], v[150:153], v[198:201], v[18:21]
	v_mfma_f32_16x16x32_bf16 v[22:25], v[158:161], v[198:201], v[22:25]
	v_mfma_f32_16x16x32_bf16 v[2:5], v[150:153], v[206:209], v[2:5]
	v_mfma_f32_16x16x32_bf16 v[6:9], v[158:161], v[206:209], v[6:9]
	v_mfma_f32_16x16x32_bf16 v[50:53], v[154:157], v[186:189], v[50:53]
	v_mfma_f32_16x16x32_bf16 v[54:57], v[162:165], v[186:189], v[54:57]
	v_mfma_f32_16x16x32_bf16 v[34:37], v[154:157], v[194:197], v[34:37]
	v_mfma_f32_16x16x32_bf16 v[38:41], v[162:165], v[194:197], v[38:41]
	v_mfma_f32_16x16x32_bf16 v[18:21], v[154:157], v[202:205], v[18:21]
	v_mfma_f32_16x16x32_bf16 v[22:25], v[162:165], v[202:205], v[22:25]
	v_mfma_f32_16x16x32_bf16 v[2:5], v[154:157], v[210:213], v[2:5]
	v_mfma_f32_16x16x32_bf16 v[6:9], v[162:165], v[210:213], v[6:9]
	s_setprio 0
	s_setprio 1
	v_mfma_f32_16x16x32_bf16 v[58:61], v[166:169], v[182:185], v[58:61]
	v_mfma_f32_16x16x32_bf16 v[62:65], v[174:177], v[182:185], v[62:65]
	v_mfma_f32_16x16x32_bf16 v[42:45], v[166:169], v[190:193], v[42:45]
	v_mfma_f32_16x16x32_bf16 v[46:49], v[174:177], v[190:193], v[46:49]
	v_mfma_f32_16x16x32_bf16 v[26:29], v[166:169], v[198:201], v[26:29]
	v_mfma_f32_16x16x32_bf16 v[30:33], v[174:177], v[198:201], v[30:33]
	v_mfma_f32_16x16x32_bf16 v[10:13], v[166:169], v[206:209], v[10:13]
	v_mfma_f32_16x16x32_bf16 v[14:17], v[174:177], v[206:209], v[14:17]
	v_mfma_f32_16x16x32_bf16 v[58:61], v[170:173], v[186:189], v[58:61]
	v_mfma_f32_16x16x32_bf16 v[62:65], v[178:181], v[186:189], v[62:65]
	v_mfma_f32_16x16x32_bf16 v[42:45], v[170:173], v[194:197], v[42:45]
	v_mfma_f32_16x16x32_bf16 v[46:49], v[178:181], v[194:197], v[46:49]
	v_mfma_f32_16x16x32_bf16 v[26:29], v[170:173], v[202:205], v[26:29]
	v_mfma_f32_16x16x32_bf16 v[30:33], v[178:181], v[202:205], v[30:33]
	v_mfma_f32_16x16x32_bf16 v[10:13], v[170:173], v[210:213], v[10:13]
	v_mfma_f32_16x16x32_bf16 v[14:17], v[178:181], v[210:213], v[14:17]
	s_setprio 0
	s_add_u32 s76, s76, 0x100
	s_addc_u32 s77, s77, 0
	s_add_u32 s29, s29, 0x100
	s_addc_u32 s30, s30, 0
	s_cmp_ge_u32 s34, s22
	s_mov_b32 s31, s34
	s_barrier
	s_cbranch_scc0 .LBB0_544
	v_readlane_b32 s24, v252, 14
	v_readlane_b32 s25, v252, 15
	s_and_b64 vcc, exec, s[24:25]
	s_cbranch_vccz .LBB0_547
	s_barrier

; #define PG8_STAGE(bufoff, gbase, voff) do { _Pragma("unroll") for (int _i = 0; _i < 2; ++_i) \
;         __builtin_amdgcn_global_load_lds((const unsigned*)((const char*)(gbase) + (voff)[_i]), (LAS unsigned*)(lds + (bufoff) + ldsw + _i * 8192), 16, 0, 0); } while (0)
; #define PG8_STAGE_A(bufoff, h, kp, nx) do { if constexpr (GATHER) { const unsigned _p = (nx) ? ng[h] : cg[h]; unsigned _v[2]; _v[0] = (_p & 0xffffu) * lda + CA2[0]; _v[1] = (_p >> 16) * lda + CA2[1]; PG8_STAGE(bufoff, kp, _v); } \
;         else { PG8_STAGE(bufoff, (kp) + (h) * hstepA, voffA); } } while (0)
; #define PG8_LDA(dst, b, h) do { _Pragma("unroll") for (int m = 0; m < 4; ++m) _Pragma("unroll") for (int k = 0; k < 2; ++k) dst[m][k] = *(const LAS bf16x8*)(lds + PG8_SA(b, h) + aoff + m * 2048 + k * 1024); } while (0)
; #define PG8_LDB(dst, b, h) do { _Pragma("unroll") for (int n = 0; n < 2; ++n) _Pragma("unroll") for (int k = 0; k < 2; ++k) dst[n][k] = *(const LAS bf16x8*)(lds + PG8_SB(b, h) + boff + n * 2048 + k * 1024); } while (0)
; #define PG8_MMA(ai, bj, At, Bt) do { __builtin_amdgcn_s_setprio(1); _Pragma("unroll") for (int m = 0; m < 4; ++m) _Pragma("unroll") for (int n = 0; n < 2; ++n) _Pragma("unroll") for (int k = 0; k < 2; ++k) \
;         acc[ai][bj][m][n] = __builtin_amdgcn_mfma_f32_16x16x32_bf16(Bt[n][k], At[m][k], acc[ai][bj][m][n], 0, 0, 0); __builtin_amdgcn_s_setprio(0); } while (0)
; #define PG8_WAIT_V(n) asm volatile("s_waitcnt vmcnt(" #n ")" ::: "memory")
;     ...
;         for (int t = 0; t < nt; t += 2) {
;             const bool last = (t == nt - 2);
;             const char* a1 = cA + (size_t)(t + 1) * kstep;
;             const char* a2 = last ? nA : cA + (size_t)(t + 2) * kstep; const char* b2 = last ? nB : cB + (size_t)(t + 2) * kstep;
;             const char* a3 = a2 + kstep; const char* b3 = b2 + kstep;
;             PG8_LDB(B0, 0, 0); PG8_LDB(B1, 0, 1); PG8_SCHED; PG8_LDA(At, 0, 0); PG8_STAGE_A(PG8_SA(1, 1), 1, a1, false);
;             PG8_WAIT_V(8); PG8_WAIT_L(0); PG8_BAR; if (cur.amask & 1) { PG8_MMA(0, 0, At, B0); PG8_MMA(0, 1, At, B1); } PG8_BAR; PG8_SCHED;
;             PG8_LDA(At, 0, 1); PG8_STAGE(PG8_SB(0, 0), b2, voffB); PG8_STAGE(PG8_SB(0, 1), b2 + hstepB, voffB); PG8_STAGE_A(PG8_SA(0, 0), 0, a2, last);
;             PG8_WAIT_V(8); PG8_WAIT_L(0); PG8_BAR; if (cur.amask & 2) { PG8_MMA(1, 0, At, B0); PG8_MMA(1, 1, At, B1); } PG8_BAR; PG8_SCHED;
.LBB0_1085:
	s_add_u32 s16, s48, 0xfff80080
	s_addc_u32 s17, s49, -1
	s_add_i32 s18, 0, 0x10000
	s_cmp_eq_u32 s15, 28
	s_cselect_b32 s53, s39, s17
	s_cselect_b32 s52, s38, s16
	v_add_u32_e32 v148, s18, v151
	s_cselect_b32 s51, s41, s14
	s_cselect_b32 s50, s40, s13
	s_add_i32 s19, 0, 0x14000
	ds_read_b128 v[144:147], v148
	ds_read_b128 v[154:157], v148 offset:1024
	ds_read_b128 v[158:161], v148 offset:2048
	ds_read_b128 v[162:165], v148 offset:3072
	v_add_u32_e32 v148, s19, v151
	ds_read_b128 v[166:169], v148
	ds_read_b128 v[170:173], v148 offset:1024
	ds_read_b128 v[174:177], v148 offset:2048
	ds_read_b128 v[178:181], v148 offset:3072
	v_lshl_add_u64 v[148:149], s[48:49], 0, v[140:141]
	s_add_i32 m0, s6, 0xc000
	ds_read_b128 v[182:185], v152
	ds_read_b128 v[186:189], v152 offset:1024
	ds_read_b128 v[190:193], v152 offset:2048
	ds_read_b128 v[194:197], v152 offset:3072
	ds_read_b128 v[198:201], v152 offset:4096
	ds_read_b128 v[202:205], v152 offset:5120
	ds_read_b128 v[206:209], v152 offset:6144
	ds_read_b128 v[210:213], v152 offset:7168
	global_load_lds_dwordx4 v[148:149], off
	v_lshl_add_u64 v[148:149], s[48:49], 0, v[142:143]
	s_add_i32 m0, s6, 0xe000
	s_nop 0
	global_load_lds_dwordx4 v[148:149], off
	s_waitcnt vmcnt(8)
	s_waitcnt lgkmcnt(0)
	s_barrier
	s_setprio 1
	s_waitcnt lgkmcnt(0)
	v_mfma_f32_16x16x32_bf16 v[126:129], v[144:147], v[182:185], v[126:129]
	v_mfma_f32_16x16x32_bf16 v[122:125], v[158:161], v[182:185], v[122:125]
	v_mfma_f32_16x16x32_bf16 v[110:113], v[144:147], v[190:193], v[110:113]
	v_mfma_f32_16x16x32_bf16 v[106:109], v[158:161], v[190:193], v[106:109]
	v_mfma_f32_16x16x32_bf16 v[94:97], v[144:147], v[198:201], v[94:97]
	v_mfma_f32_16x16x32_bf16 v[90:93], v[158:161], v[198:201], v[90:93]
	v_mfma_f32_16x16x32_bf16 v[78:81], v[144:147], v[206:209], v[78:81]
	v_mfma_f32_16x16x32_bf16 v[74:77], v[158:161], v[206:209], v[74:77]
	v_mfma_f32_16x16x32_bf16 v[126:129], v[154:157], v[186:189], v[126:129]
	v_mfma_f32_16x16x32_bf16 v[122:125], v[162:165], v[186:189], v[122:125]
	v_mfma_f32_16x16x32_bf16 v[110:113], v[154:157], v[194:197], v[110:113]
	v_mfma_f32_16x16x32_bf16 v[106:109], v[162:165], v[194:197], v[106:109]
	v_mfma_f32_16x16x32_bf16 v[94:97], v[154:157], v[202:205], v[94:97]
	v_mfma_f32_16x16x32_bf16 v[90:93], v[162:165], v[202:205], v[90:93]
	v_mfma_f32_16x16x32_bf16 v[78:81], v[154:157], v[210:213], v[78:81]
	v_mfma_f32_16x16x32_bf16 v[74:77], v[162:165], v[210:213], v[74:77]
	s_setprio 0
	s_setprio 1
	v_mfma_f32_16x16x32_bf16 v[118:121], v[166:169], v[182:185], v[118:121]
	v_mfma_f32_16x16x32_bf16 v[114:117], v[174:177], v[182:185], v[114:117]
	v_mfma_f32_16x16x32_bf16 v[102:105], v[166:169], v[190:193], v[102:105]
	v_mfma_f32_16x16x32_bf16 v[98:101], v[174:177], v[190:193], v[98:101]
	v_mfma_f32_16x16x32_bf16 v[86:89], v[166:169], v[198:201], v[86:89]
	v_mfma_f32_16x16x32_bf16 v[82:85], v[174:177], v[198:201], v[82:85]
	v_mfma_f32_16x16x32_bf16 v[70:73], v[166:169], v[206:209], v[70:73]
	v_mfma_f32_16x16x32_bf16 v[66:69], v[174:177], v[206:209], v[66:69]
	v_mfma_f32_16x16x32_bf16 v[118:121], v[170:173], v[186:189], v[118:121]
	v_mfma_f32_16x16x32_bf16 v[114:117], v[178:181], v[186:189], v[114:117]
	v_mfma_f32_16x16x32_bf16 v[102:105], v[170:173], v[194:197], v[102:105]
	v_mfma_f32_16x16x32_bf16 v[98:101], v[178:181], v[194:197], v[98:101]
	v_mfma_f32_16x16x32_bf16 v[86:89], v[170:173], v[202:205], v[86:89]
	v_mfma_f32_16x16x32_bf16 v[82:85], v[178:181], v[202:205], v[82:85]
	v_mfma_f32_16x16x32_bf16 v[70:73], v[170:173], v[210:213], v[70:73]
	v_mfma_f32_16x16x32_bf16 v[66:69], v[178:181], v[210:213], v[66:69]
	s_setprio 0
	s_barrier
	s_add_i32 s16, s18, s43
	v_lshl_add_u64 v[148:149], s[50:51], 0, v[0:1]
	s_mov_b32 m0, s16
	ds_read_b128 v[182:185], v152 offset:16384
	ds_read_b128 v[186:189], v152 offset:17408
	ds_read_b128 v[190:193], v152 offset:18432
	ds_read_b128 v[194:197], v152 offset:19456
	ds_read_b128 v[198:201], v152 offset:20480
	ds_read_b128 v[202:205], v152 offset:21504
	ds_read_b128 v[206:209], v152 offset:22528
	ds_read_b128 v[210:213], v152 offset:23552
	global_load_lds_dwordx4 v[148:149], off
	s_add_i32 m0, s16, 0x2000
	s_add_u32 s16, s50, 0x80000
	v_lshl_add_u64 v[214:215], s[50:51], 0, v[134:135]
	s_addc_u32 s17, s51, 0
	s_add_i32 s18, s19, s43
	global_load_lds_dwordx4 v[214:215], off
	v_lshl_add_u64 v[224:225], s[16:17], 0, v[0:1]
	s_mov_b32 m0, s18
	v_lshl_add_u64 v[226:227], s[52:53], 0, v[132:133]
	global_load_lds_dwordx4 v[224:225], off
	v_lshl_add_u64 v[224:225], s[16:17], 0, v[134:135]
	s_add_i32 m0, s18, 0x2000
	s_nop 0
	global_load_lds_dwordx4 v[224:225], off
	v_lshl_add_u64 v[224:225], s[52:53], 0, v[130:131]
	s_mov_b32 m0, s6
	s_nop 0
	global_load_lds_dwordx4 v[224:225], off
	s_mov_b32 m0, s7
	s_nop 0
	global_load_lds_dwordx4 v[226:227], off
	s_waitcnt vmcnt(8)
	s_waitcnt lgkmcnt(0)
	s_barrier
; #define PG8_STAGE(bufoff, gbase, voff) do { _Pragma("unroll") for (int _i = 0; _i < 2; ++_i) \
;         __builtin_amdgcn_global_load_lds((const unsigned*)((const char*)(gbase) + (voff)[_i]), (LAS unsigned*)(lds + (bufoff) + ldsw + _i * 8192), 16, 0, 0); } while (0)
; #define PG8_STAGE_A(bufoff, h, kp, nx) do { if constexpr (GATHER) { const unsigned _p = (nx) ? ng[h] : cg[h]; unsigned _v[2]; _v[0] = (_p & 0xffffu) * lda + CA2[0]; _v[1] = (_p >> 16) * lda + CA2[1]; PG8_STAGE(bufoff, kp, _v); } \
;         else { PG8_STAGE(bufoff, (kp) + (h) * hstepA, voffA); } } while (0)
; #define PG8_LDA(dst, b, h) do { _Pragma("unroll") for (int m = 0; m < 4; ++m) _Pragma("unroll") for (int k = 0; k < 2; ++k) dst[m][k] = *(const LAS bf16x8*)(lds + PG8_SA(b, h) + aoff + m * 2048 + k * 1024); } while (0)
; #define PG8_LDB(dst, b, h) do { _Pragma("unroll") for (int n = 0; n < 2; ++n) _Pragma("unroll") for (int k = 0; k < 2; ++k) dst[n][k] = *(const LAS bf16x8*)(lds + PG8_SB(b, h) + boff + n * 2048 + k * 1024); } while (0)
; #define PG8_MMA(ai, bj, At, Bt) do { __builtin_amdgcn_s_setprio(1); _Pragma("unroll") for (int m = 0; m < 4; ++m) _Pragma("unroll") for (int n = 0; n < 2; ++n) _Pragma("unroll") for (int k = 0; k < 2; ++k) \
;         acc[ai][bj][m][n] = __builtin_amdgcn_mfma_f32_16x16x32_bf16(Bt[n][k], At[m][k], acc[ai][bj][m][n], 0, 0, 0); __builtin_amdgcn_s_setprio(0); } while (0)
; #define PG8_WAIT_V(n) asm volatile("s_waitcnt vmcnt(" #n ")" ::: "memory")
; #define PG8_WAIT_L(n) asm volatile("s_waitcnt lgkmcnt(" #n ")" ::: "memory")
; #define PG8_BAR __builtin_amdgcn_s_barrier()
; #define PG8_SCHED __builtin_amdgcn_sched_barrier(0)
;     ...
;             PG8_WAIT_V(8); PG8_WAIT_L(0); PG8_BAR; if (cur.amask & 2) { PG8_MMA(1, 0, At, B0); PG8_MMA(1, 1, At, B1); } PG8_BAR; PG8_SCHED;
;             PG8_LDB(B0, 1, 0); PG8_LDB(B1, 1, 1); PG8_SCHED; PG8_LDA(At, 1, 0); PG8_STAGE_A(PG8_SA(0, 1), 1, a2, last);
;             PG8_WAIT_V(8); PG8_WAIT_L(0); PG8_BAR; if (cur.amask & 1) { PG8_MMA(0, 0, At, B0); PG8_MMA(0, 1, At, B1); } PG8_BAR; PG8_SCHED;
;             PG8_LDA(At, 1, 1); PG8_STAGE(PG8_SB(1, 0), b3, voffB); PG8_STAGE(PG8_SB(1, 1), b3 + hstepB, voffB); PG8_STAGE_A(PG8_SA(1, 0), 0, a3, last);
	s_setprio 1
	s_waitcnt lgkmcnt(0)
	v_mfma_f32_16x16x32_bf16 v[62:65], v[144:147], v[182:185], v[62:65]
	v_mfma_f32_16x16x32_bf16 v[58:61], v[158:161], v[182:185], v[58:61]
	v_mfma_f32_16x16x32_bf16 v[46:49], v[144:147], v[190:193], v[46:49]
	v_mfma_f32_16x16x32_bf16 v[42:45], v[158:161], v[190:193], v[42:45]
	v_mfma_f32_16x16x32_bf16 v[30:33], v[144:147], v[198:201], v[30:33]
	v_mfma_f32_16x16x32_bf16 v[26:29], v[158:161], v[198:201], v[26:29]
	v_mfma_f32_16x16x32_bf16 v[14:17], v[144:147], v[206:209], v[14:17]
	v_mfma_f32_16x16x32_bf16 v[10:13], v[158:161], v[206:209], v[10:13]
	v_mfma_f32_16x16x32_bf16 v[62:65], v[154:157], v[186:189], v[62:65]
	v_mfma_f32_16x16x32_bf16 v[58:61], v[162:165], v[186:189], v[58:61]
	v_mfma_f32_16x16x32_bf16 v[46:49], v[154:157], v[194:197], v[46:49]
	v_mfma_f32_16x16x32_bf16 v[42:45], v[162:165], v[194:197], v[42:45]
	v_mfma_f32_16x16x32_bf16 v[30:33], v[154:157], v[202:205], v[30:33]
	v_mfma_f32_16x16x32_bf16 v[26:29], v[162:165], v[202:205], v[26:29]
	v_mfma_f32_16x16x32_bf16 v[14:17], v[154:157], v[210:213], v[14:17]
	v_mfma_f32_16x16x32_bf16 v[10:13], v[162:165], v[210:213], v[10:13]
	s_setprio 0
	s_setprio 1
	v_mfma_f32_16x16x32_bf16 v[54:57], v[166:169], v[182:185], v[54:57]
	v_mfma_f32_16x16x32_bf16 v[50:53], v[174:177], v[182:185], v[50:53]
	v_mfma_f32_16x16x32_bf16 v[38:41], v[166:169], v[190:193], v[38:41]
	v_mfma_f32_16x16x32_bf16 v[34:37], v[174:177], v[190:193], v[34:37]
	v_mfma_f32_16x16x32_bf16 v[22:25], v[166:169], v[198:201], v[22:25]
	v_mfma_f32_16x16x32_bf16 v[18:21], v[174:177], v[198:201], v[18:21]
	v_mfma_f32_16x16x32_bf16 v[6:9], v[166:169], v[206:209], v[6:9]
	v_mfma_f32_16x16x32_bf16 v[2:5], v[174:177], v[206:209], v[2:5]
	v_mfma_f32_16x16x32_bf16 v[54:57], v[170:173], v[186:189], v[54:57]
	v_mfma_f32_16x16x32_bf16 v[50:53], v[178:181], v[186:189], v[50:53]
	v_mfma_f32_16x16x32_bf16 v[38:41], v[170:173], v[194:197], v[38:41]
	v_mfma_f32_16x16x32_bf16 v[34:37], v[178:181], v[194:197], v[34:37]
	v_mfma_f32_16x16x32_bf16 v[22:25], v[170:173], v[202:205], v[22:25]
	v_mfma_f32_16x16x32_bf16 v[18:21], v[178:181], v[202:205], v[18:21]
	v_mfma_f32_16x16x32_bf16 v[6:9], v[170:173], v[210:213], v[6:9]
	v_mfma_f32_16x16x32_bf16 v[2:5], v[178:181], v[210:213], v[2:5]
	s_setprio 0
	s_barrier
	s_add_i32 s18, 0, 0x18000
	v_add_u32_e32 v153, s18, v151
	s_add_i32 s19, 0, 0x1c000
	ds_read_b128 v[144:147], v153
	ds_read_b128 v[154:157], v153 offset:1024
	ds_read_b128 v[158:161], v153 offset:2048
	ds_read_b128 v[162:165], v153 offset:3072
	v_add_u32_e32 v153, s19, v151
	ds_read_b128 v[166:169], v153
	ds_read_b128 v[170:173], v153 offset:1024
	ds_read_b128 v[174:177], v153 offset:2048
	ds_read_b128 v[178:181], v153 offset:3072
	s_add_u32 s16, s52, 0x80000
	s_addc_u32 s17, s53, 0
	s_mov_b32 m0, s8
	v_lshl_add_u64 v[228:229], s[16:17], 0, v[130:131]
	ds_read_b128 v[182:185], v152 offset:32768
	ds_read_b128 v[186:189], v152 offset:33792
	ds_read_b128 v[190:193], v152 offset:34816
	ds_read_b128 v[194:197], v152 offset:35840
	ds_read_b128 v[198:201], v152 offset:36864
	ds_read_b128 v[202:205], v152 offset:37888
	ds_read_b128 v[206:209], v152 offset:38912
	ds_read_b128 v[210:213], v152 offset:39936
	global_load_lds_dwordx4 v[228:229], off
	v_lshl_add_u64 v[228:229], s[16:17], 0, v[132:133]
	s_mov_b32 m0, s9
	s_nop 0
	global_load_lds_dwordx4 v[228:229], off
	s_waitcnt vmcnt(8)
	s_waitcnt lgkmcnt(0)
	s_barrier
	s_setprio 1
	s_waitcnt lgkmcnt(0)
	v_mfma_f32_16x16x32_bf16 v[126:129], v[144:147], v[182:185], v[126:129]
	v_mfma_f32_16x16x32_bf16 v[122:125], v[158:161], v[182:185], v[122:125]
	v_mfma_f32_16x16x32_bf16 v[110:113], v[144:147], v[190:193], v[110:113]
	v_mfma_f32_16x16x32_bf16 v[106:109], v[158:161], v[190:193], v[106:109]
	v_mfma_f32_16x16x32_bf16 v[94:97], v[144:147], v[198:201], v[94:97]
	v_mfma_f32_16x16x32_bf16 v[90:93], v[158:161], v[198:201], v[90:93]
	v_mfma_f32_16x16x32_bf16 v[78:81], v[144:147], v[206:209], v[78:81]
	v_mfma_f32_16x16x32_bf16 v[74:77], v[158:161], v[206:209], v[74:77]
	v_mfma_f32_16x16x32_bf16 v[126:129], v[154:157], v[186:189], v[126:129]
	v_mfma_f32_16x16x32_bf16 v[122:125], v[162:165], v[186:189], v[122:125]
	v_mfma_f32_16x16x32_bf16 v[110:113], v[154:157], v[194:197], v[110:113]
	v_mfma_f32_16x16x32_bf16 v[106:109], v[162:165], v[194:197], v[106:109]
	v_mfma_f32_16x16x32_bf16 v[94:97], v[154:157], v[202:205], v[94:97]
	v_mfma_f32_16x16x32_bf16 v[90:93], v[162:165], v[202:205], v[90:93]
	v_mfma_f32_16x16x32_bf16 v[78:81], v[154:157], v[210:213], v[78:81]
	v_mfma_f32_16x16x32_bf16 v[74:77], v[162:165], v[210:213], v[74:77]
	s_setprio 0
	s_setprio 1
	v_mfma_f32_16x16x32_bf16 v[118:121], v[166:169], v[182:185], v[118:121]
	v_mfma_f32_16x16x32_bf16 v[114:117], v[174:177], v[182:185], v[114:117]
	v_mfma_f32_16x16x32_bf16 v[102:105], v[166:169], v[190:193], v[102:105]
	v_mfma_f32_16x16x32_bf16 v[98:101], v[174:177], v[190:193], v[98:101]
	v_mfma_f32_16x16x32_bf16 v[86:89], v[166:169], v[198:201], v[86:89]
	v_mfma_f32_16x16x32_bf16 v[82:85], v[174:177], v[198:201], v[82:85]
	v_mfma_f32_16x16x32_bf16 v[70:73], v[166:169], v[206:209], v[70:73]
	v_mfma_f32_16x16x32_bf16 v[66:69], v[174:177], v[206:209], v[66:69]
	v_mfma_f32_16x16x32_bf16 v[118:121], v[170:173], v[186:189], v[118:121]
	v_mfma_f32_16x16x32_bf16 v[114:117], v[178:181], v[186:189], v[114:117]
	v_mfma_f32_16x16x32_bf16 v[102:105], v[170:173], v[194:197], v[102:105]
	v_mfma_f32_16x16x32_bf16 v[98:101], v[178:181], v[194:197], v[98:101]
	v_mfma_f32_16x16x32_bf16 v[86:89], v[170:173], v[202:205], v[86:89]
	v_mfma_f32_16x16x32_bf16 v[82:85], v[178:181], v[202:205], v[82:85]
	v_mfma_f32_16x16x32_bf16 v[70:73], v[170:173], v[210:213], v[70:73]
	v_mfma_f32_16x16x32_bf16 v[66:69], v[178:181], v[210:213], v[66:69]
	s_setprio 0
	s_barrier
; #define PG8_STAGE(bufoff, gbase, voff) do { _Pragma("unroll") for (int _i = 0; _i < 2; ++_i) \
;         __builtin_amdgcn_global_load_lds((const unsigned*)((const char*)(gbase) + (voff)[_i]), (LAS unsigned*)(lds + (bufoff) + ldsw + _i * 8192), 16, 0, 0); } while (0)
; #define PG8_STAGE_A(bufoff, h, kp, nx) do { if constexpr (GATHER) { const unsigned _p = (nx) ? ng[h] : cg[h]; unsigned _v[2]; _v[0] = (_p & 0xffffu) * lda + CA2[0]; _v[1] = (_p >> 16) * lda + CA2[1]; PG8_STAGE(bufoff, kp, _v); } \
;         else { PG8_STAGE(bufoff, (kp) + (h) * hstepA, voffA); } } while (0)
; #define PG8_LDA(dst, b, h) do { _Pragma("unroll") for (int m = 0; m < 4; ++m) _Pragma("unroll") for (int k = 0; k < 2; ++k) dst[m][k] = *(const LAS bf16x8*)(lds + PG8_SA(b, h) + aoff + m * 2048 + k * 1024); } while (0)
; #define PG8_MMA(ai, bj, At, Bt) do { __builtin_amdgcn_s_setprio(1); _Pragma("unroll") for (int m = 0; m < 4; ++m) _Pragma("unroll") for (int n = 0; n < 2; ++n) _Pragma("unroll") for (int k = 0; k < 2; ++k) \
;         acc[ai][bj][m][n] = __builtin_amdgcn_mfma_f32_16x16x32_bf16(Bt[n][k], At[m][k], acc[ai][bj][m][n], 0, 0, 0); __builtin_amdgcn_s_setprio(0); } while (0)
; #define PG8_WAIT_V(n) asm volatile("s_waitcnt vmcnt(" #n ")" ::: "memory")
; #define PG8_WAIT_L(n) asm volatile("s_waitcnt lgkmcnt(" #n ")" ::: "memory")
; #define PG8_BAR __builtin_amdgcn_s_barrier()
; #define PG8_SCHED __builtin_amdgcn_sched_barrier(0)
;     ...
;             PG8_LDA(At, 1, 1); PG8_STAGE(PG8_SB(1, 0), b3, voffB); PG8_STAGE(PG8_SB(1, 1), b3 + hstepB, voffB); PG8_STAGE_A(PG8_SA(1, 0), 0, a3, last);
;             PG8_WAIT_V(8); PG8_WAIT_L(0); PG8_BAR; if (cur.amask & 2) { PG8_MMA(1, 0, At, B0); PG8_MMA(1, 1, At, B1); } PG8_BAR; PG8_SCHED;
;         }
;         if constexpr (ALIGN_EPI) { if (wr == 0) PG8_BAR; }
	s_add_i32 s16, s18, s43
	v_lshl_add_u64 v[148:149], v[148:149], 0, s[92:93]
	s_mov_b32 m0, s16
	ds_read_b128 v[182:185], v152 offset:49152
	ds_read_b128 v[186:189], v152 offset:50176
	ds_read_b128 v[190:193], v152 offset:51200
	ds_read_b128 v[194:197], v152 offset:52224
	ds_read_b128 v[198:201], v152 offset:53248
	ds_read_b128 v[202:205], v152 offset:54272
	ds_read_b128 v[206:209], v152 offset:55296
	ds_read_b128 v[210:213], v152 offset:56320
	global_load_lds_dwordx4 v[148:149], off
	s_add_i32 m0, s16, 0x2000
	s_add_u32 s16, s50, 0x80080
	v_lshl_add_u64 v[148:149], v[214:215], 0, s[92:93]
	s_addc_u32 s17, s51, 0
	s_add_i32 s18, s19, s43
	global_load_lds_dwordx4 v[148:149], off
	v_lshl_add_u64 v[148:149], s[16:17], 0, v[0:1]
	s_mov_b32 m0, s18
	s_nop 0
	global_load_lds_dwordx4 v[148:149], off
	v_lshl_add_u64 v[148:149], s[16:17], 0, v[134:135]
	s_add_i32 m0, s18, 0x2000
	s_nop 0
	global_load_lds_dwordx4 v[148:149], off
	v_lshl_add_u64 v[148:149], v[224:225], 0, s[92:93]
	s_mov_b32 m0, s10
	s_nop 0
	global_load_lds_dwordx4 v[148:149], off
	v_lshl_add_u64 v[148:149], v[226:227], 0, s[92:93]
	s_mov_b32 m0, s11
	s_nop 0
	global_load_lds_dwordx4 v[148:149], off
	s_waitcnt vmcnt(8)
	s_waitcnt lgkmcnt(0)
	s_barrier
	s_setprio 1
	s_waitcnt lgkmcnt(0)
	v_mfma_f32_16x16x32_bf16 v[62:65], v[144:147], v[182:185], v[62:65]
	v_mfma_f32_16x16x32_bf16 v[58:61], v[158:161], v[182:185], v[58:61]
	v_mfma_f32_16x16x32_bf16 v[46:49], v[144:147], v[190:193], v[46:49]
	v_mfma_f32_16x16x32_bf16 v[42:45], v[158:161], v[190:193], v[42:45]
	v_mfma_f32_16x16x32_bf16 v[30:33], v[144:147], v[198:201], v[30:33]
	v_mfma_f32_16x16x32_bf16 v[26:29], v[158:161], v[198:201], v[26:29]
	v_mfma_f32_16x16x32_bf16 v[14:17], v[144:147], v[206:209], v[14:17]
	v_mfma_f32_16x16x32_bf16 v[10:13], v[158:161], v[206:209], v[10:13]
	v_mfma_f32_16x16x32_bf16 v[62:65], v[154:157], v[186:189], v[62:65]
	v_mfma_f32_16x16x32_bf16 v[58:61], v[162:165], v[186:189], v[58:61]
	v_mfma_f32_16x16x32_bf16 v[46:49], v[154:157], v[194:197], v[46:49]
	v_mfma_f32_16x16x32_bf16 v[42:45], v[162:165], v[194:197], v[42:45]
	v_mfma_f32_16x16x32_bf16 v[30:33], v[154:157], v[202:205], v[30:33]
	v_mfma_f32_16x16x32_bf16 v[26:29], v[162:165], v[202:205], v[26:29]
	v_mfma_f32_16x16x32_bf16 v[14:17], v[154:157], v[210:213], v[14:17]
	v_mfma_f32_16x16x32_bf16 v[10:13], v[162:165], v[210:213], v[10:13]
	s_setprio 0
	s_setprio 1
	v_mfma_f32_16x16x32_bf16 v[54:57], v[166:169], v[182:185], v[54:57]
	v_mfma_f32_16x16x32_bf16 v[50:53], v[174:177], v[182:185], v[50:53]
	v_mfma_f32_16x16x32_bf16 v[38:41], v[166:169], v[190:193], v[38:41]
	v_mfma_f32_16x16x32_bf16 v[34:37], v[174:177], v[190:193], v[34:37]
	v_mfma_f32_16x16x32_bf16 v[22:25], v[166:169], v[198:201], v[22:25]
	v_mfma_f32_16x16x32_bf16 v[18:21], v[174:177], v[198:201], v[18:21]
	v_mfma_f32_16x16x32_bf16 v[6:9], v[166:169], v[206:209], v[6:9]
	v_mfma_f32_16x16x32_bf16 v[2:5], v[174:177], v[206:209], v[2:5]
	v_mfma_f32_16x16x32_bf16 v[54:57], v[170:173], v[186:189], v[54:57]
	v_mfma_f32_16x16x32_bf16 v[50:53], v[178:181], v[186:189], v[50:53]
	v_mfma_f32_16x16x32_bf16 v[38:41], v[170:173], v[194:197], v[38:41]
	v_mfma_f32_16x16x32_bf16 v[34:37], v[178:181], v[194:197], v[34:37]
	v_mfma_f32_16x16x32_bf16 v[22:25], v[170:173], v[202:205], v[22:25]
	v_mfma_f32_16x16x32_bf16 v[18:21], v[178:181], v[202:205], v[18:21]
	v_mfma_f32_16x16x32_bf16 v[6:9], v[170:173], v[210:213], v[6:9]
	v_mfma_f32_16x16x32_bf16 v[2:5], v[178:181], v[210:213], v[2:5]
	s_setprio 0
	s_add_i32 s15, s15, 2
	s_add_u32 s48, s48, 0x100
	s_addc_u32 s49, s49, 0
	s_add_u32 s13, s13, 0x100
	s_addc_u32 s14, s14, 0
	s_cmp_gt_u32 s15, 29
	s_barrier
	s_cbranch_scc0 .LBB0_1085
	v_readlane_b32 s14, v252, 14
	v_readlane_b32 s15, v252, 15
	s_and_b64 vcc, exec, s[14:15]
	s_cbranch_vccz .LBB0_1088
	s_barrier

; #define PG8_STAGE(bufoff, gbase, voff) do { _Pragma("unroll") for (int _i = 0; _i < 2; ++_i) \
;         __builtin_amdgcn_global_load_lds((const unsigned*)((const char*)(gbase) + (voff)[_i]), (LAS unsigned*)(lds + (bufoff) + ldsw + _i * 8192), 16, 0, 0); } while (0)
; #define PG8_STAGE_A(bufoff, h, kp, nx) do { if constexpr (GATHER) { const unsigned _p = (nx) ? ng[h] : cg[h]; unsigned _v[2]; _v[0] = (_p & 0xffffu) * lda + CA2[0]; _v[1] = (_p >> 16) * lda + CA2[1]; PG8_STAGE(bufoff, kp, _v); } \
;         else { PG8_STAGE(bufoff, (kp) + (h) * hstepA, voffA); } } while (0)
; #define PG8_LDA(dst, b, h) do { _Pragma("unroll") for (int m = 0; m < 4; ++m) _Pragma("unroll") for (int k = 0; k < 2; ++k) dst[m][k] = *(const LAS bf16x8*)(lds + PG8_SA(b, h) + aoff + m * 2048 + k * 1024); } while (0)
; #define PG8_LDB(dst, b, h) do { _Pragma("unroll") for (int n = 0; n < 2; ++n) _Pragma("unroll") for (int k = 0; k < 2; ++k) dst[n][k] = *(const LAS bf16x8*)(lds + PG8_SB(b, h) + boff + n * 2048 + k * 1024); } while (0)
; #define PG8_MMA(ai, bj, At, Bt) do { __builtin_amdgcn_s_setprio(1); _Pragma("unroll") for (int m = 0; m < 4; ++m) _Pragma("unroll") for (int n = 0; n < 2; ++n) _Pragma("unroll") for (int k = 0; k < 2; ++k) \
;         acc[ai][bj][m][n] = __builtin_amdgcn_mfma_f32_16x16x32_bf16(Bt[n][k], At[m][k], acc[ai][bj][m][n], 0, 0, 0); __builtin_amdgcn_s_setprio(0); } while (0)
; #define PG8_WAIT_V(n) asm volatile("s_waitcnt vmcnt(" #n ")" ::: "memory")
;     ...
;         for (int t = 0; t < nt; t += 2) {
;             const bool last = (t == nt - 2);
;             const char* a1 = cA + (size_t)(t + 1) * kstep;
;             const char* a2 = last ? nA : cA + (size_t)(t + 2) * kstep; const char* b2 = last ? nB : cB + (size_t)(t + 2) * kstep;
;             const char* a3 = a2 + kstep; const char* b3 = b2 + kstep;
;             PG8_LDB(B0, 0, 0); PG8_LDB(B1, 0, 1); PG8_SCHED; PG8_LDA(At, 0, 0); PG8_STAGE_A(PG8_SA(1, 1), 1, a1, false);
;             PG8_WAIT_V(8); PG8_WAIT_L(0); PG8_BAR; if (cur.amask & 1) { PG8_MMA(0, 0, At, B0); PG8_MMA(0, 1, At, B1); } PG8_BAR; PG8_SCHED;
;             PG8_LDA(At, 0, 1); PG8_STAGE(PG8_SB(0, 0), b2, voffB); PG8_STAGE(PG8_SB(0, 1), b2 + hstepB, voffB); PG8_STAGE_A(PG8_SA(0, 0), 0, a2, last);
;             PG8_WAIT_V(8); PG8_WAIT_L(0); PG8_BAR; if (cur.amask & 2) { PG8_MMA(1, 0, At, B0); PG8_MMA(1, 1, At, B1); } PG8_BAR; PG8_SCHED;
.LBB0_1117:
	s_add_u32 s16, s48, 0xfff80080
	s_addc_u32 s17, s49, -1
	s_add_i32 s18, 0, 0x10000
	s_cmp_eq_u32 s15, 28
	s_cselect_b32 s53, s39, s17
	s_cselect_b32 s52, s38, s16
	v_add_u32_e32 v148, s18, v151
	s_cselect_b32 s51, s41, s14
	s_cselect_b32 s50, s40, s13
	s_add_i32 s19, 0, 0x14000
	ds_read_b128 v[144:147], v148
	ds_read_b128 v[154:157], v148 offset:1024
	ds_read_b128 v[158:161], v148 offset:2048
	ds_read_b128 v[162:165], v148 offset:3072
	v_add_u32_e32 v148, s19, v151
	ds_read_b128 v[166:169], v148
	ds_read_b128 v[170:173], v148 offset:1024
	ds_read_b128 v[174:177], v148 offset:2048
	ds_read_b128 v[178:181], v148 offset:3072
	v_lshl_add_u64 v[148:149], s[48:49], 0, v[140:141]
	s_add_i32 m0, s6, 0xc000
	ds_read_b128 v[182:185], v152
	ds_read_b128 v[186:189], v152 offset:1024
	ds_read_b128 v[190:193], v152 offset:2048
	ds_read_b128 v[194:197], v152 offset:3072
	ds_read_b128 v[198:201], v152 offset:4096
	ds_read_b128 v[202:205], v152 offset:5120
	ds_read_b128 v[206:209], v152 offset:6144
	ds_read_b128 v[210:213], v152 offset:7168
	global_load_lds_dwordx4 v[148:149], off
	v_lshl_add_u64 v[148:149], s[48:49], 0, v[142:143]
	s_add_i32 m0, s6, 0xe000
	s_nop 0
	global_load_lds_dwordx4 v[148:149], off
	s_waitcnt vmcnt(8)
	s_waitcnt lgkmcnt(0)
	s_barrier
	s_setprio 1
	s_waitcnt lgkmcnt(0)
	v_mfma_f32_16x16x32_bf16 v[126:129], v[144:147], v[182:185], v[126:129]
	v_mfma_f32_16x16x32_bf16 v[122:125], v[158:161], v[182:185], v[122:125]
	v_mfma_f32_16x16x32_bf16 v[114:117], v[144:147], v[190:193], v[114:117]
	v_mfma_f32_16x16x32_bf16 v[106:109], v[158:161], v[190:193], v[106:109]
	v_mfma_f32_16x16x32_bf16 v[94:97], v[144:147], v[198:201], v[94:97]
	v_mfma_f32_16x16x32_bf16 v[90:93], v[158:161], v[198:201], v[90:93]
	v_mfma_f32_16x16x32_bf16 v[82:85], v[144:147], v[206:209], v[82:85]
	v_mfma_f32_16x16x32_bf16 v[74:77], v[158:161], v[206:209], v[74:77]
	v_mfma_f32_16x16x32_bf16 v[126:129], v[154:157], v[186:189], v[126:129]
	v_mfma_f32_16x16x32_bf16 v[122:125], v[162:165], v[186:189], v[122:125]
	v_mfma_f32_16x16x32_bf16 v[114:117], v[154:157], v[194:197], v[114:117]
	v_mfma_f32_16x16x32_bf16 v[106:109], v[162:165], v[194:197], v[106:109]
	v_mfma_f32_16x16x32_bf16 v[94:97], v[154:157], v[202:205], v[94:97]
	v_mfma_f32_16x16x32_bf16 v[90:93], v[162:165], v[202:205], v[90:93]
	v_mfma_f32_16x16x32_bf16 v[82:85], v[154:157], v[210:213], v[82:85]
	v_mfma_f32_16x16x32_bf16 v[74:77], v[162:165], v[210:213], v[74:77]
	s_setprio 0
	s_setprio 1
	v_mfma_f32_16x16x32_bf16 v[118:121], v[166:169], v[182:185], v[118:121]
	v_mfma_f32_16x16x32_bf16 v[110:113], v[174:177], v[182:185], v[110:113]
	v_mfma_f32_16x16x32_bf16 v[102:105], v[166:169], v[190:193], v[102:105]
	v_mfma_f32_16x16x32_bf16 v[98:101], v[174:177], v[190:193], v[98:101]
	v_mfma_f32_16x16x32_bf16 v[86:89], v[166:169], v[198:201], v[86:89]
	v_mfma_f32_16x16x32_bf16 v[78:81], v[174:177], v[198:201], v[78:81]
	v_mfma_f32_16x16x32_bf16 v[70:73], v[166:169], v[206:209], v[70:73]
	v_mfma_f32_16x16x32_bf16 v[66:69], v[174:177], v[206:209], v[66:69]
	v_mfma_f32_16x16x32_bf16 v[118:121], v[170:173], v[186:189], v[118:121]
	v_mfma_f32_16x16x32_bf16 v[110:113], v[178:181], v[186:189], v[110:113]
	v_mfma_f32_16x16x32_bf16 v[102:105], v[170:173], v[194:197], v[102:105]
	v_mfma_f32_16x16x32_bf16 v[98:101], v[178:181], v[194:197], v[98:101]
	v_mfma_f32_16x16x32_bf16 v[86:89], v[170:173], v[202:205], v[86:89]
	v_mfma_f32_16x16x32_bf16 v[78:81], v[178:181], v[202:205], v[78:81]
	v_mfma_f32_16x16x32_bf16 v[70:73], v[170:173], v[210:213], v[70:73]
	v_mfma_f32_16x16x32_bf16 v[66:69], v[178:181], v[210:213], v[66:69]
	s_setprio 0
	s_barrier
	s_add_i32 s16, s18, s43
	v_lshl_add_u64 v[148:149], s[50:51], 0, v[0:1]
	s_mov_b32 m0, s16
	ds_read_b128 v[182:185], v152 offset:16384
	ds_read_b128 v[186:189], v152 offset:17408
	ds_read_b128 v[190:193], v152 offset:18432
	ds_read_b128 v[194:197], v152 offset:19456
	ds_read_b128 v[198:201], v152 offset:20480
	ds_read_b128 v[202:205], v152 offset:21504
	ds_read_b128 v[206:209], v152 offset:22528
	ds_read_b128 v[210:213], v152 offset:23552
	global_load_lds_dwordx4 v[148:149], off
	s_add_i32 m0, s16, 0x2000
	s_add_u32 s16, s50, 0x80000
	v_lshl_add_u64 v[214:215], s[50:51], 0, v[134:135]
	s_addc_u32 s17, s51, 0
	s_add_i32 s18, s19, s43
	global_load_lds_dwordx4 v[214:215], off
	v_lshl_add_u64 v[224:225], s[16:17], 0, v[0:1]
	s_mov_b32 m0, s18
	v_lshl_add_u64 v[226:227], s[52:53], 0, v[132:133]
	global_load_lds_dwordx4 v[224:225], off
	v_lshl_add_u64 v[224:225], s[16:17], 0, v[134:135]
	s_add_i32 m0, s18, 0x2000
	s_nop 0
	global_load_lds_dwordx4 v[224:225], off
	v_lshl_add_u64 v[224:225], s[52:53], 0, v[130:131]
	s_mov_b32 m0, s6
	s_nop 0
	global_load_lds_dwordx4 v[224:225], off
	s_mov_b32 m0, s7
	s_nop 0
	global_load_lds_dwordx4 v[226:227], off
	s_waitcnt vmcnt(8)
	s_waitcnt lgkmcnt(0)
	s_barrier
; #define PG8_STAGE(bufoff, gbase, voff) do { _Pragma("unroll") for (int _i = 0; _i < 2; ++_i) \
;         __builtin_amdgcn_global_load_lds((const unsigned*)((const char*)(gbase) + (voff)[_i]), (LAS unsigned*)(lds + (bufoff) + ldsw + _i * 8192), 16, 0, 0); } while (0)
; #define PG8_STAGE_A(bufoff, h, kp, nx) do { if constexpr (GATHER) { const unsigned _p = (nx) ? ng[h] : cg[h]; unsigned _v[2]; _v[0] = (_p & 0xffffu) * lda + CA2[0]; _v[1] = (_p >> 16) * lda + CA2[1]; PG8_STAGE(bufoff, kp, _v); } \
;         else { PG8_STAGE(bufoff, (kp) + (h) * hstepA, voffA); } } while (0)
; #define PG8_LDA(dst, b, h) do { _Pragma("unroll") for (int m = 0; m < 4; ++m) _Pragma("unroll") for (int k = 0; k < 2; ++k) dst[m][k] = *(const LAS bf16x8*)(lds + PG8_SA(b, h) + aoff + m * 2048 + k * 1024); } while (0)
; #define PG8_LDB(dst, b, h) do { _Pragma("unroll") for (int n = 0; n < 2; ++n) _Pragma("unroll") for (int k = 0; k < 2; ++k) dst[n][k] = *(const LAS bf16x8*)(lds + PG8_SB(b, h) + boff + n * 2048 + k * 1024); } while (0)
; #define PG8_MMA(ai, bj, At, Bt) do { __builtin_amdgcn_s_setprio(1); _Pragma("unroll") for (int m = 0; m < 4; ++m) _Pragma("unroll") for (int n = 0; n < 2; ++n) _Pragma("unroll") for (int k = 0; k < 2; ++k) \
;         acc[ai][bj][m][n] = __builtin_amdgcn_mfma_f32_16x16x32_bf16(Bt[n][k], At[m][k], acc[ai][bj][m][n], 0, 0, 0); __builtin_amdgcn_s_setprio(0); } while (0)
; #define PG8_WAIT_V(n) asm volatile("s_waitcnt vmcnt(" #n ")" ::: "memory")
; #define PG8_WAIT_L(n) asm volatile("s_waitcnt lgkmcnt(" #n ")" ::: "memory")
; #define PG8_BAR __builtin_amdgcn_s_barrier()
; #define PG8_SCHED __builtin_amdgcn_sched_barrier(0)
;     ...
;             PG8_WAIT_V(8); PG8_WAIT_L(0); PG8_BAR; if (cur.amask & 2) { PG8_MMA(1, 0, At, B0); PG8_MMA(1, 1, At, B1); } PG8_BAR; PG8_SCHED;
;             PG8_LDB(B0, 1, 0); PG8_LDB(B1, 1, 1); PG8_SCHED; PG8_LDA(At, 1, 0); PG8_STAGE_A(PG8_SA(0, 1), 1, a2, last);
;             PG8_WAIT_V(8); PG8_WAIT_L(0); PG8_BAR; if (cur.amask & 1) { PG8_MMA(0, 0, At, B0); PG8_MMA(0, 1, At, B1); } PG8_BAR; PG8_SCHED;
;             PG8_LDA(At, 1, 1); PG8_STAGE(PG8_SB(1, 0), b3, voffB); PG8_STAGE(PG8_SB(1, 1), b3 + hstepB, voffB); PG8_STAGE_A(PG8_SA(1, 0), 0, a3, last);
	s_setprio 1
	s_waitcnt lgkmcnt(0)
	v_mfma_f32_16x16x32_bf16 v[62:65], v[144:147], v[182:185], v[62:65]
	v_mfma_f32_16x16x32_bf16 v[58:61], v[158:161], v[182:185], v[58:61]
	v_mfma_f32_16x16x32_bf16 v[50:53], v[144:147], v[190:193], v[50:53]
	v_mfma_f32_16x16x32_bf16 v[42:45], v[158:161], v[190:193], v[42:45]
	v_mfma_f32_16x16x32_bf16 v[30:33], v[144:147], v[198:201], v[30:33]
	v_mfma_f32_16x16x32_bf16 v[26:29], v[158:161], v[198:201], v[26:29]
	v_mfma_f32_16x16x32_bf16 v[18:21], v[144:147], v[206:209], v[18:21]
	v_mfma_f32_16x16x32_bf16 v[10:13], v[158:161], v[206:209], v[10:13]
	v_mfma_f32_16x16x32_bf16 v[62:65], v[154:157], v[186:189], v[62:65]
	v_mfma_f32_16x16x32_bf16 v[58:61], v[162:165], v[186:189], v[58:61]
	v_mfma_f32_16x16x32_bf16 v[50:53], v[154:157], v[194:197], v[50:53]
	v_mfma_f32_16x16x32_bf16 v[42:45], v[162:165], v[194:197], v[42:45]
	v_mfma_f32_16x16x32_bf16 v[30:33], v[154:157], v[202:205], v[30:33]
	v_mfma_f32_16x16x32_bf16 v[26:29], v[162:165], v[202:205], v[26:29]
	v_mfma_f32_16x16x32_bf16 v[18:21], v[154:157], v[210:213], v[18:21]
	v_mfma_f32_16x16x32_bf16 v[10:13], v[162:165], v[210:213], v[10:13]
	s_setprio 0
	s_setprio 1
	v_mfma_f32_16x16x32_bf16 v[54:57], v[166:169], v[182:185], v[54:57]
	v_mfma_f32_16x16x32_bf16 v[46:49], v[174:177], v[182:185], v[46:49]
	v_mfma_f32_16x16x32_bf16 v[38:41], v[166:169], v[190:193], v[38:41]
	v_mfma_f32_16x16x32_bf16 v[34:37], v[174:177], v[190:193], v[34:37]
	v_mfma_f32_16x16x32_bf16 v[22:25], v[166:169], v[198:201], v[22:25]
	v_mfma_f32_16x16x32_bf16 v[14:17], v[174:177], v[198:201], v[14:17]
	v_mfma_f32_16x16x32_bf16 v[6:9], v[166:169], v[206:209], v[6:9]
	v_mfma_f32_16x16x32_bf16 v[2:5], v[174:177], v[206:209], v[2:5]
	v_mfma_f32_16x16x32_bf16 v[54:57], v[170:173], v[186:189], v[54:57]
	v_mfma_f32_16x16x32_bf16 v[46:49], v[178:181], v[186:189], v[46:49]
	v_mfma_f32_16x16x32_bf16 v[38:41], v[170:173], v[194:197], v[38:41]
	v_mfma_f32_16x16x32_bf16 v[34:37], v[178:181], v[194:197], v[34:37]
	v_mfma_f32_16x16x32_bf16 v[22:25], v[170:173], v[202:205], v[22:25]
	v_mfma_f32_16x16x32_bf16 v[14:17], v[178:181], v[202:205], v[14:17]
	v_mfma_f32_16x16x32_bf16 v[6:9], v[170:173], v[210:213], v[6:9]
	v_mfma_f32_16x16x32_bf16 v[2:5], v[178:181], v[210:213], v[2:5]
	s_setprio 0
	s_barrier
	s_add_i32 s18, 0, 0x18000
	v_add_u32_e32 v153, s18, v151
	s_add_i32 s19, 0, 0x1c000
	ds_read_b128 v[144:147], v153
	ds_read_b128 v[154:157], v153 offset:1024
	ds_read_b128 v[158:161], v153 offset:2048
	ds_read_b128 v[162:165], v153 offset:3072
	v_add_u32_e32 v153, s19, v151
	ds_read_b128 v[166:169], v153
	ds_read_b128 v[170:173], v153 offset:1024
	ds_read_b128 v[174:177], v153 offset:2048
	ds_read_b128 v[178:181], v153 offset:3072
	s_add_u32 s16, s52, 0x80000
	s_addc_u32 s17, s53, 0
	s_mov_b32 m0, s8
	v_lshl_add_u64 v[228:229], s[16:17], 0, v[130:131]
	ds_read_b128 v[182:185], v152 offset:32768
	ds_read_b128 v[186:189], v152 offset:33792
	ds_read_b128 v[190:193], v152 offset:34816
	ds_read_b128 v[194:197], v152 offset:35840
	ds_read_b128 v[198:201], v152 offset:36864
	ds_read_b128 v[202:205], v152 offset:37888
	ds_read_b128 v[206:209], v152 offset:38912
	ds_read_b128 v[210:213], v152 offset:39936
	global_load_lds_dwordx4 v[228:229], off
	v_lshl_add_u64 v[228:229], s[16:17], 0, v[132:133]
	s_mov_b32 m0, s9
	s_nop 0
	global_load_lds_dwordx4 v[228:229], off
	s_waitcnt vmcnt(8)
	s_waitcnt lgkmcnt(0)
	s_barrier
	s_setprio 1
	s_waitcnt lgkmcnt(0)
	v_mfma_f32_16x16x32_bf16 v[126:129], v[144:147], v[182:185], v[126:129]
	v_mfma_f32_16x16x32_bf16 v[122:125], v[158:161], v[182:185], v[122:125]
	v_mfma_f32_16x16x32_bf16 v[114:117], v[144:147], v[190:193], v[114:117]
	v_mfma_f32_16x16x32_bf16 v[106:109], v[158:161], v[190:193], v[106:109]
	v_mfma_f32_16x16x32_bf16 v[94:97], v[144:147], v[198:201], v[94:97]
	v_mfma_f32_16x16x32_bf16 v[90:93], v[158:161], v[198:201], v[90:93]
	v_mfma_f32_16x16x32_bf16 v[82:85], v[144:147], v[206:209], v[82:85]
	v_mfma_f32_16x16x32_bf16 v[74:77], v[158:161], v[206:209], v[74:77]
	v_mfma_f32_16x16x32_bf16 v[126:129], v[154:157], v[186:189], v[126:129]
	v_mfma_f32_16x16x32_bf16 v[122:125], v[162:165], v[186:189], v[122:125]
	v_mfma_f32_16x16x32_bf16 v[114:117], v[154:157], v[194:197], v[114:117]
	v_mfma_f32_16x16x32_bf16 v[106:109], v[162:165], v[194:197], v[106:109]
	v_mfma_f32_16x16x32_bf16 v[94:97], v[154:157], v[202:205], v[94:97]
	v_mfma_f32_16x16x32_bf16 v[90:93], v[162:165], v[202:205], v[90:93]
	v_mfma_f32_16x16x32_bf16 v[82:85], v[154:157], v[210:213], v[82:85]
	v_mfma_f32_16x16x32_bf16 v[74:77], v[162:165], v[210:213], v[74:77]
	s_setprio 0
	s_setprio 1
	v_mfma_f32_16x16x32_bf16 v[118:121], v[166:169], v[182:185], v[118:121]
	v_mfma_f32_16x16x32_bf16 v[110:113], v[174:177], v[182:185], v[110:113]
	v_mfma_f32_16x16x32_bf16 v[102:105], v[166:169], v[190:193], v[102:105]
	v_mfma_f32_16x16x32_bf16 v[98:101], v[174:177], v[190:193], v[98:101]
	v_mfma_f32_16x16x32_bf16 v[86:89], v[166:169], v[198:201], v[86:89]
	v_mfma_f32_16x16x32_bf16 v[78:81], v[174:177], v[198:201], v[78:81]
	v_mfma_f32_16x16x32_bf16 v[70:73], v[166:169], v[206:209], v[70:73]
	v_mfma_f32_16x16x32_bf16 v[66:69], v[174:177], v[206:209], v[66:69]
	v_mfma_f32_16x16x32_bf16 v[118:121], v[170:173], v[186:189], v[118:121]
	v_mfma_f32_16x16x32_bf16 v[110:113], v[178:181], v[186:189], v[110:113]
	v_mfma_f32_16x16x32_bf16 v[102:105], v[170:173], v[194:197], v[102:105]
	v_mfma_f32_16x16x32_bf16 v[98:101], v[178:181], v[194:197], v[98:101]
	v_mfma_f32_16x16x32_bf16 v[86:89], v[170:173], v[202:205], v[86:89]
	v_mfma_f32_16x16x32_bf16 v[78:81], v[178:181], v[202:205], v[78:81]
	v_mfma_f32_16x16x32_bf16 v[70:73], v[170:173], v[210:213], v[70:73]
	v_mfma_f32_16x16x32_bf16 v[66:69], v[178:181], v[210:213], v[66:69]
	s_setprio 0
	s_barrier
; #define PG8_STAGE(bufoff, gbase, voff) do { _Pragma("unroll") for (int _i = 0; _i < 2; ++_i) \
;         __builtin_amdgcn_global_load_lds((const unsigned*)((const char*)(gbase) + (voff)[_i]), (LAS unsigned*)(lds + (bufoff) + ldsw + _i * 8192), 16, 0, 0); } while (0)
; #define PG8_STAGE_A(bufoff, h, kp, nx) do { if constexpr (GATHER) { const unsigned _p = (nx) ? ng[h] : cg[h]; unsigned _v[2]; _v[0] = (_p & 0xffffu) * lda + CA2[0]; _v[1] = (_p >> 16) * lda + CA2[1]; PG8_STAGE(bufoff, kp, _v); } \
;         else { PG8_STAGE(bufoff, (kp) + (h) * hstepA, voffA); } } while (0)
; #define PG8_LDA(dst, b, h) do { _Pragma("unroll") for (int m = 0; m < 4; ++m) _Pragma("unroll") for (int k = 0; k < 2; ++k) dst[m][k] = *(const LAS bf16x8*)(lds + PG8_SA(b, h) + aoff + m * 2048 + k * 1024); } while (0)
; #define PG8_MMA(ai, bj, At, Bt) do { __builtin_amdgcn_s_setprio(1); _Pragma("unroll") for (int m = 0; m < 4; ++m) _Pragma("unroll") for (int n = 0; n < 2; ++n) _Pragma("unroll") for (int k = 0; k < 2; ++k) \
;         acc[ai][bj][m][n] = __builtin_amdgcn_mfma_f32_16x16x32_bf16(Bt[n][k], At[m][k], acc[ai][bj][m][n], 0, 0, 0); __builtin_amdgcn_s_setprio(0); } while (0)
; #define PG8_WAIT_V(n) asm volatile("s_waitcnt vmcnt(" #n ")" ::: "memory")
; #define PG8_WAIT_L(n) asm volatile("s_waitcnt lgkmcnt(" #n ")" ::: "memory")
; #define PG8_BAR __builtin_amdgcn_s_barrier()
; #define PG8_SCHED __builtin_amdgcn_sched_barrier(0)
;     ...
;             PG8_LDA(At, 1, 1); PG8_STAGE(PG8_SB(1, 0), b3, voffB); PG8_STAGE(PG8_SB(1, 1), b3 + hstepB, voffB); PG8_STAGE_A(PG8_SA(1, 0), 0, a3, last);
;             PG8_WAIT_V(8); PG8_WAIT_L(0); PG8_BAR; if (cur.amask & 2) { PG8_MMA(1, 0, At, B0); PG8_MMA(1, 1, At, B1); } PG8_BAR; PG8_SCHED;
;         }
;         if constexpr (ALIGN_EPI) { if (wr == 0) PG8_BAR; }
	s_add_i32 s16, s18, s43
	v_lshl_add_u64 v[148:149], v[148:149], 0, s[92:93]
	s_mov_b32 m0, s16
	ds_read_b128 v[182:185], v152 offset:49152
	ds_read_b128 v[186:189], v152 offset:50176
	ds_read_b128 v[190:193], v152 offset:51200
	ds_read_b128 v[194:197], v152 offset:52224
	ds_read_b128 v[198:201], v152 offset:53248
	ds_read_b128 v[202:205], v152 offset:54272
	ds_read_b128 v[206:209], v152 offset:55296
	ds_read_b128 v[210:213], v152 offset:56320
	global_load_lds_dwordx4 v[148:149], off
	s_add_i32 m0, s16, 0x2000
	s_add_u32 s16, s50, 0x80080
	v_lshl_add_u64 v[148:149], v[214:215], 0, s[92:93]
	s_addc_u32 s17, s51, 0
	s_add_i32 s18, s19, s43
	global_load_lds_dwordx4 v[148:149], off
	v_lshl_add_u64 v[148:149], s[16:17], 0, v[0:1]
	s_mov_b32 m0, s18
	s_nop 0
	global_load_lds_dwordx4 v[148:149], off
	v_lshl_add_u64 v[148:149], s[16:17], 0, v[134:135]
	s_add_i32 m0, s18, 0x2000
	s_nop 0
	global_load_lds_dwordx4 v[148:149], off
	v_lshl_add_u64 v[148:149], v[224:225], 0, s[92:93]
	s_mov_b32 m0, s10
	s_nop 0
	global_load_lds_dwordx4 v[148:149], off
	v_lshl_add_u64 v[148:149], v[226:227], 0, s[92:93]
	s_mov_b32 m0, s11
	s_nop 0
	global_load_lds_dwordx4 v[148:149], off
	s_waitcnt vmcnt(8)
	s_waitcnt lgkmcnt(0)
	s_barrier
	s_setprio 1
	s_waitcnt lgkmcnt(0)
	v_mfma_f32_16x16x32_bf16 v[62:65], v[144:147], v[182:185], v[62:65]
	v_mfma_f32_16x16x32_bf16 v[58:61], v[158:161], v[182:185], v[58:61]
	v_mfma_f32_16x16x32_bf16 v[50:53], v[144:147], v[190:193], v[50:53]
	v_mfma_f32_16x16x32_bf16 v[42:45], v[158:161], v[190:193], v[42:45]
	v_mfma_f32_16x16x32_bf16 v[30:33], v[144:147], v[198:201], v[30:33]
	v_mfma_f32_16x16x32_bf16 v[26:29], v[158:161], v[198:201], v[26:29]
	v_mfma_f32_16x16x32_bf16 v[18:21], v[144:147], v[206:209], v[18:21]
	v_mfma_f32_16x16x32_bf16 v[10:13], v[158:161], v[206:209], v[10:13]
	v_mfma_f32_16x16x32_bf16 v[62:65], v[154:157], v[186:189], v[62:65]
	v_mfma_f32_16x16x32_bf16 v[58:61], v[162:165], v[186:189], v[58:61]
	v_mfma_f32_16x16x32_bf16 v[50:53], v[154:157], v[194:197], v[50:53]
	v_mfma_f32_16x16x32_bf16 v[42:45], v[162:165], v[194:197], v[42:45]
	v_mfma_f32_16x16x32_bf16 v[30:33], v[154:157], v[202:205], v[30:33]
	v_mfma_f32_16x16x32_bf16 v[26:29], v[162:165], v[202:205], v[26:29]
	v_mfma_f32_16x16x32_bf16 v[18:21], v[154:157], v[210:213], v[18:21]
	v_mfma_f32_16x16x32_bf16 v[10:13], v[162:165], v[210:213], v[10:13]
	s_setprio 0
	s_setprio 1
	v_mfma_f32_16x16x32_bf16 v[54:57], v[166:169], v[182:185], v[54:57]
	v_mfma_f32_16x16x32_bf16 v[46:49], v[174:177], v[182:185], v[46:49]
	v_mfma_f32_16x16x32_bf16 v[38:41], v[166:169], v[190:193], v[38:41]
	v_mfma_f32_16x16x32_bf16 v[34:37], v[174:177], v[190:193], v[34:37]
	v_mfma_f32_16x16x32_bf16 v[22:25], v[166:169], v[198:201], v[22:25]
	v_mfma_f32_16x16x32_bf16 v[14:17], v[174:177], v[198:201], v[14:17]
	v_mfma_f32_16x16x32_bf16 v[6:9], v[166:169], v[206:209], v[6:9]
	v_mfma_f32_16x16x32_bf16 v[2:5], v[174:177], v[206:209], v[2:5]
	v_mfma_f32_16x16x32_bf16 v[54:57], v[170:173], v[186:189], v[54:57]
	v_mfma_f32_16x16x32_bf16 v[46:49], v[178:181], v[186:189], v[46:49]
	v_mfma_f32_16x16x32_bf16 v[38:41], v[170:173], v[194:197], v[38:41]
	v_mfma_f32_16x16x32_bf16 v[34:37], v[178:181], v[194:197], v[34:37]
	v_mfma_f32_16x16x32_bf16 v[22:25], v[170:173], v[202:205], v[22:25]
	v_mfma_f32_16x16x32_bf16 v[14:17], v[178:181], v[202:205], v[14:17]
	v_mfma_f32_16x16x32_bf16 v[6:9], v[170:173], v[210:213], v[6:9]
	v_mfma_f32_16x16x32_bf16 v[2:5], v[178:181], v[210:213], v[2:5]
	s_setprio 0
	s_add_i32 s15, s15, 2
	s_add_u32 s48, s48, 0x100
	s_addc_u32 s49, s49, 0
	s_add_u32 s13, s13, 0x100
	s_addc_u32 s14, s14, 0
	s_cmp_gt_u32 s15, 29
	s_barrier
	s_cbranch_scc0 .LBB0_1117
	v_readlane_b32 s14, v252, 14
	v_readlane_b32 s15, v252, 15
	s_and_b64 vcc, exec, s[14:15]
	s_cbranch_vccz .LBB0_1120
	s_barrier

; #define PG8_STAGE(bufoff, gbase, voff) do { _Pragma("unroll") for (int _i = 0; _i < 2; ++_i) \
;         __builtin_amdgcn_global_load_lds((const unsigned*)((const char*)(gbase) + (voff)[_i]), (LAS unsigned*)(lds + (bufoff) + ldsw + _i * 8192), 16, 0, 0); } while (0)
; #define PG8_STAGE_A(bufoff, h, kp, nx) do { if constexpr (GATHER) { const unsigned _p = (nx) ? ng[h] : cg[h]; unsigned _v[2]; _v[0] = (_p & 0xffffu) * lda + CA2[0]; _v[1] = (_p >> 16) * lda + CA2[1]; PG8_STAGE(bufoff, kp, _v); } \
;         else { PG8_STAGE(bufoff, (kp) + (h) * hstepA, voffA); } } while (0)
; #define PG8_LDA(dst, b, h) do { _Pragma("unroll") for (int m = 0; m < 4; ++m) _Pragma("unroll") for (int k = 0; k < 2; ++k) dst[m][k] = *(const LAS bf16x8*)(lds + PG8_SA(b, h) + aoff + m * 2048 + k * 1024); } while (0)
; #define PG8_LDB(dst, b, h) do { _Pragma("unroll") for (int n = 0; n < 2; ++n) _Pragma("unroll") for (int k = 0; k < 2; ++k) dst[n][k] = *(const LAS bf16x8*)(lds + PG8_SB(b, h) + boff + n * 2048 + k * 1024); } while (0)
; #define PG8_MMA(ai, bj, At, Bt) do { __builtin_amdgcn_s_setprio(1); _Pragma("unroll") for (int m = 0; m < 4; ++m) _Pragma("unroll") for (int n = 0; n < 2; ++n) _Pragma("unroll") for (int k = 0; k < 2; ++k) \
;         acc[ai][bj][m][n] = __builtin_amdgcn_mfma_f32_16x16x32_bf16(Bt[n][k], At[m][k], acc[ai][bj][m][n], 0, 0, 0); __builtin_amdgcn_s_setprio(0); } while (0)
; #define PG8_WAIT_V(n) asm volatile("s_waitcnt vmcnt(" #n ")" ::: "memory")
;     ...
;         for (int t = 0; t < nt; t += 2) {
;             const bool last = (t == nt - 2);
;             const char* a1 = cA + (size_t)(t + 1) * kstep;
;             const char* a2 = last ? nA : cA + (size_t)(t + 2) * kstep; const char* b2 = last ? nB : cB + (size_t)(t + 2) * kstep;
;             const char* a3 = a2 + kstep; const char* b3 = b2 + kstep;
;             PG8_LDB(B0, 0, 0); PG8_LDB(B1, 0, 1); PG8_SCHED; PG8_LDA(At, 0, 0); PG8_STAGE_A(PG8_SA(1, 1), 1, a1, false);
;             PG8_WAIT_V(8); PG8_WAIT_L(0); PG8_BAR; if (cur.amask & 1) { PG8_MMA(0, 0, At, B0); PG8_MMA(0, 1, At, B1); } PG8_BAR; PG8_SCHED;
;             PG8_LDA(At, 0, 1); PG8_STAGE(PG8_SB(0, 0), b2, voffB); PG8_STAGE(PG8_SB(0, 1), b2 + hstepB, voffB); PG8_STAGE_A(PG8_SA(0, 0), 0, a2, last);
;             PG8_WAIT_V(8); PG8_WAIT_L(0); PG8_BAR; if (cur.amask & 2) { PG8_MMA(1, 0, At, B0); PG8_MMA(1, 1, At, B1); } PG8_BAR; PG8_SCHED;
.LBB0_1205:
	s_add_u32 s22, s44, 0xfff80080
	s_addc_u32 s23, s45, -1
	s_add_i32 s24, 0, 0x10000
	s_cmp_eq_u32 s21, 28
	s_cselect_b32 s49, s37, s23
	s_cselect_b32 s48, s36, s22
	v_add_u32_e32 v149, s24, v147
	s_cselect_b32 s47, s39, s20
	s_cselect_b32 s46, s38, s19
	s_add_i32 s25, 0, 0x14000
	ds_read_b128 v[142:145], v149
	ds_read_b128 v[150:153], v149 offset:1024
	ds_read_b128 v[154:157], v149 offset:2048
	ds_read_b128 v[158:161], v149 offset:3072
	v_add_u32_e32 v149, s25, v147
	ds_read_b128 v[162:165], v149
	ds_read_b128 v[166:169], v149 offset:1024
	ds_read_b128 v[170:173], v149 offset:2048
	ds_read_b128 v[174:177], v149 offset:3072
	v_lshl_add_u64 v[210:211], s[44:45], 0, v[138:139]
	s_add_i32 m0, s10, 0xc000
	ds_read_b128 v[178:181], v148
	ds_read_b128 v[182:185], v148 offset:1024
	ds_read_b128 v[186:189], v148 offset:2048
	ds_read_b128 v[190:193], v148 offset:3072
	ds_read_b128 v[194:197], v148 offset:4096
	ds_read_b128 v[198:201], v148 offset:5120
	ds_read_b128 v[202:205], v148 offset:6144
	ds_read_b128 v[206:209], v148 offset:7168
	global_load_lds_dwordx4 v[210:211], off
	v_lshl_add_u64 v[210:211], s[44:45], 0, v[140:141]
	s_add_i32 m0, s10, 0xe000
	s_nop 0
	global_load_lds_dwordx4 v[210:211], off
	s_waitcnt vmcnt(8)
	s_waitcnt lgkmcnt(0)
	s_barrier
	s_setprio 1
	s_waitcnt lgkmcnt(0)
	v_mfma_f32_16x16x32_bf16 v[126:129], v[142:145], v[178:181], v[126:129]
	v_mfma_f32_16x16x32_bf16 v[122:125], v[154:157], v[178:181], v[122:125]
	v_mfma_f32_16x16x32_bf16 v[118:121], v[142:145], v[186:189], v[118:121]
	v_mfma_f32_16x16x32_bf16 v[110:113], v[154:157], v[186:189], v[110:113]
	v_mfma_f32_16x16x32_bf16 v[102:105], v[142:145], v[194:197], v[102:105]
	v_mfma_f32_16x16x32_bf16 v[94:97], v[154:157], v[194:197], v[94:97]
	v_mfma_f32_16x16x32_bf16 v[86:89], v[142:145], v[202:205], v[86:89]
	v_mfma_f32_16x16x32_bf16 v[78:81], v[154:157], v[202:205], v[78:81]
	v_mfma_f32_16x16x32_bf16 v[126:129], v[150:153], v[182:185], v[126:129]
	v_mfma_f32_16x16x32_bf16 v[122:125], v[158:161], v[182:185], v[122:125]
	v_mfma_f32_16x16x32_bf16 v[118:121], v[150:153], v[190:193], v[118:121]
	v_mfma_f32_16x16x32_bf16 v[110:113], v[158:161], v[190:193], v[110:113]
	v_mfma_f32_16x16x32_bf16 v[102:105], v[150:153], v[198:201], v[102:105]
	v_mfma_f32_16x16x32_bf16 v[94:97], v[158:161], v[198:201], v[94:97]
	v_mfma_f32_16x16x32_bf16 v[86:89], v[150:153], v[206:209], v[86:89]
	v_mfma_f32_16x16x32_bf16 v[78:81], v[158:161], v[206:209], v[78:81]
	s_setprio 0
	s_setprio 1
	v_mfma_f32_16x16x32_bf16 v[114:117], v[162:165], v[178:181], v[114:117]
	v_mfma_f32_16x16x32_bf16 v[106:109], v[170:173], v[178:181], v[106:109]
	v_mfma_f32_16x16x32_bf16 v[98:101], v[162:165], v[186:189], v[98:101]
	v_mfma_f32_16x16x32_bf16 v[90:93], v[170:173], v[186:189], v[90:93]
	v_mfma_f32_16x16x32_bf16 v[82:85], v[162:165], v[194:197], v[82:85]
	v_mfma_f32_16x16x32_bf16 v[74:77], v[170:173], v[194:197], v[74:77]
	v_mfma_f32_16x16x32_bf16 v[70:73], v[162:165], v[202:205], v[70:73]
	v_mfma_f32_16x16x32_bf16 v[66:69], v[170:173], v[202:205], v[66:69]
	v_mfma_f32_16x16x32_bf16 v[114:117], v[166:169], v[182:185], v[114:117]
	v_mfma_f32_16x16x32_bf16 v[106:109], v[174:177], v[182:185], v[106:109]
	v_mfma_f32_16x16x32_bf16 v[98:101], v[166:169], v[190:193], v[98:101]
	v_mfma_f32_16x16x32_bf16 v[90:93], v[174:177], v[190:193], v[90:93]
	v_mfma_f32_16x16x32_bf16 v[82:85], v[166:169], v[198:201], v[82:85]
	v_mfma_f32_16x16x32_bf16 v[74:77], v[174:177], v[198:201], v[74:77]
	v_mfma_f32_16x16x32_bf16 v[70:73], v[166:169], v[206:209], v[70:73]
	v_mfma_f32_16x16x32_bf16 v[66:69], v[174:177], v[206:209], v[66:69]
	s_setprio 0
	s_barrier
	s_add_i32 s22, s24, s43
	v_lshl_add_u64 v[210:211], s[46:47], 0, v[0:1]
	s_mov_b32 m0, s22
	ds_read_b128 v[178:181], v148 offset:16384
	ds_read_b128 v[182:185], v148 offset:17408
	ds_read_b128 v[186:189], v148 offset:18432
	ds_read_b128 v[190:193], v148 offset:19456
	ds_read_b128 v[194:197], v148 offset:20480
	ds_read_b128 v[198:201], v148 offset:21504
	ds_read_b128 v[202:205], v148 offset:22528
	ds_read_b128 v[206:209], v148 offset:23552
	global_load_lds_dwordx4 v[210:211], off
	s_add_i32 m0, s22, 0x2000
	s_add_u32 s22, s46, 0x80000
	v_lshl_add_u64 v[212:213], s[46:47], 0, v[134:135]
	s_addc_u32 s23, s47, 0
	s_add_i32 s24, s25, s43
	global_load_lds_dwordx4 v[212:213], off
	v_lshl_add_u64 v[214:215], s[22:23], 0, v[0:1]
	s_mov_b32 m0, s24
	v_lshl_add_u64 v[224:225], s[48:49], 0, v[132:133]
	global_load_lds_dwordx4 v[214:215], off
	v_lshl_add_u64 v[214:215], s[22:23], 0, v[134:135]
	s_add_i32 m0, s24, 0x2000
	s_nop 0
	global_load_lds_dwordx4 v[214:215], off
	v_lshl_add_u64 v[214:215], s[48:49], 0, v[130:131]
	s_mov_b32 m0, s10
	s_nop 0
	global_load_lds_dwordx4 v[214:215], off
	s_mov_b32 m0, s11
	s_nop 0
	global_load_lds_dwordx4 v[224:225], off
	s_waitcnt vmcnt(8)
	s_waitcnt lgkmcnt(0)
	s_barrier
; #define PG8_STAGE(bufoff, gbase, voff) do { _Pragma("unroll") for (int _i = 0; _i < 2; ++_i) \
;         __builtin_amdgcn_global_load_lds((const unsigned*)((const char*)(gbase) + (voff)[_i]), (LAS unsigned*)(lds + (bufoff) + ldsw + _i * 8192), 16, 0, 0); } while (0)
; #define PG8_STAGE_A(bufoff, h, kp, nx) do { if constexpr (GATHER) { const unsigned _p = (nx) ? ng[h] : cg[h]; unsigned _v[2]; _v[0] = (_p & 0xffffu) * lda + CA2[0]; _v[1] = (_p >> 16) * lda + CA2[1]; PG8_STAGE(bufoff, kp, _v); } \
;         else { PG8_STAGE(bufoff, (kp) + (h) * hstepA, voffA); } } while (0)
; #define PG8_LDA(dst, b, h) do { _Pragma("unroll") for (int m = 0; m < 4; ++m) _Pragma("unroll") for (int k = 0; k < 2; ++k) dst[m][k] = *(const LAS bf16x8*)(lds + PG8_SA(b, h) + aoff + m * 2048 + k * 1024); } while (0)
; #define PG8_LDB(dst, b, h) do { _Pragma("unroll") for (int n = 0; n < 2; ++n) _Pragma("unroll") for (int k = 0; k < 2; ++k) dst[n][k] = *(const LAS bf16x8*)(lds + PG8_SB(b, h) + boff + n * 2048 + k * 1024); } while (0)
; #define PG8_MMA(ai, bj, At, Bt) do { __builtin_amdgcn_s_setprio(1); _Pragma("unroll") for (int m = 0; m < 4; ++m) _Pragma("unroll") for (int n = 0; n < 2; ++n) _Pragma("unroll") for (int k = 0; k < 2; ++k) \
;         acc[ai][bj][m][n] = __builtin_amdgcn_mfma_f32_16x16x32_bf16(Bt[n][k], At[m][k], acc[ai][bj][m][n], 0, 0, 0); __builtin_amdgcn_s_setprio(0); } while (0)
; #define PG8_WAIT_V(n) asm volatile("s_waitcnt vmcnt(" #n ")" ::: "memory")
; #define PG8_WAIT_L(n) asm volatile("s_waitcnt lgkmcnt(" #n ")" ::: "memory")
; #define PG8_BAR __builtin_amdgcn_s_barrier()
; #define PG8_SCHED __builtin_amdgcn_sched_barrier(0)
;     ...
;             PG8_WAIT_V(8); PG8_WAIT_L(0); PG8_BAR; if (cur.amask & 2) { PG8_MMA(1, 0, At, B0); PG8_MMA(1, 1, At, B1); } PG8_BAR; PG8_SCHED;
;             PG8_LDB(B0, 1, 0); PG8_LDB(B1, 1, 1); PG8_SCHED; PG8_LDA(At, 1, 0); PG8_STAGE_A(PG8_SA(0, 1), 1, a2, last);
;             PG8_WAIT_V(8); PG8_WAIT_L(0); PG8_BAR; if (cur.amask & 1) { PG8_MMA(0, 0, At, B0); PG8_MMA(0, 1, At, B1); } PG8_BAR; PG8_SCHED;
;             PG8_LDA(At, 1, 1); PG8_STAGE(PG8_SB(1, 0), b3, voffB); PG8_STAGE(PG8_SB(1, 1), b3 + hstepB, voffB); PG8_STAGE_A(PG8_SA(1, 0), 0, a3, last);
	s_setprio 1
	s_waitcnt lgkmcnt(0)
	v_mfma_f32_16x16x32_bf16 v[62:65], v[142:145], v[178:181], v[62:65]
	v_mfma_f32_16x16x32_bf16 v[58:61], v[154:157], v[178:181], v[58:61]
	v_mfma_f32_16x16x32_bf16 v[54:57], v[142:145], v[186:189], v[54:57]
	v_mfma_f32_16x16x32_bf16 v[46:49], v[154:157], v[186:189], v[46:49]
	v_mfma_f32_16x16x32_bf16 v[38:41], v[142:145], v[194:197], v[38:41]
	v_mfma_f32_16x16x32_bf16 v[30:33], v[154:157], v[194:197], v[30:33]
	v_mfma_f32_16x16x32_bf16 v[22:25], v[142:145], v[202:205], v[22:25]
	v_mfma_f32_16x16x32_bf16 v[14:17], v[154:157], v[202:205], v[14:17]
	v_mfma_f32_16x16x32_bf16 v[62:65], v[150:153], v[182:185], v[62:65]
	v_mfma_f32_16x16x32_bf16 v[58:61], v[158:161], v[182:185], v[58:61]
	v_mfma_f32_16x16x32_bf16 v[54:57], v[150:153], v[190:193], v[54:57]
	v_mfma_f32_16x16x32_bf16 v[46:49], v[158:161], v[190:193], v[46:49]
	v_mfma_f32_16x16x32_bf16 v[38:41], v[150:153], v[198:201], v[38:41]
	v_mfma_f32_16x16x32_bf16 v[30:33], v[158:161], v[198:201], v[30:33]
	v_mfma_f32_16x16x32_bf16 v[22:25], v[150:153], v[206:209], v[22:25]
	v_mfma_f32_16x16x32_bf16 v[14:17], v[158:161], v[206:209], v[14:17]
	s_setprio 0
	s_setprio 1
	v_mfma_f32_16x16x32_bf16 v[50:53], v[162:165], v[178:181], v[50:53]
	v_mfma_f32_16x16x32_bf16 v[42:45], v[170:173], v[178:181], v[42:45]
	v_mfma_f32_16x16x32_bf16 v[34:37], v[162:165], v[186:189], v[34:37]
	v_mfma_f32_16x16x32_bf16 v[26:29], v[170:173], v[186:189], v[26:29]
	v_mfma_f32_16x16x32_bf16 v[18:21], v[162:165], v[194:197], v[18:21]
	v_mfma_f32_16x16x32_bf16 v[10:13], v[170:173], v[194:197], v[10:13]
	v_mfma_f32_16x16x32_bf16 v[6:9], v[162:165], v[202:205], v[6:9]
	v_mfma_f32_16x16x32_bf16 v[2:5], v[170:173], v[202:205], v[2:5]
	v_mfma_f32_16x16x32_bf16 v[50:53], v[166:169], v[182:185], v[50:53]
	v_mfma_f32_16x16x32_bf16 v[42:45], v[174:177], v[182:185], v[42:45]
	v_mfma_f32_16x16x32_bf16 v[34:37], v[166:169], v[190:193], v[34:37]
	v_mfma_f32_16x16x32_bf16 v[26:29], v[174:177], v[190:193], v[26:29]
	v_mfma_f32_16x16x32_bf16 v[18:21], v[166:169], v[198:201], v[18:21]
	v_mfma_f32_16x16x32_bf16 v[10:13], v[174:177], v[198:201], v[10:13]
	v_mfma_f32_16x16x32_bf16 v[6:9], v[166:169], v[206:209], v[6:9]
	v_mfma_f32_16x16x32_bf16 v[2:5], v[174:177], v[206:209], v[2:5]
	s_setprio 0
	s_barrier
	s_add_i32 s24, 0, 0x18000
	v_add_u32_e32 v149, s24, v147
	s_add_i32 s25, 0, 0x1c000
	ds_read_b128 v[142:145], v149
	ds_read_b128 v[150:153], v149 offset:1024
	ds_read_b128 v[154:157], v149 offset:2048
	ds_read_b128 v[158:161], v149 offset:3072
	v_add_u32_e32 v149, s25, v147
	ds_read_b128 v[162:165], v149
	ds_read_b128 v[166:169], v149 offset:1024
	ds_read_b128 v[170:173], v149 offset:2048
	ds_read_b128 v[174:177], v149 offset:3072
	s_add_u32 s22, s48, 0x80000
	s_addc_u32 s23, s49, 0
	s_mov_b32 m0, s12
	v_lshl_add_u64 v[226:227], s[22:23], 0, v[130:131]
	ds_read_b128 v[178:181], v148 offset:32768
	ds_read_b128 v[182:185], v148 offset:33792
	ds_read_b128 v[186:189], v148 offset:34816
	ds_read_b128 v[190:193], v148 offset:35840
	ds_read_b128 v[194:197], v148 offset:36864
	ds_read_b128 v[198:201], v148 offset:37888
	ds_read_b128 v[202:205], v148 offset:38912
	ds_read_b128 v[206:209], v148 offset:39936
	global_load_lds_dwordx4 v[226:227], off
	v_lshl_add_u64 v[226:227], s[22:23], 0, v[132:133]
	s_mov_b32 m0, s13
	s_nop 0
	global_load_lds_dwordx4 v[226:227], off
	s_waitcnt vmcnt(8)
	s_waitcnt lgkmcnt(0)
	s_barrier
	s_setprio 1
	s_waitcnt lgkmcnt(0)
	v_mfma_f32_16x16x32_bf16 v[126:129], v[142:145], v[178:181], v[126:129]
	v_mfma_f32_16x16x32_bf16 v[122:125], v[154:157], v[178:181], v[122:125]
	v_mfma_f32_16x16x32_bf16 v[118:121], v[142:145], v[186:189], v[118:121]
	v_mfma_f32_16x16x32_bf16 v[110:113], v[154:157], v[186:189], v[110:113]
	v_mfma_f32_16x16x32_bf16 v[102:105], v[142:145], v[194:197], v[102:105]
	v_mfma_f32_16x16x32_bf16 v[94:97], v[154:157], v[194:197], v[94:97]
	v_mfma_f32_16x16x32_bf16 v[86:89], v[142:145], v[202:205], v[86:89]
	v_mfma_f32_16x16x32_bf16 v[78:81], v[154:157], v[202:205], v[78:81]
	v_mfma_f32_16x16x32_bf16 v[126:129], v[150:153], v[182:185], v[126:129]
	v_mfma_f32_16x16x32_bf16 v[122:125], v[158:161], v[182:185], v[122:125]
	v_mfma_f32_16x16x32_bf16 v[118:121], v[150:153], v[190:193], v[118:121]
	v_mfma_f32_16x16x32_bf16 v[110:113], v[158:161], v[190:193], v[110:113]
	v_mfma_f32_16x16x32_bf16 v[102:105], v[150:153], v[198:201], v[102:105]
	v_mfma_f32_16x16x32_bf16 v[94:97], v[158:161], v[198:201], v[94:97]
	v_mfma_f32_16x16x32_bf16 v[86:89], v[150:153], v[206:209], v[86:89]
	v_mfma_f32_16x16x32_bf16 v[78:81], v[158:161], v[206:209], v[78:81]
	s_setprio 0
	s_setprio 1
	v_mfma_f32_16x16x32_bf16 v[114:117], v[162:165], v[178:181], v[114:117]
	v_mfma_f32_16x16x32_bf16 v[106:109], v[170:173], v[178:181], v[106:109]
	v_mfma_f32_16x16x32_bf16 v[98:101], v[162:165], v[186:189], v[98:101]
	v_mfma_f32_16x16x32_bf16 v[90:93], v[170:173], v[186:189], v[90:93]
	v_mfma_f32_16x16x32_bf16 v[82:85], v[162:165], v[194:197], v[82:85]
	v_mfma_f32_16x16x32_bf16 v[74:77], v[170:173], v[194:197], v[74:77]
	v_mfma_f32_16x16x32_bf16 v[70:73], v[162:165], v[202:205], v[70:73]
	v_mfma_f32_16x16x32_bf16 v[66:69], v[170:173], v[202:205], v[66:69]
	v_mfma_f32_16x16x32_bf16 v[114:117], v[166:169], v[182:185], v[114:117]
	v_mfma_f32_16x16x32_bf16 v[106:109], v[174:177], v[182:185], v[106:109]
	v_mfma_f32_16x16x32_bf16 v[98:101], v[166:169], v[190:193], v[98:101]
	v_mfma_f32_16x16x32_bf16 v[90:93], v[174:177], v[190:193], v[90:93]
	v_mfma_f32_16x16x32_bf16 v[82:85], v[166:169], v[198:201], v[82:85]
	v_mfma_f32_16x16x32_bf16 v[74:77], v[174:177], v[198:201], v[74:77]
	v_mfma_f32_16x16x32_bf16 v[70:73], v[166:169], v[206:209], v[70:73]
	v_mfma_f32_16x16x32_bf16 v[66:69], v[174:177], v[206:209], v[66:69]
	s_setprio 0
	s_barrier
; #define PG8_STAGE(bufoff, gbase, voff) do { _Pragma("unroll") for (int _i = 0; _i < 2; ++_i) \
;         __builtin_amdgcn_global_load_lds((const unsigned*)((const char*)(gbase) + (voff)[_i]), (LAS unsigned*)(lds + (bufoff) + ldsw + _i * 8192), 16, 0, 0); } while (0)
; #define PG8_STAGE_A(bufoff, h, kp, nx) do { if constexpr (GATHER) { const unsigned _p = (nx) ? ng[h] : cg[h]; unsigned _v[2]; _v[0] = (_p & 0xffffu) * lda + CA2[0]; _v[1] = (_p >> 16) * lda + CA2[1]; PG8_STAGE(bufoff, kp, _v); } \
;         else { PG8_STAGE(bufoff, (kp) + (h) * hstepA, voffA); } } while (0)
; #define PG8_LDA(dst, b, h) do { _Pragma("unroll") for (int m = 0; m < 4; ++m) _Pragma("unroll") for (int k = 0; k < 2; ++k) dst[m][k] = *(const LAS bf16x8*)(lds + PG8_SA(b, h) + aoff + m * 2048 + k * 1024); } while (0)
; #define PG8_MMA(ai, bj, At, Bt) do { __builtin_amdgcn_s_setprio(1); _Pragma("unroll") for (int m = 0; m < 4; ++m) _Pragma("unroll") for (int n = 0; n < 2; ++n) _Pragma("unroll") for (int k = 0; k < 2; ++k) \
;         acc[ai][bj][m][n] = __builtin_amdgcn_mfma_f32_16x16x32_bf16(Bt[n][k], At[m][k], acc[ai][bj][m][n], 0, 0, 0); __builtin_amdgcn_s_setprio(0); } while (0)
; #define PG8_WAIT_V(n) asm volatile("s_waitcnt vmcnt(" #n ")" ::: "memory")
; #define PG8_WAIT_L(n) asm volatile("s_waitcnt lgkmcnt(" #n ")" ::: "memory")
; #define PG8_BAR __builtin_amdgcn_s_barrier()
; #define PG8_SCHED __builtin_amdgcn_sched_barrier(0)
;     ...
;             PG8_LDA(At, 1, 1); PG8_STAGE(PG8_SB(1, 0), b3, voffB); PG8_STAGE(PG8_SB(1, 1), b3 + hstepB, voffB); PG8_STAGE_A(PG8_SA(1, 0), 0, a3, last);
;             PG8_WAIT_V(8); PG8_WAIT_L(0); PG8_BAR; if (cur.amask & 2) { PG8_MMA(1, 0, At, B0); PG8_MMA(1, 1, At, B1); } PG8_BAR; PG8_SCHED;
;         }
;         if constexpr (ALIGN_EPI) { if (wr == 0) PG8_BAR; }
	s_add_i32 s22, s24, s43
	v_lshl_add_u64 v[210:211], v[210:211], 0, s[92:93]
	s_mov_b32 m0, s22
	ds_read_b128 v[178:181], v148 offset:49152
	ds_read_b128 v[182:185], v148 offset:50176
	ds_read_b128 v[186:189], v148 offset:51200
	ds_read_b128 v[190:193], v148 offset:52224
	ds_read_b128 v[194:197], v148 offset:53248
	ds_read_b128 v[198:201], v148 offset:54272
	ds_read_b128 v[202:205], v148 offset:55296
	ds_read_b128 v[206:209], v148 offset:56320
	global_load_lds_dwordx4 v[210:211], off
	s_add_i32 m0, s22, 0x2000
	s_add_u32 s22, s46, 0x80080
	v_lshl_add_u64 v[210:211], v[212:213], 0, s[92:93]
	s_addc_u32 s23, s47, 0
	s_add_i32 s24, s25, s43
	global_load_lds_dwordx4 v[210:211], off
	v_lshl_add_u64 v[210:211], s[22:23], 0, v[0:1]
	s_mov_b32 m0, s24
	s_nop 0
	global_load_lds_dwordx4 v[210:211], off
	v_lshl_add_u64 v[210:211], s[22:23], 0, v[134:135]
	s_add_i32 m0, s24, 0x2000
	s_nop 0
	global_load_lds_dwordx4 v[210:211], off
	v_lshl_add_u64 v[210:211], v[214:215], 0, s[92:93]
	s_mov_b32 m0, s16
	s_nop 0
	global_load_lds_dwordx4 v[210:211], off
	v_lshl_add_u64 v[210:211], v[224:225], 0, s[92:93]
	s_mov_b32 m0, s17
	s_nop 0
	global_load_lds_dwordx4 v[210:211], off
	s_waitcnt vmcnt(8)
	s_waitcnt lgkmcnt(0)
	s_barrier
	s_setprio 1
	s_waitcnt lgkmcnt(0)
	v_mfma_f32_16x16x32_bf16 v[62:65], v[142:145], v[178:181], v[62:65]
	v_mfma_f32_16x16x32_bf16 v[58:61], v[154:157], v[178:181], v[58:61]
	v_mfma_f32_16x16x32_bf16 v[54:57], v[142:145], v[186:189], v[54:57]
	v_mfma_f32_16x16x32_bf16 v[46:49], v[154:157], v[186:189], v[46:49]
	v_mfma_f32_16x16x32_bf16 v[38:41], v[142:145], v[194:197], v[38:41]
	v_mfma_f32_16x16x32_bf16 v[30:33], v[154:157], v[194:197], v[30:33]
	v_mfma_f32_16x16x32_bf16 v[22:25], v[142:145], v[202:205], v[22:25]
	v_mfma_f32_16x16x32_bf16 v[14:17], v[154:157], v[202:205], v[14:17]
	v_mfma_f32_16x16x32_bf16 v[62:65], v[150:153], v[182:185], v[62:65]
	v_mfma_f32_16x16x32_bf16 v[58:61], v[158:161], v[182:185], v[58:61]
	v_mfma_f32_16x16x32_bf16 v[54:57], v[150:153], v[190:193], v[54:57]
	v_mfma_f32_16x16x32_bf16 v[46:49], v[158:161], v[190:193], v[46:49]
	v_mfma_f32_16x16x32_bf16 v[38:41], v[150:153], v[198:201], v[38:41]
	v_mfma_f32_16x16x32_bf16 v[30:33], v[158:161], v[198:201], v[30:33]
	v_mfma_f32_16x16x32_bf16 v[22:25], v[150:153], v[206:209], v[22:25]
	v_mfma_f32_16x16x32_bf16 v[14:17], v[158:161], v[206:209], v[14:17]
	s_setprio 0
	s_setprio 1
	v_mfma_f32_16x16x32_bf16 v[50:53], v[162:165], v[178:181], v[50:53]
	v_mfma_f32_16x16x32_bf16 v[42:45], v[170:173], v[178:181], v[42:45]
	v_mfma_f32_16x16x32_bf16 v[34:37], v[162:165], v[186:189], v[34:37]
	v_mfma_f32_16x16x32_bf16 v[26:29], v[170:173], v[186:189], v[26:29]
	v_mfma_f32_16x16x32_bf16 v[18:21], v[162:165], v[194:197], v[18:21]
	v_mfma_f32_16x16x32_bf16 v[10:13], v[170:173], v[194:197], v[10:13]
	v_mfma_f32_16x16x32_bf16 v[6:9], v[162:165], v[202:205], v[6:9]
	v_mfma_f32_16x16x32_bf16 v[2:5], v[170:173], v[202:205], v[2:5]
	v_mfma_f32_16x16x32_bf16 v[50:53], v[166:169], v[182:185], v[50:53]
	v_mfma_f32_16x16x32_bf16 v[42:45], v[174:177], v[182:185], v[42:45]
	v_mfma_f32_16x16x32_bf16 v[34:37], v[166:169], v[190:193], v[34:37]
	v_mfma_f32_16x16x32_bf16 v[26:29], v[174:177], v[190:193], v[26:29]
	v_mfma_f32_16x16x32_bf16 v[18:21], v[166:169], v[198:201], v[18:21]
	v_mfma_f32_16x16x32_bf16 v[10:13], v[174:177], v[198:201], v[10:13]
	v_mfma_f32_16x16x32_bf16 v[6:9], v[166:169], v[206:209], v[6:9]
	v_mfma_f32_16x16x32_bf16 v[2:5], v[174:177], v[206:209], v[2:5]
	s_setprio 0
	s_add_i32 s21, s21, 2
	s_add_u32 s44, s44, 0x100
	s_addc_u32 s45, s45, 0
	s_add_u32 s19, s19, 0x100
	s_addc_u32 s20, s20, 0
	s_cmp_gt_u32 s21, 29
	s_barrier
	s_cbranch_scc0 .LBB0_1205
	v_readlane_b32 s20, v252, 14
	v_readlane_b32 s21, v252, 15
	s_and_b64 vcc, exec, s[20:21]
	s_cbranch_vccz .LBB0_1208
	s_barrier

; #define PG8_STAGE(bufoff, gbase, voff) do { _Pragma("unroll") for (int _i = 0; _i < 2; ++_i) \
;         __builtin_amdgcn_global_load_lds((const unsigned*)((const char*)(gbase) + (voff)[_i]), (LAS unsigned*)(lds + (bufoff) + ldsw + _i * 8192), 16, 0, 0); } while (0)
; #define PG8_STAGE_A(bufoff, h, kp, nx) do { if constexpr (GATHER) { const unsigned _p = (nx) ? ng[h] : cg[h]; unsigned _v[2]; _v[0] = (_p & 0xffffu) * lda + CA2[0]; _v[1] = (_p >> 16) * lda + CA2[1]; PG8_STAGE(bufoff, kp, _v); } \
;         else { PG8_STAGE(bufoff, (kp) + (h) * hstepA, voffA); } } while (0)
; #define PG8_LDA(dst, b, h) do { _Pragma("unroll") for (int m = 0; m < 4; ++m) _Pragma("unroll") for (int k = 0; k < 2; ++k) dst[m][k] = *(const LAS bf16x8*)(lds + PG8_SA(b, h) + aoff + m * 2048 + k * 1024); } while (0)
; #define PG8_WAIT_V(n) asm volatile("s_waitcnt vmcnt(" #n ")" ::: "memory")
;     ...
;         for (int t = 0; t < nt; t += 2) {
;             const bool last = (t == nt - 2);
;             const char* a1 = cA + (size_t)(t + 1) * kstep;
;             const char* a2 = last ? nA : cA + (size_t)(t + 2) * kstep; const char* b2 = last ? nB : cB + (size_t)(t + 2) * kstep;
;             const char* a3 = a2 + kstep; const char* b3 = b2 + kstep;
;             PG8_LDB(B0, 0, 0); PG8_LDB(B1, 0, 1); PG8_SCHED; PG8_LDA(At, 0, 0); PG8_STAGE_A(PG8_SA(1, 1), 1, a1, false);
;             PG8_WAIT_V(8); PG8_WAIT_L(0); PG8_BAR; if (cur.amask & 1) { PG8_MMA(0, 0, At, B0); PG8_MMA(0, 1, At, B1); } PG8_BAR; PG8_SCHED;
;             PG8_LDA(At, 0, 1); PG8_STAGE(PG8_SB(0, 0), b2, voffB); PG8_STAGE(PG8_SB(0, 1), b2 + hstepB, voffB); PG8_STAGE_A(PG8_SA(0, 0), 0, a2, last);
;             PG8_WAIT_V(8); PG8_WAIT_L(0); PG8_BAR; if (cur.amask & 2) { PG8_MMA(1, 0, At, B0); PG8_MMA(1, 1, At, B1); } PG8_BAR; PG8_SCHED;
;             PG8_LDB(B0, 1, 0); PG8_LDB(B1, 1, 1); PG8_SCHED; PG8_LDA(At, 1, 0); PG8_STAGE_A(PG8_SA(0, 1), 1, a2, last);
;             PG8_WAIT_V(8); PG8_WAIT_L(0); PG8_BAR; if (cur.amask & 1) { PG8_MMA(0, 0, At, B0); PG8_MMA(0, 1, At, B1); } PG8_BAR; PG8_SCHED;
;             PG8_LDA(At, 1, 1); PG8_STAGE(PG8_SB(1, 0), b3, voffB); PG8_STAGE(PG8_SB(1, 1), b3 + hstepB, voffB); PG8_STAGE_A(PG8_SA(1, 0), 0, a3, last);
;             PG8_WAIT_V(8); PG8_WAIT_L(0); PG8_BAR; if (cur.amask & 2) { PG8_MMA(1, 0, At, B0); PG8_MMA(1, 1, At, B1); } PG8_BAR; PG8_SCHED;
.LBB0_1280:
	s_add_u32 s23, s36, s56
	s_addc_u32 s24, s37, s57
	s_add_u32 s23, s23, 0x100
	s_addc_u32 s24, s24, 0
	s_add_u32 s25, s20, s56
	s_addc_u32 s26, s21, s57
	s_add_i32 s27, 0, 0x10000
	s_cmpk_eq_i32 s56, 0x300
	s_cselect_b32 s61, s53, s24
	s_cselect_b32 s60, s52, s23
	s_cselect_b32 s59, s41, s26
	s_cselect_b32 s58, s40, s25
	s_add_i32 s23, 0, 0x14000
	v_add_u32_e32 v160, s27, v146
	v_add_u32_e32 v176, s23, v146
	ds_read_b128 v[148:151], v160
	ds_read_b128 v[152:155], v160 offset:1024
	ds_read_b128 v[156:159], v160 offset:2048
	ds_read_b128 v[160:163], v160 offset:3072
	ds_read_b128 v[164:167], v176
	ds_read_b128 v[168:171], v176 offset:1024
	ds_read_b128 v[172:175], v176 offset:2048
	ds_read_b128 v[176:179], v176 offset:3072
	v_lshl_add_u64 v[212:213], v[140:141], 0, s[56:57]
	s_add_i32 m0, s10, 0xc000
	ds_read_b128 v[180:183], v147
	ds_read_b128 v[184:187], v147 offset:1024
	ds_read_b128 v[188:191], v147 offset:2048
	ds_read_b128 v[192:195], v147 offset:3072
	ds_read_b128 v[196:199], v147 offset:4096
	ds_read_b128 v[200:203], v147 offset:5120
	ds_read_b128 v[204:207], v147 offset:6144
	ds_read_b128 v[208:211], v147 offset:7168
	global_load_lds_dwordx4 v[212:213], off
	v_lshl_add_u64 v[212:213], v[142:143], 0, s[56:57]
	s_add_i32 m0, s10, 0xe000
	s_nop 0
	global_load_lds_dwordx4 v[212:213], off
	s_waitcnt vmcnt(8)
	s_waitcnt lgkmcnt(0)
	s_barrier
	s_setprio 1
	s_waitcnt lgkmcnt(0)
	v_mfma_f32_16x16x32_bf16 v[126:129], v[148:151], v[180:183], v[126:129]
	v_mfma_f32_16x16x32_bf16 v[122:125], v[156:159], v[180:183], v[122:125]
	v_mfma_f32_16x16x32_bf16 v[114:117], v[148:151], v[188:191], v[114:117]
	v_mfma_f32_16x16x32_bf16 v[106:109], v[156:159], v[188:191], v[106:109]
	v_mfma_f32_16x16x32_bf16 v[102:105], v[148:151], v[196:199], v[102:105]
	v_mfma_f32_16x16x32_bf16 v[94:97], v[156:159], v[196:199], v[94:97]
	v_mfma_f32_16x16x32_bf16 v[86:89], v[148:151], v[204:207], v[86:89]
	v_mfma_f32_16x16x32_bf16 v[78:81], v[156:159], v[204:207], v[78:81]
	v_mfma_f32_16x16x32_bf16 v[126:129], v[152:155], v[184:187], v[126:129]
	v_mfma_f32_16x16x32_bf16 v[122:125], v[160:163], v[184:187], v[122:125]
	v_mfma_f32_16x16x32_bf16 v[114:117], v[152:155], v[192:195], v[114:117]
	v_mfma_f32_16x16x32_bf16 v[106:109], v[160:163], v[192:195], v[106:109]
	v_mfma_f32_16x16x32_bf16 v[102:105], v[152:155], v[200:203], v[102:105]
	v_mfma_f32_16x16x32_bf16 v[94:97], v[160:163], v[200:203], v[94:97]
	v_mfma_f32_16x16x32_bf16 v[86:89], v[152:155], v[208:211], v[86:89]
	v_mfma_f32_16x16x32_bf16 v[78:81], v[160:163], v[208:211], v[78:81]
	s_setprio 0
	s_setprio 1
	v_mfma_f32_16x16x32_bf16 v[118:121], v[164:167], v[180:183], v[118:121]
	v_mfma_f32_16x16x32_bf16 v[110:113], v[172:175], v[180:183], v[110:113]
	v_mfma_f32_16x16x32_bf16 v[98:101], v[164:167], v[188:191], v[98:101]
	v_mfma_f32_16x16x32_bf16 v[90:93], v[172:175], v[188:191], v[90:93]
	v_mfma_f32_16x16x32_bf16 v[82:85], v[164:167], v[196:199], v[82:85]
	v_mfma_f32_16x16x32_bf16 v[74:77], v[172:175], v[196:199], v[74:77]
	v_mfma_f32_16x16x32_bf16 v[70:73], v[164:167], v[204:207], v[70:73]
	v_mfma_f32_16x16x32_bf16 v[66:69], v[172:175], v[204:207], v[66:69]
	v_mfma_f32_16x16x32_bf16 v[118:121], v[168:171], v[184:187], v[118:121]
	v_mfma_f32_16x16x32_bf16 v[110:113], v[176:179], v[184:187], v[110:113]
	v_mfma_f32_16x16x32_bf16 v[98:101], v[168:171], v[192:195], v[98:101]
	v_mfma_f32_16x16x32_bf16 v[90:93], v[176:179], v[192:195], v[90:93]
	v_mfma_f32_16x16x32_bf16 v[82:85], v[168:171], v[200:203], v[82:85]
	v_mfma_f32_16x16x32_bf16 v[74:77], v[176:179], v[200:203], v[74:77]
	v_mfma_f32_16x16x32_bf16 v[70:73], v[168:171], v[208:211], v[70:73]
	v_mfma_f32_16x16x32_bf16 v[66:69], v[176:179], v[208:211], v[66:69]
	s_setprio 0
	s_barrier
	s_add_i32 s24, s27, s43
	v_lshl_add_u64 v[212:213], s[58:59], 0, v[0:1]
	s_mov_b32 m0, s24
	ds_read_b128 v[180:183], v147 offset:16384
	ds_read_b128 v[184:187], v147 offset:17408
	ds_read_b128 v[188:191], v147 offset:18432
	ds_read_b128 v[192:195], v147 offset:19456
	ds_read_b128 v[196:199], v147 offset:20480
	ds_read_b128 v[200:203], v147 offset:21504
	ds_read_b128 v[204:207], v147 offset:22528
	ds_read_b128 v[208:211], v147 offset:23552
	global_load_lds_dwordx4 v[212:213], off
	s_add_i32 m0, s24, 0x2000
	s_add_u32 s24, s58, 0x80000
	v_lshl_add_u64 v[214:215], s[58:59], 0, v[130:131]
	s_addc_u32 s25, s59, 0
	s_add_i32 s23, s23, s43
	global_load_lds_dwordx4 v[214:215], off
	v_lshl_add_u64 v[224:225], s[24:25], 0, v[0:1]
	s_mov_b32 m0, s23
	v_lshl_add_u64 v[226:227], s[60:61], 0, v[132:133]
	global_load_lds_dwordx4 v[224:225], off
	v_lshl_add_u64 v[224:225], s[24:25], 0, v[130:131]
	s_add_i32 m0, s23, 0x2000
	s_nop 0
	global_load_lds_dwordx4 v[224:225], off
	v_lshl_add_u64 v[224:225], s[60:61], 0, v[134:135]
	s_mov_b32 m0, s10
	s_nop 0
	global_load_lds_dwordx4 v[224:225], off
	s_mov_b32 m0, s11
	s_nop 0
	global_load_lds_dwordx4 v[226:227], off
	s_waitcnt vmcnt(8)
	s_waitcnt lgkmcnt(0)
	s_barrier
; #define PG8_STAGE(bufoff, gbase, voff) do { _Pragma("unroll") for (int _i = 0; _i < 2; ++_i) \
;         __builtin_amdgcn_global_load_lds((const unsigned*)((const char*)(gbase) + (voff)[_i]), (LAS unsigned*)(lds + (bufoff) + ldsw + _i * 8192), 16, 0, 0); } while (0)
; #define PG8_STAGE_A(bufoff, h, kp, nx) do { if constexpr (GATHER) { const unsigned _p = (nx) ? ng[h] : cg[h]; unsigned _v[2]; _v[0] = (_p & 0xffffu) * lda + CA2[0]; _v[1] = (_p >> 16) * lda + CA2[1]; PG8_STAGE(bufoff, kp, _v); } \
;         else { PG8_STAGE(bufoff, (kp) + (h) * hstepA, voffA); } } while (0)
; #define PG8_LDA(dst, b, h) do { _Pragma("unroll") for (int m = 0; m < 4; ++m) _Pragma("unroll") for (int k = 0; k < 2; ++k) dst[m][k] = *(const LAS bf16x8*)(lds + PG8_SA(b, h) + aoff + m * 2048 + k * 1024); } while (0)
; #define PG8_LDB(dst, b, h) do { _Pragma("unroll") for (int n = 0; n < 2; ++n) _Pragma("unroll") for (int k = 0; k < 2; ++k) dst[n][k] = *(const LAS bf16x8*)(lds + PG8_SB(b, h) + boff + n * 2048 + k * 1024); } while (0)
; #define PG8_MMA(ai, bj, At, Bt) do { __builtin_amdgcn_s_setprio(1); _Pragma("unroll") for (int m = 0; m < 4; ++m) _Pragma("unroll") for (int n = 0; n < 2; ++n) _Pragma("unroll") for (int k = 0; k < 2; ++k) \
;         acc[ai][bj][m][n] = __builtin_amdgcn_mfma_f32_16x16x32_bf16(Bt[n][k], At[m][k], acc[ai][bj][m][n], 0, 0, 0); __builtin_amdgcn_s_setprio(0); } while (0)
; #define PG8_WAIT_V(n) asm volatile("s_waitcnt vmcnt(" #n ")" ::: "memory")
; #define PG8_WAIT_L(n) asm volatile("s_waitcnt lgkmcnt(" #n ")" ::: "memory")
; #define PG8_BAR __builtin_amdgcn_s_barrier()
; #define PG8_SCHED __builtin_amdgcn_sched_barrier(0)
;     ...
;             PG8_WAIT_V(8); PG8_WAIT_L(0); PG8_BAR; if (cur.amask & 2) { PG8_MMA(1, 0, At, B0); PG8_MMA(1, 1, At, B1); } PG8_BAR; PG8_SCHED;
;             PG8_LDB(B0, 1, 0); PG8_LDB(B1, 1, 1); PG8_SCHED; PG8_LDA(At, 1, 0); PG8_STAGE_A(PG8_SA(0, 1), 1, a2, last);
;             PG8_WAIT_V(8); PG8_WAIT_L(0); PG8_BAR; if (cur.amask & 1) { PG8_MMA(0, 0, At, B0); PG8_MMA(0, 1, At, B1); } PG8_BAR; PG8_SCHED;
;             PG8_LDA(At, 1, 1); PG8_STAGE(PG8_SB(1, 0), b3, voffB); PG8_STAGE(PG8_SB(1, 1), b3 + hstepB, voffB); PG8_STAGE_A(PG8_SA(1, 0), 0, a3, last);
;             PG8_WAIT_V(8); PG8_WAIT_L(0); PG8_BAR; if (cur.amask & 2) { PG8_MMA(1, 0, At, B0); PG8_MMA(1, 1, At, B1); } PG8_BAR; PG8_SCHED;
	s_setprio 1
	s_waitcnt lgkmcnt(0)
	v_mfma_f32_16x16x32_bf16 v[62:65], v[148:151], v[180:183], v[62:65]
	v_mfma_f32_16x16x32_bf16 v[58:61], v[156:159], v[180:183], v[58:61]
	v_mfma_f32_16x16x32_bf16 v[54:57], v[148:151], v[188:191], v[54:57]
	v_mfma_f32_16x16x32_bf16 v[46:49], v[156:159], v[188:191], v[46:49]
	v_mfma_f32_16x16x32_bf16 v[38:41], v[148:151], v[196:199], v[38:41]
	v_mfma_f32_16x16x32_bf16 v[30:33], v[156:159], v[196:199], v[30:33]
	v_mfma_f32_16x16x32_bf16 v[22:25], v[148:151], v[204:207], v[22:25]
	v_mfma_f32_16x16x32_bf16 v[14:17], v[156:159], v[204:207], v[14:17]
	v_mfma_f32_16x16x32_bf16 v[62:65], v[152:155], v[184:187], v[62:65]
	v_mfma_f32_16x16x32_bf16 v[58:61], v[160:163], v[184:187], v[58:61]
	v_mfma_f32_16x16x32_bf16 v[54:57], v[152:155], v[192:195], v[54:57]
	v_mfma_f32_16x16x32_bf16 v[46:49], v[160:163], v[192:195], v[46:49]
	v_mfma_f32_16x16x32_bf16 v[38:41], v[152:155], v[200:203], v[38:41]
	v_mfma_f32_16x16x32_bf16 v[30:33], v[160:163], v[200:203], v[30:33]
	v_mfma_f32_16x16x32_bf16 v[22:25], v[152:155], v[208:211], v[22:25]
	v_mfma_f32_16x16x32_bf16 v[14:17], v[160:163], v[208:211], v[14:17]
	s_setprio 0
	s_setprio 1
	v_mfma_f32_16x16x32_bf16 v[50:53], v[164:167], v[180:183], v[50:53]
	v_mfma_f32_16x16x32_bf16 v[42:45], v[172:175], v[180:183], v[42:45]
	v_mfma_f32_16x16x32_bf16 v[34:37], v[164:167], v[188:191], v[34:37]
	v_mfma_f32_16x16x32_bf16 v[26:29], v[172:175], v[188:191], v[26:29]
	v_mfma_f32_16x16x32_bf16 v[18:21], v[164:167], v[196:199], v[18:21]
	v_mfma_f32_16x16x32_bf16 v[10:13], v[172:175], v[196:199], v[10:13]
	v_mfma_f32_16x16x32_bf16 v[6:9], v[164:167], v[204:207], v[6:9]
	v_mfma_f32_16x16x32_bf16 v[2:5], v[172:175], v[204:207], v[2:5]
	v_mfma_f32_16x16x32_bf16 v[50:53], v[168:171], v[184:187], v[50:53]
	v_mfma_f32_16x16x32_bf16 v[42:45], v[176:179], v[184:187], v[42:45]
	v_mfma_f32_16x16x32_bf16 v[34:37], v[168:171], v[192:195], v[34:37]
	v_mfma_f32_16x16x32_bf16 v[26:29], v[176:179], v[192:195], v[26:29]
	v_mfma_f32_16x16x32_bf16 v[18:21], v[168:171], v[200:203], v[18:21]
	v_mfma_f32_16x16x32_bf16 v[10:13], v[176:179], v[200:203], v[10:13]
	v_mfma_f32_16x16x32_bf16 v[6:9], v[168:171], v[208:211], v[6:9]
	v_mfma_f32_16x16x32_bf16 v[2:5], v[176:179], v[208:211], v[2:5]
	s_setprio 0
	s_barrier
	s_add_i32 s23, 0, 0x18000
	s_add_i32 s26, 0, 0x1c000
	v_add_u32_e32 v160, s23, v146
	v_add_u32_e32 v176, s26, v146
	ds_read_b128 v[148:151], v160
	ds_read_b128 v[152:155], v160 offset:1024
	ds_read_b128 v[156:159], v160 offset:2048
	ds_read_b128 v[160:163], v160 offset:3072
	ds_read_b128 v[164:167], v176
	ds_read_b128 v[168:171], v176 offset:1024
	ds_read_b128 v[172:175], v176 offset:2048
	ds_read_b128 v[176:179], v176 offset:3072
	s_add_u32 s24, s60, 0x80000
	s_addc_u32 s25, s61, 0
	s_mov_b32 m0, s12
	v_lshl_add_u64 v[228:229], s[24:25], 0, v[134:135]
	ds_read_b128 v[180:183], v147 offset:32768
	ds_read_b128 v[184:187], v147 offset:33792
	ds_read_b128 v[188:191], v147 offset:34816
	ds_read_b128 v[192:195], v147 offset:35840
	ds_read_b128 v[196:199], v147 offset:36864
	ds_read_b128 v[200:203], v147 offset:37888
	ds_read_b128 v[204:207], v147 offset:38912
	ds_read_b128 v[208:211], v147 offset:39936
	global_load_lds_dwordx4 v[228:229], off
	v_lshl_add_u64 v[228:229], s[24:25], 0, v[132:133]
	s_mov_b32 m0, s13
	s_nop 0
	global_load_lds_dwordx4 v[228:229], off
	s_waitcnt vmcnt(8)
	s_waitcnt lgkmcnt(0)
	s_barrier
	s_setprio 1
	s_waitcnt lgkmcnt(0)
	v_mfma_f32_16x16x32_bf16 v[126:129], v[148:151], v[180:183], v[126:129]
	v_mfma_f32_16x16x32_bf16 v[122:125], v[156:159], v[180:183], v[122:125]
	v_mfma_f32_16x16x32_bf16 v[114:117], v[148:151], v[188:191], v[114:117]
	v_mfma_f32_16x16x32_bf16 v[106:109], v[156:159], v[188:191], v[106:109]
	v_mfma_f32_16x16x32_bf16 v[102:105], v[148:151], v[196:199], v[102:105]
	v_mfma_f32_16x16x32_bf16 v[94:97], v[156:159], v[196:199], v[94:97]
	v_mfma_f32_16x16x32_bf16 v[86:89], v[148:151], v[204:207], v[86:89]
	v_mfma_f32_16x16x32_bf16 v[78:81], v[156:159], v[204:207], v[78:81]
	v_mfma_f32_16x16x32_bf16 v[126:129], v[152:155], v[184:187], v[126:129]
	v_mfma_f32_16x16x32_bf16 v[122:125], v[160:163], v[184:187], v[122:125]
	v_mfma_f32_16x16x32_bf16 v[114:117], v[152:155], v[192:195], v[114:117]
	v_mfma_f32_16x16x32_bf16 v[106:109], v[160:163], v[192:195], v[106:109]
	v_mfma_f32_16x16x32_bf16 v[102:105], v[152:155], v[200:203], v[102:105]
	v_mfma_f32_16x16x32_bf16 v[94:97], v[160:163], v[200:203], v[94:97]
	v_mfma_f32_16x16x32_bf16 v[86:89], v[152:155], v[208:211], v[86:89]
	v_mfma_f32_16x16x32_bf16 v[78:81], v[160:163], v[208:211], v[78:81]
	s_setprio 0
	s_setprio 1
	v_mfma_f32_16x16x32_bf16 v[118:121], v[164:167], v[180:183], v[118:121]
	v_mfma_f32_16x16x32_bf16 v[110:113], v[172:175], v[180:183], v[110:113]
	v_mfma_f32_16x16x32_bf16 v[98:101], v[164:167], v[188:191], v[98:101]
	v_mfma_f32_16x16x32_bf16 v[90:93], v[172:175], v[188:191], v[90:93]
	v_mfma_f32_16x16x32_bf16 v[82:85], v[164:167], v[196:199], v[82:85]
	v_mfma_f32_16x16x32_bf16 v[74:77], v[172:175], v[196:199], v[74:77]
	v_mfma_f32_16x16x32_bf16 v[70:73], v[164:167], v[204:207], v[70:73]
	v_mfma_f32_16x16x32_bf16 v[66:69], v[172:175], v[204:207], v[66:69]
	v_mfma_f32_16x16x32_bf16 v[118:121], v[168:171], v[184:187], v[118:121]
	v_mfma_f32_16x16x32_bf16 v[110:113], v[176:179], v[184:187], v[110:113]
	v_mfma_f32_16x16x32_bf16 v[98:101], v[168:171], v[192:195], v[98:101]
	v_mfma_f32_16x16x32_bf16 v[90:93], v[176:179], v[192:195], v[90:93]
	v_mfma_f32_16x16x32_bf16 v[82:85], v[168:171], v[200:203], v[82:85]
	v_mfma_f32_16x16x32_bf16 v[74:77], v[176:179], v[200:203], v[74:77]
	v_mfma_f32_16x16x32_bf16 v[70:73], v[168:171], v[208:211], v[70:73]
	v_mfma_f32_16x16x32_bf16 v[66:69], v[176:179], v[208:211], v[66:69]
	s_setprio 0
	s_barrier
; #define PG8_MMA(ai, bj, At, Bt) do { __builtin_amdgcn_s_setprio(1); _Pragma("unroll") for (int m = 0; m < 4; ++m) _Pragma("unroll") for (int n = 0; n < 2; ++n) _Pragma("unroll") for (int k = 0; k < 2; ++k) \
;         acc[ai][bj][m][n] = __builtin_amdgcn_mfma_f32_16x16x32_bf16(Bt[n][k], At[m][k], acc[ai][bj][m][n], 0, 0, 0); __builtin_amdgcn_s_setprio(0); } while (0)
; #define PG8_WAIT_V(n) asm volatile("s_waitcnt vmcnt(" #n ")" ::: "memory")
; #define PG8_WAIT_L(n) asm volatile("s_waitcnt lgkmcnt(" #n ")" ::: "memory")
; #define PG8_BAR __builtin_amdgcn_s_barrier()
; #define PG8_SCHED __builtin_amdgcn_sched_barrier(0)
;     ...
;             PG8_WAIT_V(8); PG8_WAIT_L(0); PG8_BAR; if (cur.amask & 2) { PG8_MMA(1, 0, At, B0); PG8_MMA(1, 1, At, B1); } PG8_BAR; PG8_SCHED;
;         }
;     ...
; #pragma unroll
;         for (int a = 0; a < 2; ++a)
; #pragma unroll
;             for (int b = 0; b < 2; ++b)
; #pragma unroll
;                 for (int m = 0; m < 4; ++m)
; #pragma unroll
;                     for (int n = 0; n < 2; ++n) acc[a][b][m][n] = (f32x4){0.f, 0.f, 0.f, 0.f};
;         cur = nxt; cA = nA; cB = nB; ++ui; nt = PG8_NT(cur);
	s_add_i32 s23, s23, s43
	v_lshl_add_u64 v[212:213], v[212:213], 0, s[92:93]
	s_mov_b32 m0, s23
	ds_read_b128 v[180:183], v147 offset:49152
	ds_read_b128 v[184:187], v147 offset:50176
	ds_read_b128 v[188:191], v147 offset:51200
	ds_read_b128 v[192:195], v147 offset:52224
	ds_read_b128 v[196:199], v147 offset:53248
	ds_read_b128 v[200:203], v147 offset:54272
	ds_read_b128 v[204:207], v147 offset:55296
	ds_read_b128 v[208:211], v147 offset:56320
	global_load_lds_dwordx4 v[212:213], off
	s_add_i32 m0, s23, 0x2000
	s_add_u32 s24, s58, 0x80080
	v_lshl_add_u64 v[212:213], v[214:215], 0, s[92:93]
	s_addc_u32 s25, s59, 0
	s_add_i32 s23, s26, s43
	global_load_lds_dwordx4 v[212:213], off
	v_lshl_add_u64 v[212:213], s[24:25], 0, v[0:1]
	s_mov_b32 m0, s23
	s_nop 0
	global_load_lds_dwordx4 v[212:213], off
	v_lshl_add_u64 v[212:213], s[24:25], 0, v[130:131]
	s_add_i32 m0, s23, 0x2000
	s_nop 0
	global_load_lds_dwordx4 v[212:213], off
	v_lshl_add_u64 v[212:213], v[224:225], 0, s[92:93]
	s_mov_b32 m0, s16
	s_nop 0
	global_load_lds_dwordx4 v[212:213], off
	v_lshl_add_u64 v[212:213], v[226:227], 0, s[92:93]
	s_mov_b32 m0, s17
	s_nop 0
	global_load_lds_dwordx4 v[212:213], off
	s_waitcnt vmcnt(8)
	s_waitcnt lgkmcnt(0)
	s_barrier
	s_setprio 1
	s_waitcnt lgkmcnt(0)
	v_mfma_f32_16x16x32_bf16 v[62:65], v[148:151], v[180:183], v[62:65]
	v_mfma_f32_16x16x32_bf16 v[58:61], v[156:159], v[180:183], v[58:61]
	v_mfma_f32_16x16x32_bf16 v[54:57], v[148:151], v[188:191], v[54:57]
	v_mfma_f32_16x16x32_bf16 v[46:49], v[156:159], v[188:191], v[46:49]
	v_mfma_f32_16x16x32_bf16 v[38:41], v[148:151], v[196:199], v[38:41]
	v_mfma_f32_16x16x32_bf16 v[30:33], v[156:159], v[196:199], v[30:33]
	v_mfma_f32_16x16x32_bf16 v[22:25], v[148:151], v[204:207], v[22:25]
	v_mfma_f32_16x16x32_bf16 v[14:17], v[156:159], v[204:207], v[14:17]
	v_mfma_f32_16x16x32_bf16 v[62:65], v[152:155], v[184:187], v[62:65]
	v_mfma_f32_16x16x32_bf16 v[58:61], v[160:163], v[184:187], v[58:61]
	v_mfma_f32_16x16x32_bf16 v[54:57], v[152:155], v[192:195], v[54:57]
	v_mfma_f32_16x16x32_bf16 v[46:49], v[160:163], v[192:195], v[46:49]
	v_mfma_f32_16x16x32_bf16 v[38:41], v[152:155], v[200:203], v[38:41]
	v_mfma_f32_16x16x32_bf16 v[30:33], v[160:163], v[200:203], v[30:33]
	v_mfma_f32_16x16x32_bf16 v[22:25], v[152:155], v[208:211], v[22:25]
	v_mfma_f32_16x16x32_bf16 v[14:17], v[160:163], v[208:211], v[14:17]
	s_setprio 0
	s_setprio 1
	v_mfma_f32_16x16x32_bf16 v[50:53], v[164:167], v[180:183], v[50:53]
	v_mfma_f32_16x16x32_bf16 v[42:45], v[172:175], v[180:183], v[42:45]
	v_mfma_f32_16x16x32_bf16 v[34:37], v[164:167], v[188:191], v[34:37]
	v_mfma_f32_16x16x32_bf16 v[26:29], v[172:175], v[188:191], v[26:29]
	v_mfma_f32_16x16x32_bf16 v[18:21], v[164:167], v[196:199], v[18:21]
	v_mfma_f32_16x16x32_bf16 v[10:13], v[172:175], v[196:199], v[10:13]
	v_mfma_f32_16x16x32_bf16 v[6:9], v[164:167], v[204:207], v[6:9]
	v_mfma_f32_16x16x32_bf16 v[2:5], v[172:175], v[204:207], v[2:5]
	v_mfma_f32_16x16x32_bf16 v[50:53], v[168:171], v[184:187], v[50:53]
	v_mfma_f32_16x16x32_bf16 v[42:45], v[176:179], v[184:187], v[42:45]
	v_mfma_f32_16x16x32_bf16 v[34:37], v[168:171], v[192:195], v[34:37]
	v_mfma_f32_16x16x32_bf16 v[26:29], v[176:179], v[192:195], v[26:29]
	v_mfma_f32_16x16x32_bf16 v[18:21], v[168:171], v[200:203], v[18:21]
	v_mfma_f32_16x16x32_bf16 v[10:13], v[176:179], v[200:203], v[10:13]
	v_mfma_f32_16x16x32_bf16 v[6:9], v[168:171], v[208:211], v[6:9]
	v_mfma_f32_16x16x32_bf16 v[2:5], v[176:179], v[208:211], v[2:5]
	s_setprio 0
	s_add_i32 s22, s22, 2
	s_add_u32 s56, s56, 0x100
	s_addc_u32 s57, s57, 0
	s_cmp_gt_u32 s22, 5
	s_barrier
	s_cbranch_scc0 .LBB0_1280
	s_add_u32 s56, s20, 0xffffff00
	s_addc_u32 s57, s21, -1
	s_andn2_b64 vcc, exec, s[50:51]
	s_cbranch_vccnz .LBB0_1283
	v_mov_b32_e32 v2, 0
	s_mov_b64 s[4:5], s[38:39]
	s_mov_b64 s[36:37], s[52:53]
	s_mov_b32 s18, s19
	v_mov_b32_e32 v3, v2
	v_mov_b32_e32 v4, v2
	v_mov_b32_e32 v5, v2
	v_mov_b32_e32 v6, v2
	v_mov_b32_e32 v7, v2
	v_mov_b32_e32 v8, v2
	v_mov_b32_e32 v9, v2
	v_mov_b32_e32 v10, v2
	v_mov_b32_e32 v11, v2
	v_mov_b32_e32 v12, v2
	v_mov_b32_e32 v13, v2
	v_mov_b32_e32 v18, v2
	v_mov_b32_e32 v19, v2
	v_mov_b32_e32 v20, v2
	v_mov_b32_e32 v21, v2
	v_mov_b32_e32 v26, v2
	v_mov_b32_e32 v27, v2
	v_mov_b32_e32 v28, v2
	v_mov_b32_e32 v29, v2
	v_mov_b32_e32 v34, v2
	v_mov_b32_e32 v35, v2
	v_mov_b32_e32 v36, v2
	v_mov_b32_e32 v37, v2
	v_mov_b32_e32 v42, v2
	v_mov_b32_e32 v43, v2
	v_mov_b32_e32 v44, v2
	v_mov_b32_e32 v45, v2
	v_mov_b32_e32 v50, v2
	v_mov_b32_e32 v51, v2
	v_mov_b32_e32 v52, v2
	v_mov_b32_e32 v53, v2
	v_mov_b32_e32 v14, v2
	v_mov_b32_e32 v15, v2
	v_mov_b32_e32 v16, v2
	v_mov_b32_e32 v17, v2
	v_mov_b32_e32 v22, v2
	v_mov_b32_e32 v23, v2
	v_mov_b32_e32 v24, v2
	v_mov_b32_e32 v25, v2
	v_mov_b32_e32 v30, v2
	v_mov_b32_e32 v31, v2
	v_mov_b32_e32 v32, v2
	v_mov_b32_e32 v33, v2
	v_mov_b32_e32 v38, v2
	v_mov_b32_e32 v39, v2
	v_mov_b32_e32 v40, v2
	v_mov_b32_e32 v41, v2
	v_mov_b32_e32 v46, v2
	v_mov_b32_e32 v47, v2
	v_mov_b32_e32 v48, v2
	v_mov_b32_e32 v49, v2
	v_mov_b32_e32 v54, v2
	v_mov_b32_e32 v55, v2
	v_mov_b32_e32 v56, v2
	v_mov_b32_e32 v57, v2
	v_mov_b32_e32 v58, v2
	v_mov_b32_e32 v59, v2
	v_mov_b32_e32 v60, v2
	v_mov_b32_e32 v61, v2
	v_mov_b32_e32 v62, v2
	v_mov_b32_e32 v63, v2
	v_mov_b32_e32 v64, v2
	v_mov_b32_e32 v65, v2
	v_mov_b32_e32 v66, v2
	v_mov_b32_e32 v67, v2
	v_mov_b32_e32 v68, v2
	v_mov_b32_e32 v69, v2
	v_mov_b32_e32 v70, v2
	v_mov_b32_e32 v71, v2
	v_mov_b32_e32 v72, v2
	v_mov_b32_e32 v73, v2
	v_mov_b32_e32 v74, v2
	v_mov_b32_e32 v75, v2
	v_mov_b32_e32 v76, v2
	v_mov_b32_e32 v77, v2
	v_mov_b32_e32 v82, v2
	v_mov_b32_e32 v83, v2
	v_mov_b32_e32 v84, v2
	v_mov_b32_e32 v85, v2
	v_mov_b32_e32 v90, v2
	v_mov_b32_e32 v91, v2
	v_mov_b32_e32 v92, v2
	v_mov_b32_e32 v93, v2
	v_mov_b32_e32 v98, v2
	v_mov_b32_e32 v99, v2
	v_mov_b32_e32 v100, v2
	v_mov_b32_e32 v101, v2
	v_mov_b32_e32 v110, v2
	v_mov_b32_e32 v111, v2
	v_mov_b32_e32 v112, v2
	v_mov_b32_e32 v113, v2
	v_mov_b32_e32 v118, v2
	v_mov_b32_e32 v119, v2
	v_mov_b32_e32 v120, v2
	v_mov_b32_e32 v121, v2
	v_mov_b32_e32 v78, v2
	v_mov_b32_e32 v79, v2
	v_mov_b32_e32 v80, v2
	v_mov_b32_e32 v81, v2
	v_mov_b32_e32 v86, v2
	v_mov_b32_e32 v87, v2
	v_mov_b32_e32 v88, v2
	v_mov_b32_e32 v89, v2
	v_mov_b32_e32 v94, v2
	v_mov_b32_e32 v95, v2
	v_mov_b32_e32 v96, v2
	v_mov_b32_e32 v97, v2
	v_mov_b32_e32 v102, v2
	v_mov_b32_e32 v103, v2
	v_mov_b32_e32 v104, v2
	v_mov_b32_e32 v105, v2
	v_mov_b32_e32 v106, v2
	v_mov_b32_e32 v107, v2
	v_mov_b32_e32 v108, v2
	v_mov_b32_e32 v109, v2
	v_mov_b32_e32 v114, v2
	v_mov_b32_e32 v115, v2
	v_mov_b32_e32 v116, v2
	v_mov_b32_e32 v117, v2
	v_mov_b32_e32 v122, v2
	v_mov_b32_e32 v123, v2
	v_mov_b32_e32 v124, v2
	v_mov_b32_e32 v125, v2
	v_mov_b32_e32 v126, v2
	v_mov_b32_e32 v127, v2
	v_mov_b32_e32 v128, v2
	v_mov_b32_e32 v129, v2
	s_branch .LBB0_1284

; #define PG8_STAGE(bufoff, gbase, voff) do { _Pragma("unroll") for (int _i = 0; _i < 2; ++_i) \
;         __builtin_amdgcn_global_load_lds((const unsigned*)((const char*)(gbase) + (voff)[_i]), (LAS unsigned*)(lds + (bufoff) + ldsw + _i * 8192), 16, 0, 0); } while (0)
; #define PG8_STAGE_A(bufoff, h, kp, nx) do { if constexpr (GATHER) { const unsigned _p = (nx) ? ng[h] : cg[h]; unsigned _v[2]; _v[0] = (_p & 0xffffu) * lda + CA2[0]; _v[1] = (_p >> 16) * lda + CA2[1]; PG8_STAGE(bufoff, kp, _v); } \
;         else { PG8_STAGE(bufoff, (kp) + (h) * hstepA, voffA); } } while (0)
; #define PG8_LDA(dst, b, h) do { _Pragma("unroll") for (int m = 0; m < 4; ++m) _Pragma("unroll") for (int k = 0; k < 2; ++k) dst[m][k] = *(const LAS bf16x8*)(lds + PG8_SA(b, h) + aoff + m * 2048 + k * 1024); } while (0)
; #define PG8_LDB(dst, b, h) do { _Pragma("unroll") for (int n = 0; n < 2; ++n) _Pragma("unroll") for (int k = 0; k < 2; ++k) dst[n][k] = *(const LAS bf16x8*)(lds + PG8_SB(b, h) + boff + n * 2048 + k * 1024); } while (0)
; #define PG8_MMA(ai, bj, At, Bt) do { __builtin_amdgcn_s_setprio(1); _Pragma("unroll") for (int m = 0; m < 4; ++m) _Pragma("unroll") for (int n = 0; n < 2; ++n) _Pragma("unroll") for (int k = 0; k < 2; ++k) \
;         acc[ai][bj][m][n] = __builtin_amdgcn_mfma_f32_16x16x32_bf16(Bt[n][k], At[m][k], acc[ai][bj][m][n], 0, 0, 0); __builtin_amdgcn_s_setprio(0); } while (0)
; #define PG8_WAIT_V(n) asm volatile("s_waitcnt vmcnt(" #n ")" ::: "memory")
;     ...
;         for (int t = 0; t < nt; t += 2) {
;             const bool last = (t == nt - 2);
;             const char* a1 = cA + (size_t)(t + 1) * kstep;
;             const char* a2 = last ? nA : cA + (size_t)(t + 2) * kstep; const char* b2 = last ? nB : cB + (size_t)(t + 2) * kstep;
;             const char* a3 = a2 + kstep; const char* b3 = b2 + kstep;
;             PG8_LDB(B0, 0, 0); PG8_LDB(B1, 0, 1); PG8_SCHED; PG8_LDA(At, 0, 0); PG8_STAGE_A(PG8_SA(1, 1), 1, a1, false);
;             PG8_WAIT_V(8); PG8_WAIT_L(0); PG8_BAR; if (cur.amask & 1) { PG8_MMA(0, 0, At, B0); PG8_MMA(0, 1, At, B1); } PG8_BAR; PG8_SCHED;
;             PG8_LDA(At, 0, 1); PG8_STAGE(PG8_SB(0, 0), b2, voffB); PG8_STAGE(PG8_SB(0, 1), b2 + hstepB, voffB); PG8_STAGE_A(PG8_SA(0, 0), 0, a2, last);
;             PG8_WAIT_V(8); PG8_WAIT_L(0); PG8_BAR; if (cur.amask & 2) { PG8_MMA(1, 0, At, B0); PG8_MMA(1, 1, At, B1); } PG8_BAR; PG8_SCHED;
.LBB0_1315:
	s_add_u32 s22, s48, 0xfff80080
	s_addc_u32 s23, s49, -1
	s_add_i32 s24, 0, 0x10000
	s_cmp_eq_u32 s21, 4
	s_cselect_b32 s53, s5, s23
	s_cselect_b32 s52, s4, s22
	v_add_u32_e32 v149, s24, v147
	s_cselect_b32 s51, s37, s20
	s_cselect_b32 s50, s36, s19
	s_add_i32 s25, 0, 0x14000
	ds_read_b128 v[142:145], v149
	ds_read_b128 v[150:153], v149 offset:1024
	ds_read_b128 v[154:157], v149 offset:2048
	ds_read_b128 v[158:161], v149 offset:3072
	v_add_u32_e32 v149, s25, v147
	ds_read_b128 v[162:165], v149
	ds_read_b128 v[166:169], v149 offset:1024
	ds_read_b128 v[170:173], v149 offset:2048
	ds_read_b128 v[174:177], v149 offset:3072
	v_lshl_add_u64 v[210:211], s[48:49], 0, v[138:139]
	s_add_i32 m0, s10, 0xc000
	ds_read_b128 v[178:181], v148
	ds_read_b128 v[182:185], v148 offset:1024
	ds_read_b128 v[186:189], v148 offset:2048
	ds_read_b128 v[190:193], v148 offset:3072
	ds_read_b128 v[194:197], v148 offset:4096
	ds_read_b128 v[198:201], v148 offset:5120
	ds_read_b128 v[202:205], v148 offset:6144
	ds_read_b128 v[206:209], v148 offset:7168
	global_load_lds_dwordx4 v[210:211], off
	v_lshl_add_u64 v[210:211], s[48:49], 0, v[140:141]
	s_add_i32 m0, s10, 0xe000
	s_nop 0
	global_load_lds_dwordx4 v[210:211], off
	s_waitcnt vmcnt(8)
	s_waitcnt lgkmcnt(0)
	s_barrier
	s_setprio 1
	s_waitcnt lgkmcnt(0)
	v_mfma_f32_16x16x32_bf16 v[126:129], v[142:145], v[178:181], v[126:129]
	v_mfma_f32_16x16x32_bf16 v[122:125], v[154:157], v[178:181], v[122:125]
	v_mfma_f32_16x16x32_bf16 v[118:121], v[142:145], v[186:189], v[118:121]
	v_mfma_f32_16x16x32_bf16 v[110:113], v[154:157], v[186:189], v[110:113]
	v_mfma_f32_16x16x32_bf16 v[102:105], v[142:145], v[194:197], v[102:105]
	v_mfma_f32_16x16x32_bf16 v[94:97], v[154:157], v[194:197], v[94:97]
	v_mfma_f32_16x16x32_bf16 v[86:89], v[142:145], v[202:205], v[86:89]
	v_mfma_f32_16x16x32_bf16 v[78:81], v[154:157], v[202:205], v[78:81]
	v_mfma_f32_16x16x32_bf16 v[126:129], v[150:153], v[182:185], v[126:129]
	v_mfma_f32_16x16x32_bf16 v[122:125], v[158:161], v[182:185], v[122:125]
	v_mfma_f32_16x16x32_bf16 v[118:121], v[150:153], v[190:193], v[118:121]
	v_mfma_f32_16x16x32_bf16 v[110:113], v[158:161], v[190:193], v[110:113]
	v_mfma_f32_16x16x32_bf16 v[102:105], v[150:153], v[198:201], v[102:105]
	v_mfma_f32_16x16x32_bf16 v[94:97], v[158:161], v[198:201], v[94:97]
	v_mfma_f32_16x16x32_bf16 v[86:89], v[150:153], v[206:209], v[86:89]
	v_mfma_f32_16x16x32_bf16 v[78:81], v[158:161], v[206:209], v[78:81]
	s_setprio 0
	s_setprio 1
	v_mfma_f32_16x16x32_bf16 v[114:117], v[162:165], v[178:181], v[114:117]
	v_mfma_f32_16x16x32_bf16 v[106:109], v[170:173], v[178:181], v[106:109]
	v_mfma_f32_16x16x32_bf16 v[98:101], v[162:165], v[186:189], v[98:101]
	v_mfma_f32_16x16x32_bf16 v[90:93], v[170:173], v[186:189], v[90:93]
	v_mfma_f32_16x16x32_bf16 v[82:85], v[162:165], v[194:197], v[82:85]
	v_mfma_f32_16x16x32_bf16 v[74:77], v[170:173], v[194:197], v[74:77]
	v_mfma_f32_16x16x32_bf16 v[70:73], v[162:165], v[202:205], v[70:73]
	v_mfma_f32_16x16x32_bf16 v[66:69], v[170:173], v[202:205], v[66:69]
	v_mfma_f32_16x16x32_bf16 v[114:117], v[166:169], v[182:185], v[114:117]
	v_mfma_f32_16x16x32_bf16 v[106:109], v[174:177], v[182:185], v[106:109]
	v_mfma_f32_16x16x32_bf16 v[98:101], v[166:169], v[190:193], v[98:101]
	v_mfma_f32_16x16x32_bf16 v[90:93], v[174:177], v[190:193], v[90:93]
	v_mfma_f32_16x16x32_bf16 v[82:85], v[166:169], v[198:201], v[82:85]
	v_mfma_f32_16x16x32_bf16 v[74:77], v[174:177], v[198:201], v[74:77]
	v_mfma_f32_16x16x32_bf16 v[70:73], v[166:169], v[206:209], v[70:73]
	v_mfma_f32_16x16x32_bf16 v[66:69], v[174:177], v[206:209], v[66:69]
	s_setprio 0
	s_barrier
	s_add_i32 s22, s24, s43
	v_lshl_add_u64 v[210:211], s[50:51], 0, v[0:1]
	s_mov_b32 m0, s22
	ds_read_b128 v[178:181], v148 offset:16384
	ds_read_b128 v[182:185], v148 offset:17408
	ds_read_b128 v[186:189], v148 offset:18432
	ds_read_b128 v[190:193], v148 offset:19456
	ds_read_b128 v[194:197], v148 offset:20480
	ds_read_b128 v[198:201], v148 offset:21504
	ds_read_b128 v[202:205], v148 offset:22528
	ds_read_b128 v[206:209], v148 offset:23552
	global_load_lds_dwordx4 v[210:211], off
	s_add_i32 m0, s22, 0x2000
	s_add_u32 s22, s50, 0x80000
	v_lshl_add_u64 v[212:213], s[50:51], 0, v[130:131]
	s_addc_u32 s23, s51, 0
	s_add_i32 s24, s25, s43
	global_load_lds_dwordx4 v[212:213], off
	v_lshl_add_u64 v[214:215], s[22:23], 0, v[0:1]
	s_mov_b32 m0, s24
	v_lshl_add_u64 v[224:225], s[52:53], 0, v[132:133]
	global_load_lds_dwordx4 v[214:215], off
	v_lshl_add_u64 v[214:215], s[22:23], 0, v[130:131]
	s_add_i32 m0, s24, 0x2000
	s_nop 0
	global_load_lds_dwordx4 v[214:215], off
	v_lshl_add_u64 v[214:215], s[52:53], 0, v[134:135]
	s_mov_b32 m0, s10
	s_nop 0
	global_load_lds_dwordx4 v[214:215], off
	s_mov_b32 m0, s11
	s_nop 0
	global_load_lds_dwordx4 v[224:225], off
	s_waitcnt vmcnt(8)
	s_waitcnt lgkmcnt(0)
	s_barrier
; #define PG8_STAGE(bufoff, gbase, voff) do { _Pragma("unroll") for (int _i = 0; _i < 2; ++_i) \
;         __builtin_amdgcn_global_load_lds((const unsigned*)((const char*)(gbase) + (voff)[_i]), (LAS unsigned*)(lds + (bufoff) + ldsw + _i * 8192), 16, 0, 0); } while (0)
; #define PG8_STAGE_A(bufoff, h, kp, nx) do { if constexpr (GATHER) { const unsigned _p = (nx) ? ng[h] : cg[h]; unsigned _v[2]; _v[0] = (_p & 0xffffu) * lda + CA2[0]; _v[1] = (_p >> 16) * lda + CA2[1]; PG8_STAGE(bufoff, kp, _v); } \
;         else { PG8_STAGE(bufoff, (kp) + (h) * hstepA, voffA); } } while (0)
; #define PG8_LDA(dst, b, h) do { _Pragma("unroll") for (int m = 0; m < 4; ++m) _Pragma("unroll") for (int k = 0; k < 2; ++k) dst[m][k] = *(const LAS bf16x8*)(lds + PG8_SA(b, h) + aoff + m * 2048 + k * 1024); } while (0)
; #define PG8_LDB(dst, b, h) do { _Pragma("unroll") for (int n = 0; n < 2; ++n) _Pragma("unroll") for (int k = 0; k < 2; ++k) dst[n][k] = *(const LAS bf16x8*)(lds + PG8_SB(b, h) + boff + n * 2048 + k * 1024); } while (0)
; #define PG8_MMA(ai, bj, At, Bt) do { __builtin_amdgcn_s_setprio(1); _Pragma("unroll") for (int m = 0; m < 4; ++m) _Pragma("unroll") for (int n = 0; n < 2; ++n) _Pragma("unroll") for (int k = 0; k < 2; ++k) \
;         acc[ai][bj][m][n] = __builtin_amdgcn_mfma_f32_16x16x32_bf16(Bt[n][k], At[m][k], acc[ai][bj][m][n], 0, 0, 0); __builtin_amdgcn_s_setprio(0); } while (0)
; #define PG8_WAIT_V(n) asm volatile("s_waitcnt vmcnt(" #n ")" ::: "memory")
; #define PG8_WAIT_L(n) asm volatile("s_waitcnt lgkmcnt(" #n ")" ::: "memory")
; #define PG8_BAR __builtin_amdgcn_s_barrier()
; #define PG8_SCHED __builtin_amdgcn_sched_barrier(0)
;     ...
;             PG8_WAIT_V(8); PG8_WAIT_L(0); PG8_BAR; if (cur.amask & 2) { PG8_MMA(1, 0, At, B0); PG8_MMA(1, 1, At, B1); } PG8_BAR; PG8_SCHED;
;             PG8_LDB(B0, 1, 0); PG8_LDB(B1, 1, 1); PG8_SCHED; PG8_LDA(At, 1, 0); PG8_STAGE_A(PG8_SA(0, 1), 1, a2, last);
;             PG8_WAIT_V(8); PG8_WAIT_L(0); PG8_BAR; if (cur.amask & 1) { PG8_MMA(0, 0, At, B0); PG8_MMA(0, 1, At, B1); } PG8_BAR; PG8_SCHED;
;             PG8_LDA(At, 1, 1); PG8_STAGE(PG8_SB(1, 0), b3, voffB); PG8_STAGE(PG8_SB(1, 1), b3 + hstepB, voffB); PG8_STAGE_A(PG8_SA(1, 0), 0, a3, last);
;             PG8_WAIT_V(8); PG8_WAIT_L(0); PG8_BAR; if (cur.amask & 2) { PG8_MMA(1, 0, At, B0); PG8_MMA(1, 1, At, B1); } PG8_BAR; PG8_SCHED;
	s_setprio 1
	s_waitcnt lgkmcnt(0)
	v_mfma_f32_16x16x32_bf16 v[62:65], v[142:145], v[178:181], v[62:65]
	v_mfma_f32_16x16x32_bf16 v[58:61], v[154:157], v[178:181], v[58:61]
	v_mfma_f32_16x16x32_bf16 v[54:57], v[142:145], v[186:189], v[54:57]
	v_mfma_f32_16x16x32_bf16 v[46:49], v[154:157], v[186:189], v[46:49]
	v_mfma_f32_16x16x32_bf16 v[38:41], v[142:145], v[194:197], v[38:41]
	v_mfma_f32_16x16x32_bf16 v[30:33], v[154:157], v[194:197], v[30:33]
	v_mfma_f32_16x16x32_bf16 v[22:25], v[142:145], v[202:205], v[22:25]
	v_mfma_f32_16x16x32_bf16 v[14:17], v[154:157], v[202:205], v[14:17]
	v_mfma_f32_16x16x32_bf16 v[62:65], v[150:153], v[182:185], v[62:65]
	v_mfma_f32_16x16x32_bf16 v[58:61], v[158:161], v[182:185], v[58:61]
	v_mfma_f32_16x16x32_bf16 v[54:57], v[150:153], v[190:193], v[54:57]
	v_mfma_f32_16x16x32_bf16 v[46:49], v[158:161], v[190:193], v[46:49]
	v_mfma_f32_16x16x32_bf16 v[38:41], v[150:153], v[198:201], v[38:41]
	v_mfma_f32_16x16x32_bf16 v[30:33], v[158:161], v[198:201], v[30:33]
	v_mfma_f32_16x16x32_bf16 v[22:25], v[150:153], v[206:209], v[22:25]
	v_mfma_f32_16x16x32_bf16 v[14:17], v[158:161], v[206:209], v[14:17]
	s_setprio 0
	s_setprio 1
	v_mfma_f32_16x16x32_bf16 v[50:53], v[162:165], v[178:181], v[50:53]
	v_mfma_f32_16x16x32_bf16 v[42:45], v[170:173], v[178:181], v[42:45]
	v_mfma_f32_16x16x32_bf16 v[34:37], v[162:165], v[186:189], v[34:37]
	v_mfma_f32_16x16x32_bf16 v[26:29], v[170:173], v[186:189], v[26:29]
	v_mfma_f32_16x16x32_bf16 v[18:21], v[162:165], v[194:197], v[18:21]
	v_mfma_f32_16x16x32_bf16 v[10:13], v[170:173], v[194:197], v[10:13]
	v_mfma_f32_16x16x32_bf16 v[6:9], v[162:165], v[202:205], v[6:9]
	v_mfma_f32_16x16x32_bf16 v[2:5], v[170:173], v[202:205], v[2:5]
	v_mfma_f32_16x16x32_bf16 v[50:53], v[166:169], v[182:185], v[50:53]
	v_mfma_f32_16x16x32_bf16 v[42:45], v[174:177], v[182:185], v[42:45]
	v_mfma_f32_16x16x32_bf16 v[34:37], v[166:169], v[190:193], v[34:37]
	v_mfma_f32_16x16x32_bf16 v[26:29], v[174:177], v[190:193], v[26:29]
	v_mfma_f32_16x16x32_bf16 v[18:21], v[166:169], v[198:201], v[18:21]
	v_mfma_f32_16x16x32_bf16 v[10:13], v[174:177], v[198:201], v[10:13]
	v_mfma_f32_16x16x32_bf16 v[6:9], v[166:169], v[206:209], v[6:9]
	v_mfma_f32_16x16x32_bf16 v[2:5], v[174:177], v[206:209], v[2:5]
	s_setprio 0
	s_barrier
	s_add_i32 s24, 0, 0x18000
	v_add_u32_e32 v149, s24, v147
	s_add_i32 s25, 0, 0x1c000
	ds_read_b128 v[142:145], v149
	ds_read_b128 v[150:153], v149 offset:1024
	ds_read_b128 v[154:157], v149 offset:2048
	ds_read_b128 v[158:161], v149 offset:3072
	v_add_u32_e32 v149, s25, v147
	ds_read_b128 v[162:165], v149
	ds_read_b128 v[166:169], v149 offset:1024
	ds_read_b128 v[170:173], v149 offset:2048
	ds_read_b128 v[174:177], v149 offset:3072
	s_add_u32 s22, s52, 0x80000
	s_addc_u32 s23, s53, 0
	s_mov_b32 m0, s12
	v_lshl_add_u64 v[226:227], s[22:23], 0, v[134:135]
	ds_read_b128 v[178:181], v148 offset:32768
	ds_read_b128 v[182:185], v148 offset:33792
	ds_read_b128 v[186:189], v148 offset:34816
	ds_read_b128 v[190:193], v148 offset:35840
	ds_read_b128 v[194:197], v148 offset:36864
	ds_read_b128 v[198:201], v148 offset:37888
	ds_read_b128 v[202:205], v148 offset:38912
	ds_read_b128 v[206:209], v148 offset:39936
	global_load_lds_dwordx4 v[226:227], off
	v_lshl_add_u64 v[226:227], s[22:23], 0, v[132:133]
	s_mov_b32 m0, s13
	s_nop 0
	global_load_lds_dwordx4 v[226:227], off
	s_waitcnt vmcnt(8)
	s_waitcnt lgkmcnt(0)
	s_barrier
	s_setprio 1
	s_waitcnt lgkmcnt(0)
	v_mfma_f32_16x16x32_bf16 v[126:129], v[142:145], v[178:181], v[126:129]
	v_mfma_f32_16x16x32_bf16 v[122:125], v[154:157], v[178:181], v[122:125]
	v_mfma_f32_16x16x32_bf16 v[118:121], v[142:145], v[186:189], v[118:121]
	v_mfma_f32_16x16x32_bf16 v[110:113], v[154:157], v[186:189], v[110:113]
	v_mfma_f32_16x16x32_bf16 v[102:105], v[142:145], v[194:197], v[102:105]
	v_mfma_f32_16x16x32_bf16 v[94:97], v[154:157], v[194:197], v[94:97]
	v_mfma_f32_16x16x32_bf16 v[86:89], v[142:145], v[202:205], v[86:89]
	v_mfma_f32_16x16x32_bf16 v[78:81], v[154:157], v[202:205], v[78:81]
	v_mfma_f32_16x16x32_bf16 v[126:129], v[150:153], v[182:185], v[126:129]
	v_mfma_f32_16x16x32_bf16 v[122:125], v[158:161], v[182:185], v[122:125]
	v_mfma_f32_16x16x32_bf16 v[118:121], v[150:153], v[190:193], v[118:121]
	v_mfma_f32_16x16x32_bf16 v[110:113], v[158:161], v[190:193], v[110:113]
	v_mfma_f32_16x16x32_bf16 v[102:105], v[150:153], v[198:201], v[102:105]
	v_mfma_f32_16x16x32_bf16 v[94:97], v[158:161], v[198:201], v[94:97]
	v_mfma_f32_16x16x32_bf16 v[86:89], v[150:153], v[206:209], v[86:89]
	v_mfma_f32_16x16x32_bf16 v[78:81], v[158:161], v[206:209], v[78:81]
	s_setprio 0
	s_setprio 1
	v_mfma_f32_16x16x32_bf16 v[114:117], v[162:165], v[178:181], v[114:117]
	v_mfma_f32_16x16x32_bf16 v[106:109], v[170:173], v[178:181], v[106:109]
	v_mfma_f32_16x16x32_bf16 v[98:101], v[162:165], v[186:189], v[98:101]
	v_mfma_f32_16x16x32_bf16 v[90:93], v[170:173], v[186:189], v[90:93]
	v_mfma_f32_16x16x32_bf16 v[82:85], v[162:165], v[194:197], v[82:85]
	v_mfma_f32_16x16x32_bf16 v[74:77], v[170:173], v[194:197], v[74:77]
	v_mfma_f32_16x16x32_bf16 v[70:73], v[162:165], v[202:205], v[70:73]
	v_mfma_f32_16x16x32_bf16 v[66:69], v[170:173], v[202:205], v[66:69]
	v_mfma_f32_16x16x32_bf16 v[114:117], v[166:169], v[182:185], v[114:117]
	v_mfma_f32_16x16x32_bf16 v[106:109], v[174:177], v[182:185], v[106:109]
	v_mfma_f32_16x16x32_bf16 v[98:101], v[166:169], v[190:193], v[98:101]
	v_mfma_f32_16x16x32_bf16 v[90:93], v[174:177], v[190:193], v[90:93]
	v_mfma_f32_16x16x32_bf16 v[82:85], v[166:169], v[198:201], v[82:85]
	v_mfma_f32_16x16x32_bf16 v[74:77], v[174:177], v[198:201], v[74:77]
	v_mfma_f32_16x16x32_bf16 v[70:73], v[166:169], v[206:209], v[70:73]
	v_mfma_f32_16x16x32_bf16 v[66:69], v[174:177], v[206:209], v[66:69]
	s_setprio 0
	s_barrier
; #define PG8_MMA(ai, bj, At, Bt) do { __builtin_amdgcn_s_setprio(1); _Pragma("unroll") for (int m = 0; m < 4; ++m) _Pragma("unroll") for (int n = 0; n < 2; ++n) _Pragma("unroll") for (int k = 0; k < 2; ++k) \
;         acc[ai][bj][m][n] = __builtin_amdgcn_mfma_f32_16x16x32_bf16(Bt[n][k], At[m][k], acc[ai][bj][m][n], 0, 0, 0); __builtin_amdgcn_s_setprio(0); } while (0)
; #define PG8_WAIT_V(n) asm volatile("s_waitcnt vmcnt(" #n ")" ::: "memory")
; #define PG8_WAIT_L(n) asm volatile("s_waitcnt lgkmcnt(" #n ")" ::: "memory")
; #define PG8_BAR __builtin_amdgcn_s_barrier()
; #define PG8_SCHED __builtin_amdgcn_sched_barrier(0)
;     ...
;             PG8_WAIT_V(8); PG8_WAIT_L(0); PG8_BAR; if (cur.amask & 2) { PG8_MMA(1, 0, At, B0); PG8_MMA(1, 1, At, B1); } PG8_BAR; PG8_SCHED;
;         }
;         if constexpr (ALIGN_EPI) { if (wr == 0) PG8_BAR; }
	s_add_i32 s22, s24, s43
	v_lshl_add_u64 v[210:211], v[210:211], 0, s[92:93]
	s_mov_b32 m0, s22
	ds_read_b128 v[178:181], v148 offset:49152
	ds_read_b128 v[182:185], v148 offset:50176
	ds_read_b128 v[186:189], v148 offset:51200
	ds_read_b128 v[190:193], v148 offset:52224
	ds_read_b128 v[194:197], v148 offset:53248
	ds_read_b128 v[198:201], v148 offset:54272
	ds_read_b128 v[202:205], v148 offset:55296
	ds_read_b128 v[206:209], v148 offset:56320
	global_load_lds_dwordx4 v[210:211], off
	s_add_i32 m0, s22, 0x2000
	s_add_u32 s22, s50, 0x80080
	v_lshl_add_u64 v[210:211], v[212:213], 0, s[92:93]
	s_addc_u32 s23, s51, 0
	s_add_i32 s24, s25, s43
	global_load_lds_dwordx4 v[210:211], off
	v_lshl_add_u64 v[210:211], s[22:23], 0, v[0:1]
	s_mov_b32 m0, s24
	s_nop 0
	global_load_lds_dwordx4 v[210:211], off
	v_lshl_add_u64 v[210:211], s[22:23], 0, v[130:131]
	s_add_i32 m0, s24, 0x2000
	s_nop 0
	global_load_lds_dwordx4 v[210:211], off
	v_lshl_add_u64 v[210:211], v[214:215], 0, s[92:93]
	s_mov_b32 m0, s16
	s_nop 0
	global_load_lds_dwordx4 v[210:211], off
	v_lshl_add_u64 v[210:211], v[224:225], 0, s[92:93]
	s_mov_b32 m0, s17
	s_nop 0
	global_load_lds_dwordx4 v[210:211], off
	s_waitcnt vmcnt(8)
	s_waitcnt lgkmcnt(0)
	s_barrier
	s_setprio 1
	s_waitcnt lgkmcnt(0)
	v_mfma_f32_16x16x32_bf16 v[62:65], v[142:145], v[178:181], v[62:65]
	v_mfma_f32_16x16x32_bf16 v[58:61], v[154:157], v[178:181], v[58:61]
	v_mfma_f32_16x16x32_bf16 v[54:57], v[142:145], v[186:189], v[54:57]
	v_mfma_f32_16x16x32_bf16 v[46:49], v[154:157], v[186:189], v[46:49]
	v_mfma_f32_16x16x32_bf16 v[38:41], v[142:145], v[194:197], v[38:41]
	v_mfma_f32_16x16x32_bf16 v[30:33], v[154:157], v[194:197], v[30:33]
	v_mfma_f32_16x16x32_bf16 v[22:25], v[142:145], v[202:205], v[22:25]
	v_mfma_f32_16x16x32_bf16 v[14:17], v[154:157], v[202:205], v[14:17]
	v_mfma_f32_16x16x32_bf16 v[62:65], v[150:153], v[182:185], v[62:65]
	v_mfma_f32_16x16x32_bf16 v[58:61], v[158:161], v[182:185], v[58:61]
	v_mfma_f32_16x16x32_bf16 v[54:57], v[150:153], v[190:193], v[54:57]
	v_mfma_f32_16x16x32_bf16 v[46:49], v[158:161], v[190:193], v[46:49]
	v_mfma_f32_16x16x32_bf16 v[38:41], v[150:153], v[198:201], v[38:41]
	v_mfma_f32_16x16x32_bf16 v[30:33], v[158:161], v[198:201], v[30:33]
	v_mfma_f32_16x16x32_bf16 v[22:25], v[150:153], v[206:209], v[22:25]
	v_mfma_f32_16x16x32_bf16 v[14:17], v[158:161], v[206:209], v[14:17]
	s_setprio 0
	s_setprio 1
	v_mfma_f32_16x16x32_bf16 v[50:53], v[162:165], v[178:181], v[50:53]
	v_mfma_f32_16x16x32_bf16 v[42:45], v[170:173], v[178:181], v[42:45]
	v_mfma_f32_16x16x32_bf16 v[34:37], v[162:165], v[186:189], v[34:37]
	v_mfma_f32_16x16x32_bf16 v[26:29], v[170:173], v[186:189], v[26:29]
	v_mfma_f32_16x16x32_bf16 v[18:21], v[162:165], v[194:197], v[18:21]
	v_mfma_f32_16x16x32_bf16 v[10:13], v[170:173], v[194:197], v[10:13]
	v_mfma_f32_16x16x32_bf16 v[6:9], v[162:165], v[202:205], v[6:9]
	v_mfma_f32_16x16x32_bf16 v[2:5], v[170:173], v[202:205], v[2:5]
	v_mfma_f32_16x16x32_bf16 v[50:53], v[166:169], v[182:185], v[50:53]
	v_mfma_f32_16x16x32_bf16 v[42:45], v[174:177], v[182:185], v[42:45]
	v_mfma_f32_16x16x32_bf16 v[34:37], v[166:169], v[190:193], v[34:37]
	v_mfma_f32_16x16x32_bf16 v[26:29], v[174:177], v[190:193], v[26:29]
	v_mfma_f32_16x16x32_bf16 v[18:21], v[166:169], v[198:201], v[18:21]
	v_mfma_f32_16x16x32_bf16 v[10:13], v[174:177], v[198:201], v[10:13]
	v_mfma_f32_16x16x32_bf16 v[6:9], v[166:169], v[206:209], v[6:9]
	v_mfma_f32_16x16x32_bf16 v[2:5], v[174:177], v[206:209], v[2:5]
	s_setprio 0
	s_add_i32 s21, s21, 2
	s_add_u32 s48, s48, 0x100
	s_addc_u32 s49, s49, 0
	s_add_u32 s19, s19, 0x100
	s_addc_u32 s20, s20, 0
	s_cmp_gt_u32 s21, 5
	s_barrier
	s_cbranch_scc0 .LBB0_1315
	v_readlane_b32 s20, v252, 14
	v_readlane_b32 s21, v252, 15
	s_and_b64 vcc, exec, s[20:21]
	s_cbranch_vccz .LBB0_1318
	s_barrier

; #define PG8_STAGE(bufoff, gbase, voff) do { _Pragma("unroll") for (int _i = 0; _i < 2; ++_i) \
;         __builtin_amdgcn_global_load_lds((const unsigned*)((const char*)(gbase) + (voff)[_i]), (LAS unsigned*)(lds + (bufoff) + ldsw + _i * 8192), 16, 0, 0); } while (0)
; #define PG8_STAGE_A(bufoff, h, kp, nx) do { if constexpr (GATHER) { const unsigned _p = (nx) ? ng[h] : cg[h]; unsigned _v[2]; _v[0] = (_p & 0xffffu) * lda + CA2[0]; _v[1] = (_p >> 16) * lda + CA2[1]; PG8_STAGE(bufoff, kp, _v); } \
;         else { PG8_STAGE(bufoff, (kp) + (h) * hstepA, voffA); } } while (0)
; #define PG8_LDA(dst, b, h) do { _Pragma("unroll") for (int m = 0; m < 4; ++m) _Pragma("unroll") for (int k = 0; k < 2; ++k) dst[m][k] = *(const LAS bf16x8*)(lds + PG8_SA(b, h) + aoff + m * 2048 + k * 1024); } while (0)
; #define PG8_LDB(dst, b, h) do { _Pragma("unroll") for (int n = 0; n < 2; ++n) _Pragma("unroll") for (int k = 0; k < 2; ++k) dst[n][k] = *(const LAS bf16x8*)(lds + PG8_SB(b, h) + boff + n * 2048 + k * 1024); } while (0)
; #define PG8_MMA(ai, bj, At, Bt) do { __builtin_amdgcn_s_setprio(1); _Pragma("unroll") for (int m = 0; m < 4; ++m) _Pragma("unroll") for (int n = 0; n < 2; ++n) _Pragma("unroll") for (int k = 0; k < 2; ++k) \
;         acc[ai][bj][m][n] = __builtin_amdgcn_mfma_f32_16x16x32_bf16(Bt[n][k], At[m][k], acc[ai][bj][m][n], 0, 0, 0); __builtin_amdgcn_s_setprio(0); } while (0)
; #define PG8_WAIT_V(n) asm volatile("s_waitcnt vmcnt(" #n ")" ::: "memory")
;     ...
;         for (int t = 0; t < nt; t += 2) {
;             const bool last = (t == nt - 2);
;             const char* a1 = cA + (size_t)(t + 1) * kstep;
;             const char* a2 = last ? nA : cA + (size_t)(t + 2) * kstep; const char* b2 = last ? nB : cB + (size_t)(t + 2) * kstep;
;             const char* a3 = a2 + kstep; const char* b3 = b2 + kstep;
;             PG8_LDB(B0, 0, 0); PG8_LDB(B1, 0, 1); PG8_SCHED; PG8_LDA(At, 0, 0); PG8_STAGE_A(PG8_SA(1, 1), 1, a1, false);
;             PG8_WAIT_V(8); PG8_WAIT_L(0); PG8_BAR; if (cur.amask & 1) { PG8_MMA(0, 0, At, B0); PG8_MMA(0, 1, At, B1); } PG8_BAR; PG8_SCHED;
;             PG8_LDA(At, 0, 1); PG8_STAGE(PG8_SB(0, 0), b2, voffB); PG8_STAGE(PG8_SB(0, 1), b2 + hstepB, voffB); PG8_STAGE_A(PG8_SA(0, 0), 0, a2, last);
;             PG8_WAIT_V(8); PG8_WAIT_L(0); PG8_BAR; if (cur.amask & 2) { PG8_MMA(1, 0, At, B0); PG8_MMA(1, 1, At, B1); } PG8_BAR; PG8_SCHED;
.LBB0_1392:
	s_add_u32 s20, s48, 0xfffc0080
	s_addc_u32 s21, s49, -1
	s_add_i32 s22, 0, 0x10000
	s_cmp_eq_u32 s19, 12
	s_cselect_b32 s53, s39, s21
	s_cselect_b32 s52, s38, s20
	v_add_u32_e32 v148, s22, v151
	s_cselect_b32 s51, s41, s18
	s_cselect_b32 s50, s40, s17
	s_add_i32 s23, 0, 0x14000
	ds_read_b128 v[144:147], v148
	ds_read_b128 v[154:157], v148 offset:1024
	ds_read_b128 v[158:161], v148 offset:2048
	ds_read_b128 v[162:165], v148 offset:3072
	v_add_u32_e32 v148, s23, v151
	ds_read_b128 v[166:169], v148
	ds_read_b128 v[170:173], v148 offset:1024
	ds_read_b128 v[174:177], v148 offset:2048
	ds_read_b128 v[178:181], v148 offset:3072
	v_lshl_add_u64 v[148:149], s[48:49], 0, v[140:141]
	s_add_i32 m0, s10, 0xc000
	ds_read_b128 v[182:185], v152
	ds_read_b128 v[186:189], v152 offset:1024
	ds_read_b128 v[190:193], v152 offset:2048
	ds_read_b128 v[194:197], v152 offset:3072
	ds_read_b128 v[198:201], v152 offset:4096
	ds_read_b128 v[202:205], v152 offset:5120
	ds_read_b128 v[206:209], v152 offset:6144
	ds_read_b128 v[210:213], v152 offset:7168
	global_load_lds_dwordx4 v[148:149], off
	v_lshl_add_u64 v[148:149], s[48:49], 0, v[142:143]
	s_add_i32 m0, s10, 0xe000
	s_nop 0
	global_load_lds_dwordx4 v[148:149], off
	s_waitcnt vmcnt(8)
	s_waitcnt lgkmcnt(0)
	s_barrier
	s_setprio 1
	s_waitcnt lgkmcnt(0)
	v_mfma_f32_16x16x32_bf16 v[126:129], v[144:147], v[182:185], v[126:129]
	v_mfma_f32_16x16x32_bf16 v[122:125], v[158:161], v[182:185], v[122:125]
	v_mfma_f32_16x16x32_bf16 v[110:113], v[144:147], v[190:193], v[110:113]
	v_mfma_f32_16x16x32_bf16 v[106:109], v[158:161], v[190:193], v[106:109]
	v_mfma_f32_16x16x32_bf16 v[94:97], v[144:147], v[198:201], v[94:97]
	v_mfma_f32_16x16x32_bf16 v[90:93], v[158:161], v[198:201], v[90:93]
	v_mfma_f32_16x16x32_bf16 v[78:81], v[144:147], v[206:209], v[78:81]
	v_mfma_f32_16x16x32_bf16 v[74:77], v[158:161], v[206:209], v[74:77]
	v_mfma_f32_16x16x32_bf16 v[126:129], v[154:157], v[186:189], v[126:129]
	v_mfma_f32_16x16x32_bf16 v[122:125], v[162:165], v[186:189], v[122:125]
	v_mfma_f32_16x16x32_bf16 v[110:113], v[154:157], v[194:197], v[110:113]
	v_mfma_f32_16x16x32_bf16 v[106:109], v[162:165], v[194:197], v[106:109]
	v_mfma_f32_16x16x32_bf16 v[94:97], v[154:157], v[202:205], v[94:97]
	v_mfma_f32_16x16x32_bf16 v[90:93], v[162:165], v[202:205], v[90:93]
	v_mfma_f32_16x16x32_bf16 v[78:81], v[154:157], v[210:213], v[78:81]
	v_mfma_f32_16x16x32_bf16 v[74:77], v[162:165], v[210:213], v[74:77]
	s_setprio 0
	s_setprio 1
	v_mfma_f32_16x16x32_bf16 v[118:121], v[166:169], v[182:185], v[118:121]
	v_mfma_f32_16x16x32_bf16 v[114:117], v[174:177], v[182:185], v[114:117]
	v_mfma_f32_16x16x32_bf16 v[102:105], v[166:169], v[190:193], v[102:105]
	v_mfma_f32_16x16x32_bf16 v[98:101], v[174:177], v[190:193], v[98:101]
	v_mfma_f32_16x16x32_bf16 v[86:89], v[166:169], v[198:201], v[86:89]
	v_mfma_f32_16x16x32_bf16 v[82:85], v[174:177], v[198:201], v[82:85]
	v_mfma_f32_16x16x32_bf16 v[70:73], v[166:169], v[206:209], v[70:73]
	v_mfma_f32_16x16x32_bf16 v[66:69], v[174:177], v[206:209], v[66:69]
	v_mfma_f32_16x16x32_bf16 v[118:121], v[170:173], v[186:189], v[118:121]
	v_mfma_f32_16x16x32_bf16 v[114:117], v[178:181], v[186:189], v[114:117]
	v_mfma_f32_16x16x32_bf16 v[102:105], v[170:173], v[194:197], v[102:105]
	v_mfma_f32_16x16x32_bf16 v[98:101], v[178:181], v[194:197], v[98:101]
	v_mfma_f32_16x16x32_bf16 v[86:89], v[170:173], v[202:205], v[86:89]
	v_mfma_f32_16x16x32_bf16 v[82:85], v[178:181], v[202:205], v[82:85]
	v_mfma_f32_16x16x32_bf16 v[70:73], v[170:173], v[210:213], v[70:73]
	v_mfma_f32_16x16x32_bf16 v[66:69], v[178:181], v[210:213], v[66:69]
	s_setprio 0
	s_barrier
	s_add_i32 s20, s22, s43
	v_lshl_add_u64 v[148:149], s[50:51], 0, v[0:1]
	s_mov_b32 m0, s20
	ds_read_b128 v[182:185], v152 offset:16384
	ds_read_b128 v[186:189], v152 offset:17408
	ds_read_b128 v[190:193], v152 offset:18432
	ds_read_b128 v[194:197], v152 offset:19456
	ds_read_b128 v[198:201], v152 offset:20480
	ds_read_b128 v[202:205], v152 offset:21504
	ds_read_b128 v[206:209], v152 offset:22528
	ds_read_b128 v[210:213], v152 offset:23552
	global_load_lds_dwordx4 v[148:149], off
	s_add_i32 m0, s20, 0x2000
	s_add_u32 s20, s50, 0x40000
	v_lshl_add_u64 v[214:215], s[50:51], 0, v[130:131]
	s_addc_u32 s21, s51, 0
	s_add_i32 s22, s23, s43
	global_load_lds_dwordx4 v[214:215], off
	v_lshl_add_u64 v[224:225], s[20:21], 0, v[0:1]
	s_mov_b32 m0, s22
	v_lshl_add_u64 v[226:227], s[52:53], 0, v[132:133]
	global_load_lds_dwordx4 v[224:225], off
	v_lshl_add_u64 v[224:225], s[20:21], 0, v[130:131]
	s_add_i32 m0, s22, 0x2000
	s_nop 0
	global_load_lds_dwordx4 v[224:225], off
	v_lshl_add_u64 v[224:225], s[52:53], 0, v[134:135]
	s_mov_b32 m0, s10
	s_nop 0
	global_load_lds_dwordx4 v[224:225], off
	s_mov_b32 m0, s11
	s_nop 0
	global_load_lds_dwordx4 v[226:227], off
	s_waitcnt vmcnt(8)
	s_waitcnt lgkmcnt(0)
	s_barrier
; #define PG8_STAGE(bufoff, gbase, voff) do { _Pragma("unroll") for (int _i = 0; _i < 2; ++_i) \
;         __builtin_amdgcn_global_load_lds((const unsigned*)((const char*)(gbase) + (voff)[_i]), (LAS unsigned*)(lds + (bufoff) + ldsw + _i * 8192), 16, 0, 0); } while (0)
; #define PG8_STAGE_A(bufoff, h, kp, nx) do { if constexpr (GATHER) { const unsigned _p = (nx) ? ng[h] : cg[h]; unsigned _v[2]; _v[0] = (_p & 0xffffu) * lda + CA2[0]; _v[1] = (_p >> 16) * lda + CA2[1]; PG8_STAGE(bufoff, kp, _v); } \
;         else { PG8_STAGE(bufoff, (kp) + (h) * hstepA, voffA); } } while (0)
; #define PG8_LDA(dst, b, h) do { _Pragma("unroll") for (int m = 0; m < 4; ++m) _Pragma("unroll") for (int k = 0; k < 2; ++k) dst[m][k] = *(const LAS bf16x8*)(lds + PG8_SA(b, h) + aoff + m * 2048 + k * 1024); } while (0)
; #define PG8_LDB(dst, b, h) do { _Pragma("unroll") for (int n = 0; n < 2; ++n) _Pragma("unroll") for (int k = 0; k < 2; ++k) dst[n][k] = *(const LAS bf16x8*)(lds + PG8_SB(b, h) + boff + n * 2048 + k * 1024); } while (0)
; #define PG8_MMA(ai, bj, At, Bt) do { __builtin_amdgcn_s_setprio(1); _Pragma("unroll") for (int m = 0; m < 4; ++m) _Pragma("unroll") for (int n = 0; n < 2; ++n) _Pragma("unroll") for (int k = 0; k < 2; ++k) \
;         acc[ai][bj][m][n] = __builtin_amdgcn_mfma_f32_16x16x32_bf16(Bt[n][k], At[m][k], acc[ai][bj][m][n], 0, 0, 0); __builtin_amdgcn_s_setprio(0); } while (0)
; #define PG8_WAIT_V(n) asm volatile("s_waitcnt vmcnt(" #n ")" ::: "memory")
; #define PG8_WAIT_L(n) asm volatile("s_waitcnt lgkmcnt(" #n ")" ::: "memory")
; #define PG8_BAR __builtin_amdgcn_s_barrier()
; #define PG8_SCHED __builtin_amdgcn_sched_barrier(0)
;     ...
;             PG8_WAIT_V(8); PG8_WAIT_L(0); PG8_BAR; if (cur.amask & 2) { PG8_MMA(1, 0, At, B0); PG8_MMA(1, 1, At, B1); } PG8_BAR; PG8_SCHED;
;             PG8_LDB(B0, 1, 0); PG8_LDB(B1, 1, 1); PG8_SCHED; PG8_LDA(At, 1, 0); PG8_STAGE_A(PG8_SA(0, 1), 1, a2, last);
;             PG8_WAIT_V(8); PG8_WAIT_L(0); PG8_BAR; if (cur.amask & 1) { PG8_MMA(0, 0, At, B0); PG8_MMA(0, 1, At, B1); } PG8_BAR; PG8_SCHED;
;             PG8_LDA(At, 1, 1); PG8_STAGE(PG8_SB(1, 0), b3, voffB); PG8_STAGE(PG8_SB(1, 1), b3 + hstepB, voffB); PG8_STAGE_A(PG8_SA(1, 0), 0, a3, last);
;             PG8_WAIT_V(8); PG8_WAIT_L(0); PG8_BAR; if (cur.amask & 2) { PG8_MMA(1, 0, At, B0); PG8_MMA(1, 1, At, B1); } PG8_BAR; PG8_SCHED;
	s_setprio 1
	s_waitcnt lgkmcnt(0)
	v_mfma_f32_16x16x32_bf16 v[62:65], v[144:147], v[182:185], v[62:65]
	v_mfma_f32_16x16x32_bf16 v[58:61], v[158:161], v[182:185], v[58:61]
	v_mfma_f32_16x16x32_bf16 v[46:49], v[144:147], v[190:193], v[46:49]
	v_mfma_f32_16x16x32_bf16 v[42:45], v[158:161], v[190:193], v[42:45]
	v_mfma_f32_16x16x32_bf16 v[30:33], v[144:147], v[198:201], v[30:33]
	v_mfma_f32_16x16x32_bf16 v[26:29], v[158:161], v[198:201], v[26:29]
	v_mfma_f32_16x16x32_bf16 v[14:17], v[144:147], v[206:209], v[14:17]
	v_mfma_f32_16x16x32_bf16 v[10:13], v[158:161], v[206:209], v[10:13]
	v_mfma_f32_16x16x32_bf16 v[62:65], v[154:157], v[186:189], v[62:65]
	v_mfma_f32_16x16x32_bf16 v[58:61], v[162:165], v[186:189], v[58:61]
	v_mfma_f32_16x16x32_bf16 v[46:49], v[154:157], v[194:197], v[46:49]
	v_mfma_f32_16x16x32_bf16 v[42:45], v[162:165], v[194:197], v[42:45]
	v_mfma_f32_16x16x32_bf16 v[30:33], v[154:157], v[202:205], v[30:33]
	v_mfma_f32_16x16x32_bf16 v[26:29], v[162:165], v[202:205], v[26:29]
	v_mfma_f32_16x16x32_bf16 v[14:17], v[154:157], v[210:213], v[14:17]
	v_mfma_f32_16x16x32_bf16 v[10:13], v[162:165], v[210:213], v[10:13]
	s_setprio 0
	s_setprio 1
	v_mfma_f32_16x16x32_bf16 v[54:57], v[166:169], v[182:185], v[54:57]
	v_mfma_f32_16x16x32_bf16 v[50:53], v[174:177], v[182:185], v[50:53]
	v_mfma_f32_16x16x32_bf16 v[38:41], v[166:169], v[190:193], v[38:41]
	v_mfma_f32_16x16x32_bf16 v[34:37], v[174:177], v[190:193], v[34:37]
	v_mfma_f32_16x16x32_bf16 v[22:25], v[166:169], v[198:201], v[22:25]
	v_mfma_f32_16x16x32_bf16 v[18:21], v[174:177], v[198:201], v[18:21]
	v_mfma_f32_16x16x32_bf16 v[6:9], v[166:169], v[206:209], v[6:9]
	v_mfma_f32_16x16x32_bf16 v[2:5], v[174:177], v[206:209], v[2:5]
	v_mfma_f32_16x16x32_bf16 v[54:57], v[170:173], v[186:189], v[54:57]
	v_mfma_f32_16x16x32_bf16 v[50:53], v[178:181], v[186:189], v[50:53]
	v_mfma_f32_16x16x32_bf16 v[38:41], v[170:173], v[194:197], v[38:41]
	v_mfma_f32_16x16x32_bf16 v[34:37], v[178:181], v[194:197], v[34:37]
	v_mfma_f32_16x16x32_bf16 v[22:25], v[170:173], v[202:205], v[22:25]
	v_mfma_f32_16x16x32_bf16 v[18:21], v[178:181], v[202:205], v[18:21]
	v_mfma_f32_16x16x32_bf16 v[6:9], v[170:173], v[210:213], v[6:9]
	v_mfma_f32_16x16x32_bf16 v[2:5], v[178:181], v[210:213], v[2:5]
	s_setprio 0
	s_barrier
	s_add_i32 s22, 0, 0x18000
	v_add_u32_e32 v153, s22, v151
	s_add_i32 s23, 0, 0x1c000
	ds_read_b128 v[144:147], v153
	ds_read_b128 v[154:157], v153 offset:1024
	ds_read_b128 v[158:161], v153 offset:2048
	ds_read_b128 v[162:165], v153 offset:3072
	v_add_u32_e32 v153, s23, v151
	ds_read_b128 v[166:169], v153
	ds_read_b128 v[170:173], v153 offset:1024
	ds_read_b128 v[174:177], v153 offset:2048
	ds_read_b128 v[178:181], v153 offset:3072
	s_add_u32 s20, s52, 0x40000
	s_addc_u32 s21, s53, 0
	s_mov_b32 m0, s12
	v_lshl_add_u64 v[228:229], s[20:21], 0, v[134:135]
	ds_read_b128 v[182:185], v152 offset:32768
	ds_read_b128 v[186:189], v152 offset:33792
	ds_read_b128 v[190:193], v152 offset:34816
	ds_read_b128 v[194:197], v152 offset:35840
	ds_read_b128 v[198:201], v152 offset:36864
	ds_read_b128 v[202:205], v152 offset:37888
	ds_read_b128 v[206:209], v152 offset:38912
	ds_read_b128 v[210:213], v152 offset:39936
	global_load_lds_dwordx4 v[228:229], off
	v_lshl_add_u64 v[228:229], s[20:21], 0, v[132:133]
	s_mov_b32 m0, s13
	s_nop 0
	global_load_lds_dwordx4 v[228:229], off
	s_waitcnt vmcnt(8)
	s_waitcnt lgkmcnt(0)
	s_barrier
	s_setprio 1
	s_waitcnt lgkmcnt(0)
	v_mfma_f32_16x16x32_bf16 v[126:129], v[144:147], v[182:185], v[126:129]
	v_mfma_f32_16x16x32_bf16 v[122:125], v[158:161], v[182:185], v[122:125]
	v_mfma_f32_16x16x32_bf16 v[110:113], v[144:147], v[190:193], v[110:113]
	v_mfma_f32_16x16x32_bf16 v[106:109], v[158:161], v[190:193], v[106:109]
	v_mfma_f32_16x16x32_bf16 v[94:97], v[144:147], v[198:201], v[94:97]
	v_mfma_f32_16x16x32_bf16 v[90:93], v[158:161], v[198:201], v[90:93]
	v_mfma_f32_16x16x32_bf16 v[78:81], v[144:147], v[206:209], v[78:81]
	v_mfma_f32_16x16x32_bf16 v[74:77], v[158:161], v[206:209], v[74:77]
	v_mfma_f32_16x16x32_bf16 v[126:129], v[154:157], v[186:189], v[126:129]
	v_mfma_f32_16x16x32_bf16 v[122:125], v[162:165], v[186:189], v[122:125]
	v_mfma_f32_16x16x32_bf16 v[110:113], v[154:157], v[194:197], v[110:113]
	v_mfma_f32_16x16x32_bf16 v[106:109], v[162:165], v[194:197], v[106:109]
	v_mfma_f32_16x16x32_bf16 v[94:97], v[154:157], v[202:205], v[94:97]
	v_mfma_f32_16x16x32_bf16 v[90:93], v[162:165], v[202:205], v[90:93]
	v_mfma_f32_16x16x32_bf16 v[78:81], v[154:157], v[210:213], v[78:81]
	v_mfma_f32_16x16x32_bf16 v[74:77], v[162:165], v[210:213], v[74:77]
	s_setprio 0
	s_setprio 1
	v_mfma_f32_16x16x32_bf16 v[118:121], v[166:169], v[182:185], v[118:121]
	v_mfma_f32_16x16x32_bf16 v[114:117], v[174:177], v[182:185], v[114:117]
	v_mfma_f32_16x16x32_bf16 v[102:105], v[166:169], v[190:193], v[102:105]
	v_mfma_f32_16x16x32_bf16 v[98:101], v[174:177], v[190:193], v[98:101]
	v_mfma_f32_16x16x32_bf16 v[86:89], v[166:169], v[198:201], v[86:89]
	v_mfma_f32_16x16x32_bf16 v[82:85], v[174:177], v[198:201], v[82:85]
	v_mfma_f32_16x16x32_bf16 v[70:73], v[166:169], v[206:209], v[70:73]
	v_mfma_f32_16x16x32_bf16 v[66:69], v[174:177], v[206:209], v[66:69]
	v_mfma_f32_16x16x32_bf16 v[118:121], v[170:173], v[186:189], v[118:121]
	v_mfma_f32_16x16x32_bf16 v[114:117], v[178:181], v[186:189], v[114:117]
	v_mfma_f32_16x16x32_bf16 v[102:105], v[170:173], v[194:197], v[102:105]
	v_mfma_f32_16x16x32_bf16 v[98:101], v[178:181], v[194:197], v[98:101]
	v_mfma_f32_16x16x32_bf16 v[86:89], v[170:173], v[202:205], v[86:89]
	v_mfma_f32_16x16x32_bf16 v[82:85], v[178:181], v[202:205], v[82:85]
	v_mfma_f32_16x16x32_bf16 v[70:73], v[170:173], v[210:213], v[70:73]
	v_mfma_f32_16x16x32_bf16 v[66:69], v[178:181], v[210:213], v[66:69]
	s_setprio 0
	s_barrier
; #define PG8_MMA(ai, bj, At, Bt) do { __builtin_amdgcn_s_setprio(1); _Pragma("unroll") for (int m = 0; m < 4; ++m) _Pragma("unroll") for (int n = 0; n < 2; ++n) _Pragma("unroll") for (int k = 0; k < 2; ++k) \
;         acc[ai][bj][m][n] = __builtin_amdgcn_mfma_f32_16x16x32_bf16(Bt[n][k], At[m][k], acc[ai][bj][m][n], 0, 0, 0); __builtin_amdgcn_s_setprio(0); } while (0)
; #define PG8_WAIT_V(n) asm volatile("s_waitcnt vmcnt(" #n ")" ::: "memory")
; #define PG8_WAIT_L(n) asm volatile("s_waitcnt lgkmcnt(" #n ")" ::: "memory")
; #define PG8_BAR __builtin_amdgcn_s_barrier()
; #define PG8_SCHED __builtin_amdgcn_sched_barrier(0)
;     ...
;             PG8_WAIT_V(8); PG8_WAIT_L(0); PG8_BAR; if (cur.amask & 2) { PG8_MMA(1, 0, At, B0); PG8_MMA(1, 1, At, B1); } PG8_BAR; PG8_SCHED;
;         }
;         if constexpr (ALIGN_EPI) { if (wr == 0) PG8_BAR; }
	s_add_i32 s20, s22, s43
	v_lshl_add_u64 v[148:149], v[148:149], 0, s[92:93]
	s_mov_b32 m0, s20
	ds_read_b128 v[182:185], v152 offset:49152
	ds_read_b128 v[186:189], v152 offset:50176
	ds_read_b128 v[190:193], v152 offset:51200
	ds_read_b128 v[194:197], v152 offset:52224
	ds_read_b128 v[198:201], v152 offset:53248
	ds_read_b128 v[202:205], v152 offset:54272
	ds_read_b128 v[206:209], v152 offset:55296
	ds_read_b128 v[210:213], v152 offset:56320
	global_load_lds_dwordx4 v[148:149], off
	s_add_i32 m0, s20, 0x2000
	s_add_u32 s20, s50, 0x40080
	v_lshl_add_u64 v[148:149], v[214:215], 0, s[92:93]
	s_addc_u32 s21, s51, 0
	s_add_i32 s22, s23, s43
	global_load_lds_dwordx4 v[148:149], off
	v_lshl_add_u64 v[148:149], s[20:21], 0, v[0:1]
	s_mov_b32 m0, s22
	s_nop 0
	global_load_lds_dwordx4 v[148:149], off
	v_lshl_add_u64 v[148:149], s[20:21], 0, v[130:131]
	s_add_i32 m0, s22, 0x2000
	s_nop 0
	global_load_lds_dwordx4 v[148:149], off
	v_lshl_add_u64 v[148:149], v[224:225], 0, s[92:93]
	s_mov_b32 m0, s14
	s_nop 0
	global_load_lds_dwordx4 v[148:149], off
	v_lshl_add_u64 v[148:149], v[226:227], 0, s[92:93]
	s_mov_b32 m0, s15
	s_nop 0
	global_load_lds_dwordx4 v[148:149], off
	s_waitcnt vmcnt(8)
	s_waitcnt lgkmcnt(0)
	s_barrier
	s_setprio 1
	s_waitcnt lgkmcnt(0)
	v_mfma_f32_16x16x32_bf16 v[62:65], v[144:147], v[182:185], v[62:65]
	v_mfma_f32_16x16x32_bf16 v[58:61], v[158:161], v[182:185], v[58:61]
	v_mfma_f32_16x16x32_bf16 v[46:49], v[144:147], v[190:193], v[46:49]
	v_mfma_f32_16x16x32_bf16 v[42:45], v[158:161], v[190:193], v[42:45]
	v_mfma_f32_16x16x32_bf16 v[30:33], v[144:147], v[198:201], v[30:33]
	v_mfma_f32_16x16x32_bf16 v[26:29], v[158:161], v[198:201], v[26:29]
	v_mfma_f32_16x16x32_bf16 v[14:17], v[144:147], v[206:209], v[14:17]
	v_mfma_f32_16x16x32_bf16 v[10:13], v[158:161], v[206:209], v[10:13]
	v_mfma_f32_16x16x32_bf16 v[62:65], v[154:157], v[186:189], v[62:65]
	v_mfma_f32_16x16x32_bf16 v[58:61], v[162:165], v[186:189], v[58:61]
	v_mfma_f32_16x16x32_bf16 v[46:49], v[154:157], v[194:197], v[46:49]
	v_mfma_f32_16x16x32_bf16 v[42:45], v[162:165], v[194:197], v[42:45]
	v_mfma_f32_16x16x32_bf16 v[30:33], v[154:157], v[202:205], v[30:33]
	v_mfma_f32_16x16x32_bf16 v[26:29], v[162:165], v[202:205], v[26:29]
	v_mfma_f32_16x16x32_bf16 v[14:17], v[154:157], v[210:213], v[14:17]
	v_mfma_f32_16x16x32_bf16 v[10:13], v[162:165], v[210:213], v[10:13]
	s_setprio 0
	s_setprio 1
	v_mfma_f32_16x16x32_bf16 v[54:57], v[166:169], v[182:185], v[54:57]
	v_mfma_f32_16x16x32_bf16 v[50:53], v[174:177], v[182:185], v[50:53]
	v_mfma_f32_16x16x32_bf16 v[38:41], v[166:169], v[190:193], v[38:41]
	v_mfma_f32_16x16x32_bf16 v[34:37], v[174:177], v[190:193], v[34:37]
	v_mfma_f32_16x16x32_bf16 v[22:25], v[166:169], v[198:201], v[22:25]
	v_mfma_f32_16x16x32_bf16 v[18:21], v[174:177], v[198:201], v[18:21]
	v_mfma_f32_16x16x32_bf16 v[6:9], v[166:169], v[206:209], v[6:9]
	v_mfma_f32_16x16x32_bf16 v[2:5], v[174:177], v[206:209], v[2:5]
	v_mfma_f32_16x16x32_bf16 v[54:57], v[170:173], v[186:189], v[54:57]
	v_mfma_f32_16x16x32_bf16 v[50:53], v[178:181], v[186:189], v[50:53]
	v_mfma_f32_16x16x32_bf16 v[38:41], v[170:173], v[194:197], v[38:41]
	v_mfma_f32_16x16x32_bf16 v[34:37], v[178:181], v[194:197], v[34:37]
	v_mfma_f32_16x16x32_bf16 v[22:25], v[170:173], v[202:205], v[22:25]
	v_mfma_f32_16x16x32_bf16 v[18:21], v[178:181], v[202:205], v[18:21]
	v_mfma_f32_16x16x32_bf16 v[6:9], v[170:173], v[210:213], v[6:9]
	v_mfma_f32_16x16x32_bf16 v[2:5], v[178:181], v[210:213], v[2:5]
	s_setprio 0
	s_add_i32 s19, s19, 2
	s_add_u32 s48, s48, 0x100
	s_addc_u32 s49, s49, 0
	s_add_u32 s17, s17, 0x100
	s_addc_u32 s18, s18, 0
	s_cmp_gt_u32 s19, 13
	s_barrier
	s_cbranch_scc0 .LBB0_1392
	v_readlane_b32 s18, v252, 14
	v_readlane_b32 s19, v252, 15
	s_and_b64 vcc, exec, s[18:19]
	s_cbranch_vccz .LBB0_1395
	s_barrier
